# K-loops: the leading wave half waits for its LDS-DMA pieces after its MFMA block (one barrier later) instead of at the end of its load phase; trailing half unchanged
# baseline (speedup 1.0000x reference)
; #define PG8_STAGE(bufoff, gbase, voff) do { _Pragma("unroll") for (int _i = 0; _i < 2; ++_i) \
;         __builtin_amdgcn_global_load_lds((const unsigned*)((const char*)(gbase) + (voff)[_i]), (LAS unsigned*)(lds + (bufoff) + ldsw + _i * 8192), 16, 0, 0); } while (0)
; #define PG8_LDA(dst, b, h) do { _Pragma("unroll") for (int m = 0; m < 4; ++m) _Pragma("unroll") for (int k = 0; k < 2; ++k) dst[m][k] = *(const LAS bf16x8*)(lds + PG8_SA(b, h) + ((aoff ^ (k * 64)) + m * 2048)); } while (0)
; #define PG8_LDB(dst, b, h) do { _Pragma("unroll") for (int n = 0; n < 2; ++n) _Pragma("unroll") for (int k = 0; k < 2; ++k) dst[n][k] = *(const LAS bf16x8*)(lds + PG8_SB(b, h) + ((boff ^ (k * 64)) + n * 2048)); } while (0)
;     ...
;         for (int t = 0; t < nt; t += 2) {
;             const bool last = (t == nt - 2);
;             const char* a1 = cA + (size_t)(t + 1) * kstepA;
;             const char* a2 = last ? nA : cA + (size_t)(t + 2) * kstepA; const char* b2 = last ? nB : cB + (size_t)(t + 2) * kstepB;
;             const char* a3 = a2 + kstepA; const char* b3 = b2 + kstepB;
;             unsigned vs[2][2];
;             if constexpr (GATHER) {
;                 if (last && has_next) {
; #pragma unroll
;                     for (int hh = 0; hh < 2; ++hh)
; #pragma unroll
;                         for (int i = 0; i < 2; ++i) voffN[hh][i] = (unsigned)idxl[(ui + 1) * 256 + hh * HALF + sR[i]] * (unsigned)(K * 2) + (unsigned)sC[i] * 2u;
;                 }
; #pragma unroll
;                 for (int hh = 0; hh < 2; ++hh)
; #pragma unroll
;                     for (int i = 0; i < 2; ++i) vs[hh][i] = last ? voffN[hh][i] : voffA[hh][i];
;             } else {
; #pragma unroll
;                 for (int hh = 0; hh < 2; ++hh)
; #pragma unroll
;                     for (int i = 0; i < 2; ++i) vs[hh][i] = voffA[hh][i];
;             }
;             PG8_LDB(B0, 0, 0); PG8_LDB(B1, 0, 1); PG8_SCHED; PG8_LDA(At, 0, 0); PG8_STAGE(PG8_SA(1, 1), a1, voffA[1]);
;             PG8_WAIT_V(8); PG8_WAIT_L(0); PG8_BAR; if (do0) { PG8_MMA(0, 0, At, B0); PG8_MMA(0, 1, At, B1); } PG8_BAR; PG8_SCHED;
;             PG8_LDA(At, 0, 1); PG8_STAGE(PG8_SB(0, 0), b2, voffB); PG8_STAGE(PG8_SB(0, 1), b2 + hstep, voffB); PG8_STAGE(PG8_SA(0, 0), a2, vs[0]);
;             PG8_WAIT_V(8); PG8_WAIT_L(0); PG8_BAR; if (do1) { PG8_MMA(1, 0, At, B0); PG8_MMA(1, 1, At, B1); } PG8_BAR; PG8_SCHED;
.LBB0_192:
	ds_read_b128 v[158:161], v166
	ds_read_b128 v[180:183], v167
	ds_read_b128 v[184:187], v168
	ds_read_b128 v[188:191], v169
	ds_read_b128 v[192:195], v170
	ds_read_b128 v[200:203], v171
	ds_read_b128 v[204:207], v172
	ds_read_b128 v[208:211], v173
	s_add_u32 s28, s4, 0x80
	s_addc_u32 s29, s5, 0
	s_cmp_eq_u32 s64, 12
	s_cselect_b32 s35, s17, s29
	s_cselect_b32 s34, s60, s28
	s_cselect_b32 s29, s19, s63
	s_cselect_b32 s28, s61, s62
	v_lshl_add_u64 v[162:163], s[4:5], 0, v[152:153]
	s_add_i32 m0, s25, 0xc000
	ds_read_b128 v[212:215], v174
	ds_read_b128 v[216:219], v174 offset:2048
	ds_read_b128 v[220:223], v175
	ds_read_b128 v[224:227], v175 offset:2048
	ds_read_b128 v[228:231], v174 offset:4096
	ds_read_b128 v[232:235], v174 offset:6144
	ds_read_b128 v[236:239], v175 offset:4096
	ds_read_b128 v[240:243], v175 offset:6144
	global_load_lds_dwordx4 v[162:163], off
	v_lshl_add_u64 v[162:163], s[4:5], 0, v[150:151]
	s_add_i32 m0, s25, 0xe000
	s_add_u32 s30, s28, 0x4000
	global_load_lds_dwordx4 v[162:163], off
	s_mov_b64 vcc, s[6:7]
	s_cbranch_vccz .Lwm_in0n_0
	s_waitcnt vmcnt(8)
.Lwm_in0n_0:
	s_waitcnt lgkmcnt(0)
	s_addc_u32 s31, s29, 0
	s_barrier
	s_setprio 1
	s_waitcnt lgkmcnt(0)
	v_mfma_f32_16x16x32_bf16 v[126:129], v[158:161], v[212:215], v[126:129]
	v_mfma_f32_16x16x32_bf16 v[122:125], v[184:187], v[212:215], v[122:125]
	v_mfma_f32_16x16x32_bf16 v[110:113], v[158:161], v[216:219], v[110:113]
	v_mfma_f32_16x16x32_bf16 v[106:109], v[184:187], v[216:219], v[106:109]
	v_mfma_f32_16x16x32_bf16 v[94:97], v[158:161], v[228:231], v[94:97]
	v_mfma_f32_16x16x32_bf16 v[90:93], v[184:187], v[228:231], v[90:93]
	v_mfma_f32_16x16x32_bf16 v[78:81], v[158:161], v[232:235], v[78:81]
	v_mfma_f32_16x16x32_bf16 v[74:77], v[184:187], v[232:235], v[74:77]
	v_mfma_f32_16x16x32_bf16 v[126:129], v[180:183], v[220:223], v[126:129]
	v_mfma_f32_16x16x32_bf16 v[122:125], v[188:191], v[220:223], v[122:125]
	v_mfma_f32_16x16x32_bf16 v[110:113], v[180:183], v[224:227], v[110:113]
	v_mfma_f32_16x16x32_bf16 v[106:109], v[188:191], v[224:227], v[106:109]
	v_mfma_f32_16x16x32_bf16 v[94:97], v[180:183], v[236:239], v[94:97]
	v_mfma_f32_16x16x32_bf16 v[90:93], v[188:191], v[236:239], v[90:93]
	v_mfma_f32_16x16x32_bf16 v[78:81], v[180:183], v[240:243], v[78:81]
	v_mfma_f32_16x16x32_bf16 v[74:77], v[188:191], v[240:243], v[74:77]
	s_setprio 0
	s_setprio 1
	v_mfma_f32_16x16x32_bf16 v[118:121], v[192:195], v[212:215], v[118:121]
	v_mfma_f32_16x16x32_bf16 v[114:117], v[204:207], v[212:215], v[114:117]
	v_mfma_f32_16x16x32_bf16 v[102:105], v[192:195], v[216:219], v[102:105]
	v_mfma_f32_16x16x32_bf16 v[98:101], v[204:207], v[216:219], v[98:101]
	v_mfma_f32_16x16x32_bf16 v[86:89], v[192:195], v[228:231], v[86:89]
	v_mfma_f32_16x16x32_bf16 v[82:85], v[204:207], v[228:231], v[82:85]
	v_mfma_f32_16x16x32_bf16 v[70:73], v[192:195], v[232:235], v[70:73]
	v_mfma_f32_16x16x32_bf16 v[66:69], v[204:207], v[232:235], v[66:69]
	v_mfma_f32_16x16x32_bf16 v[118:121], v[200:203], v[220:223], v[118:121]
	v_mfma_f32_16x16x32_bf16 v[114:117], v[208:211], v[220:223], v[114:117]
	v_mfma_f32_16x16x32_bf16 v[102:105], v[200:203], v[224:227], v[102:105]
	v_mfma_f32_16x16x32_bf16 v[98:101], v[208:211], v[224:227], v[98:101]
	v_mfma_f32_16x16x32_bf16 v[86:89], v[200:203], v[236:239], v[86:89]
	v_mfma_f32_16x16x32_bf16 v[82:85], v[208:211], v[236:239], v[82:85]
	v_mfma_f32_16x16x32_bf16 v[70:73], v[200:203], v[240:243], v[70:73]
	v_mfma_f32_16x16x32_bf16 v[66:69], v[208:211], v[240:243], v[66:69]
	s_setprio 0
	s_waitcnt vmcnt(8)
	s_barrier
	s_add_i32 s65, s56, s37
	v_lshl_add_u64 v[162:163], s[28:29], 0, v[130:131]
	s_mov_b32 m0, s65
	ds_read_b128 v[212:215], v174 offset:16384
	ds_read_b128 v[216:219], v174 offset:18432
	ds_read_b128 v[220:223], v175 offset:16384
	ds_read_b128 v[224:227], v175 offset:18432
	ds_read_b128 v[228:231], v174 offset:20480
	ds_read_b128 v[232:235], v174 offset:22528
	ds_read_b128 v[236:239], v175 offset:20480
	ds_read_b128 v[240:243], v175 offset:22528
	global_load_lds_dwordx4 v[162:163], off
	s_add_i32 m0, s65, 0x2000
	s_add_u32 s66, s28, 0x40000
	v_lshl_add_u64 v[162:163], s[28:29], 0, v[132:133]
	s_addc_u32 s67, s29, 0
	s_add_i32 s65, s57, s37
	global_load_lds_dwordx4 v[162:163], off
	v_lshl_add_u64 v[162:163], s[66:67], 0, v[130:131]
	s_mov_b32 m0, s65
	v_lshl_add_u64 v[196:197], s[34:35], 0, v[136:137]
	global_load_lds_dwordx4 v[162:163], off
	v_lshl_add_u64 v[162:163], s[66:67], 0, v[132:133]
	s_add_i32 m0, s65, 0x2000
	s_nop 0
	global_load_lds_dwordx4 v[162:163], off
	v_lshl_add_u64 v[162:163], s[34:35], 0, v[134:135]
	s_mov_b32 m0, s25
	s_nop 0
	global_load_lds_dwordx4 v[162:163], off
	s_mov_b32 m0, s27
	s_nop 0
	global_load_lds_dwordx4 v[196:197], off
	s_bitcmp1_b32 s6, 0
	s_cbranch_scc0 .Lwm_in0n_1
	s_waitcnt vmcnt(8)
; #define PG8_STAGE(bufoff, gbase, voff) do { _Pragma("unroll") for (int _i = 0; _i < 2; ++_i) \
;         __builtin_amdgcn_global_load_lds((const unsigned*)((const char*)(gbase) + (voff)[_i]), (LAS unsigned*)(lds + (bufoff) + ldsw + _i * 8192), 16, 0, 0); } while (0)
; #define PG8_LDA(dst, b, h) do { _Pragma("unroll") for (int m = 0; m < 4; ++m) _Pragma("unroll") for (int k = 0; k < 2; ++k) dst[m][k] = *(const LAS bf16x8*)(lds + PG8_SA(b, h) + ((aoff ^ (k * 64)) + m * 2048)); } while (0)
; #define PG8_LDB(dst, b, h) do { _Pragma("unroll") for (int n = 0; n < 2; ++n) _Pragma("unroll") for (int k = 0; k < 2; ++k) dst[n][k] = *(const LAS bf16x8*)(lds + PG8_SB(b, h) + ((boff ^ (k * 64)) + n * 2048)); } while (0)
; #define PG8_MMA(ai, bj, At, Bt) do { __builtin_amdgcn_s_setprio(1); _Pragma("unroll") for (int m = 0; m < 4; ++m) _Pragma("unroll") for (int n = 0; n < 2; ++n) _Pragma("unroll") for (int k = 0; k < 2; ++k) \
;         acc[ai][bj][m][n] = __builtin_amdgcn_mfma_f32_16x16x32_bf16(Bt[n][k], At[m][k], acc[ai][bj][m][n], 0, 0, 0); __builtin_amdgcn_s_setprio(0); } while (0)
; #define PG8_WAIT_V(n) asm volatile("s_waitcnt vmcnt(" #n ")" ::: "memory")
; #define PG8_WAIT_L(n) asm volatile("s_waitcnt lgkmcnt(" #n ")" ::: "memory")
; #define PG8_BAR __builtin_amdgcn_s_barrier()
; #define PG8_SCHED __builtin_amdgcn_sched_barrier(0)
;     ...
;             PG8_WAIT_V(8); PG8_WAIT_L(0); PG8_BAR; if (do1) { PG8_MMA(1, 0, At, B0); PG8_MMA(1, 1, At, B1); } PG8_BAR; PG8_SCHED;
;             PG8_LDB(B0, 1, 0); PG8_LDB(B1, 1, 1); PG8_SCHED; PG8_LDA(At, 1, 0); PG8_STAGE(PG8_SA(0, 1), a2, vs[1]);
;             PG8_WAIT_V(8); PG8_WAIT_L(0); PG8_BAR; if (do0) { PG8_MMA(0, 0, At, B0); PG8_MMA(0, 1, At, B1); } PG8_BAR; PG8_SCHED;
.Lwm_in0n_1:
	s_waitcnt lgkmcnt(0)
	s_barrier
	s_setprio 1
	s_waitcnt lgkmcnt(0)
	v_mfma_f32_16x16x32_bf16 v[62:65], v[158:161], v[212:215], v[62:65]
	v_mfma_f32_16x16x32_bf16 v[58:61], v[184:187], v[212:215], v[58:61]
	v_mfma_f32_16x16x32_bf16 v[46:49], v[158:161], v[216:219], v[46:49]
	v_mfma_f32_16x16x32_bf16 v[42:45], v[184:187], v[216:219], v[42:45]
	v_mfma_f32_16x16x32_bf16 v[30:33], v[158:161], v[228:231], v[30:33]
	v_mfma_f32_16x16x32_bf16 v[26:29], v[184:187], v[228:231], v[26:29]
	v_mfma_f32_16x16x32_bf16 v[14:17], v[158:161], v[232:235], v[14:17]
	v_mfma_f32_16x16x32_bf16 v[10:13], v[184:187], v[232:235], v[10:13]
	v_mfma_f32_16x16x32_bf16 v[62:65], v[180:183], v[220:223], v[62:65]
	v_mfma_f32_16x16x32_bf16 v[58:61], v[188:191], v[220:223], v[58:61]
	v_mfma_f32_16x16x32_bf16 v[46:49], v[180:183], v[224:227], v[46:49]
	v_mfma_f32_16x16x32_bf16 v[42:45], v[188:191], v[224:227], v[42:45]
	v_mfma_f32_16x16x32_bf16 v[30:33], v[180:183], v[236:239], v[30:33]
	v_mfma_f32_16x16x32_bf16 v[26:29], v[188:191], v[236:239], v[26:29]
	v_mfma_f32_16x16x32_bf16 v[14:17], v[180:183], v[240:243], v[14:17]
	v_mfma_f32_16x16x32_bf16 v[10:13], v[188:191], v[240:243], v[10:13]
	s_setprio 0
	s_setprio 1
	v_mfma_f32_16x16x32_bf16 v[54:57], v[192:195], v[212:215], v[54:57]
	v_mfma_f32_16x16x32_bf16 v[50:53], v[204:207], v[212:215], v[50:53]
	v_mfma_f32_16x16x32_bf16 v[38:41], v[192:195], v[216:219], v[38:41]
	v_mfma_f32_16x16x32_bf16 v[34:37], v[204:207], v[216:219], v[34:37]
	v_mfma_f32_16x16x32_bf16 v[22:25], v[192:195], v[228:231], v[22:25]
	v_mfma_f32_16x16x32_bf16 v[18:21], v[204:207], v[228:231], v[18:21]
	v_mfma_f32_16x16x32_bf16 v[6:9], v[192:195], v[232:235], v[6:9]
	v_mfma_f32_16x16x32_bf16 v[2:5], v[204:207], v[232:235], v[2:5]
	v_mfma_f32_16x16x32_bf16 v[54:57], v[200:203], v[220:223], v[54:57]
	v_mfma_f32_16x16x32_bf16 v[50:53], v[208:211], v[220:223], v[50:53]
	v_mfma_f32_16x16x32_bf16 v[38:41], v[200:203], v[224:227], v[38:41]
	v_mfma_f32_16x16x32_bf16 v[34:37], v[208:211], v[224:227], v[34:37]
	v_mfma_f32_16x16x32_bf16 v[22:25], v[200:203], v[236:239], v[22:25]
	v_mfma_f32_16x16x32_bf16 v[18:21], v[208:211], v[236:239], v[18:21]
	v_mfma_f32_16x16x32_bf16 v[6:9], v[200:203], v[240:243], v[6:9]
	v_mfma_f32_16x16x32_bf16 v[2:5], v[208:211], v[240:243], v[2:5]
	s_setprio 0
	s_waitcnt vmcnt(8)
	s_barrier
	s_add_i32 s65, 0, 0x18000
	v_add_u32_e32 v142, s65, v145
	v_add_u32_e32 v180, s65, v165
	s_add_i32 s66, 0, 0x1c000
	ds_read_b128 v[158:161], v142
	ds_read_b128 v[180:183], v180
	ds_read_b128 v[184:187], v176
	ds_read_b128 v[188:191], v177
	v_add_u32_e32 v142, s66, v145
	v_add_u32_e32 v199, s66, v165
	ds_read_b128 v[192:195], v142
	ds_read_b128 v[200:203], v199
	ds_read_b128 v[204:207], v178
	ds_read_b128 v[208:211], v179
	s_mov_b32 m0, s38
	v_lshl_add_u64 v[244:245], s[34:35], 0, v[138:139]
	ds_read_b128 v[212:215], v174 offset:32768
	ds_read_b128 v[216:219], v174 offset:34816
	ds_read_b128 v[220:223], v175 offset:32768
	ds_read_b128 v[224:227], v175 offset:34816
	ds_read_b128 v[228:231], v174 offset:36864
	ds_read_b128 v[232:235], v174 offset:38912
	ds_read_b128 v[236:239], v175 offset:36864
	ds_read_b128 v[240:243], v175 offset:38912
	global_load_lds_dwordx4 v[244:245], off
	v_lshl_add_u64 v[244:245], s[34:35], 0, v[140:141]
	s_mov_b32 m0, s39
	s_nop 0
	global_load_lds_dwordx4 v[244:245], off
	s_bitcmp1_b32 s6, 0
	s_cbranch_scc0 .Lwm_in0n_2
	s_waitcnt vmcnt(8)
; #define PG8_STAGE(bufoff, gbase, voff) do { _Pragma("unroll") for (int _i = 0; _i < 2; ++_i) \
;         __builtin_amdgcn_global_load_lds((const unsigned*)((const char*)(gbase) + (voff)[_i]), (LAS unsigned*)(lds + (bufoff) + ldsw + _i * 8192), 16, 0, 0); } while (0)
; #define PG8_LDA(dst, b, h) do { _Pragma("unroll") for (int m = 0; m < 4; ++m) _Pragma("unroll") for (int k = 0; k < 2; ++k) dst[m][k] = *(const LAS bf16x8*)(lds + PG8_SA(b, h) + ((aoff ^ (k * 64)) + m * 2048)); } while (0)
; #define PG8_MMA(ai, bj, At, Bt) do { __builtin_amdgcn_s_setprio(1); _Pragma("unroll") for (int m = 0; m < 4; ++m) _Pragma("unroll") for (int n = 0; n < 2; ++n) _Pragma("unroll") for (int k = 0; k < 2; ++k) \
;         acc[ai][bj][m][n] = __builtin_amdgcn_mfma_f32_16x16x32_bf16(Bt[n][k], At[m][k], acc[ai][bj][m][n], 0, 0, 0); __builtin_amdgcn_s_setprio(0); } while (0)
; #define PG8_WAIT_V(n) asm volatile("s_waitcnt vmcnt(" #n ")" ::: "memory")
; #define PG8_WAIT_L(n) asm volatile("s_waitcnt lgkmcnt(" #n ")" ::: "memory")
; #define PG8_BAR __builtin_amdgcn_s_barrier()
; #define PG8_SCHED __builtin_amdgcn_sched_barrier(0)
;     ...
;             PG8_WAIT_V(8); PG8_WAIT_L(0); PG8_BAR; if (do0) { PG8_MMA(0, 0, At, B0); PG8_MMA(0, 1, At, B1); } PG8_BAR; PG8_SCHED;
;             PG8_LDA(At, 1, 1); PG8_STAGE(PG8_SB(1, 0), b3, voffB); PG8_STAGE(PG8_SB(1, 1), b3 + hstep, voffB); PG8_STAGE(PG8_SA(1, 0), a3, vs[0]);
;             PG8_WAIT_V(8); PG8_WAIT_L(0); PG8_BAR; if (do1) { PG8_MMA(1, 0, At, B0); PG8_MMA(1, 1, At, B1); } PG8_BAR; PG8_SCHED;
;         }
.Lwm_in0n_2:
	s_waitcnt lgkmcnt(0)
	s_barrier
	s_setprio 1
	s_waitcnt lgkmcnt(0)
	v_mfma_f32_16x16x32_bf16 v[126:129], v[158:161], v[212:215], v[126:129]
	v_mfma_f32_16x16x32_bf16 v[122:125], v[184:187], v[212:215], v[122:125]
	v_mfma_f32_16x16x32_bf16 v[110:113], v[158:161], v[216:219], v[110:113]
	v_mfma_f32_16x16x32_bf16 v[106:109], v[184:187], v[216:219], v[106:109]
	v_mfma_f32_16x16x32_bf16 v[94:97], v[158:161], v[228:231], v[94:97]
	v_mfma_f32_16x16x32_bf16 v[90:93], v[184:187], v[228:231], v[90:93]
	v_mfma_f32_16x16x32_bf16 v[78:81], v[158:161], v[232:235], v[78:81]
	v_mfma_f32_16x16x32_bf16 v[74:77], v[184:187], v[232:235], v[74:77]
	v_mfma_f32_16x16x32_bf16 v[126:129], v[180:183], v[220:223], v[126:129]
	v_mfma_f32_16x16x32_bf16 v[122:125], v[188:191], v[220:223], v[122:125]
	v_mfma_f32_16x16x32_bf16 v[110:113], v[180:183], v[224:227], v[110:113]
	v_mfma_f32_16x16x32_bf16 v[106:109], v[188:191], v[224:227], v[106:109]
	v_mfma_f32_16x16x32_bf16 v[94:97], v[180:183], v[236:239], v[94:97]
	v_mfma_f32_16x16x32_bf16 v[90:93], v[188:191], v[236:239], v[90:93]
	v_mfma_f32_16x16x32_bf16 v[78:81], v[180:183], v[240:243], v[78:81]
	v_mfma_f32_16x16x32_bf16 v[74:77], v[188:191], v[240:243], v[74:77]
	s_setprio 0
	s_setprio 1
	v_mfma_f32_16x16x32_bf16 v[118:121], v[192:195], v[212:215], v[118:121]
	v_mfma_f32_16x16x32_bf16 v[114:117], v[204:207], v[212:215], v[114:117]
	v_mfma_f32_16x16x32_bf16 v[102:105], v[192:195], v[216:219], v[102:105]
	v_mfma_f32_16x16x32_bf16 v[98:101], v[204:207], v[216:219], v[98:101]
	v_mfma_f32_16x16x32_bf16 v[86:89], v[192:195], v[228:231], v[86:89]
	v_mfma_f32_16x16x32_bf16 v[82:85], v[204:207], v[228:231], v[82:85]
	v_mfma_f32_16x16x32_bf16 v[70:73], v[192:195], v[232:235], v[70:73]
	v_mfma_f32_16x16x32_bf16 v[66:69], v[204:207], v[232:235], v[66:69]
	v_mfma_f32_16x16x32_bf16 v[118:121], v[200:203], v[220:223], v[118:121]
	v_mfma_f32_16x16x32_bf16 v[114:117], v[208:211], v[220:223], v[114:117]
	v_mfma_f32_16x16x32_bf16 v[102:105], v[200:203], v[224:227], v[102:105]
	v_mfma_f32_16x16x32_bf16 v[98:101], v[208:211], v[224:227], v[98:101]
	v_mfma_f32_16x16x32_bf16 v[86:89], v[200:203], v[236:239], v[86:89]
	v_mfma_f32_16x16x32_bf16 v[82:85], v[208:211], v[236:239], v[82:85]
	v_mfma_f32_16x16x32_bf16 v[70:73], v[200:203], v[240:243], v[70:73]
	v_mfma_f32_16x16x32_bf16 v[66:69], v[208:211], v[240:243], v[66:69]
	s_setprio 0
	s_waitcnt vmcnt(8)
	s_barrier
	s_add_i32 s34, s65, s37
	v_lshl_add_u64 v[244:245], s[30:31], 0, v[130:131]
	s_mov_b32 m0, s34
	ds_read_b128 v[212:215], v174 offset:49152
	ds_read_b128 v[216:219], v174 offset:51200
	ds_read_b128 v[220:223], v175 offset:49152
	ds_read_b128 v[224:227], v175 offset:51200
	ds_read_b128 v[228:231], v174 offset:53248
	ds_read_b128 v[232:235], v174 offset:55296
	ds_read_b128 v[236:239], v175 offset:53248
	ds_read_b128 v[240:243], v175 offset:55296
	global_load_lds_dwordx4 v[244:245], off
	s_add_i32 m0, s34, 0x2000
	s_add_u32 s28, s28, 0x44000
	v_lshl_add_u64 v[244:245], s[30:31], 0, v[132:133]
	s_addc_u32 s29, s29, 0
	s_add_i32 s30, s66, s37
	global_load_lds_dwordx4 v[244:245], off
	v_lshl_add_u64 v[244:245], s[28:29], 0, v[130:131]
	s_mov_b32 m0, s30
	v_lshl_add_u64 v[162:163], v[162:163], 0, s[8:9]
	global_load_lds_dwordx4 v[244:245], off
	v_lshl_add_u64 v[244:245], s[28:29], 0, v[132:133]
	s_add_i32 m0, s30, 0x2000
	s_nop 0
	global_load_lds_dwordx4 v[244:245], off
	s_mov_b32 m0, s51
	s_nop 0
	global_load_lds_dwordx4 v[162:163], off
	v_lshl_add_u64 v[162:163], v[196:197], 0, s[8:9]
	s_mov_b32 m0, s54
	s_nop 0
	global_load_lds_dwordx4 v[162:163], off
	s_bitcmp1_b32 s6, 0
	s_cbranch_scc0 .Lwm_in0n_3
	s_waitcnt vmcnt(8)
.Lwm_in0n_3:
	s_waitcnt lgkmcnt(0)
	s_barrier
	s_setprio 1
	s_waitcnt lgkmcnt(0)
	v_mfma_f32_16x16x32_bf16 v[62:65], v[158:161], v[212:215], v[62:65]
	v_mfma_f32_16x16x32_bf16 v[58:61], v[184:187], v[212:215], v[58:61]
	v_mfma_f32_16x16x32_bf16 v[46:49], v[158:161], v[216:219], v[46:49]
	v_mfma_f32_16x16x32_bf16 v[42:45], v[184:187], v[216:219], v[42:45]
	v_mfma_f32_16x16x32_bf16 v[30:33], v[158:161], v[228:231], v[30:33]
	v_mfma_f32_16x16x32_bf16 v[26:29], v[184:187], v[228:231], v[26:29]
	v_mfma_f32_16x16x32_bf16 v[14:17], v[158:161], v[232:235], v[14:17]
	v_mfma_f32_16x16x32_bf16 v[10:13], v[184:187], v[232:235], v[10:13]
	v_mfma_f32_16x16x32_bf16 v[62:65], v[180:183], v[220:223], v[62:65]
	v_mfma_f32_16x16x32_bf16 v[58:61], v[188:191], v[220:223], v[58:61]
	v_mfma_f32_16x16x32_bf16 v[46:49], v[180:183], v[224:227], v[46:49]
	v_mfma_f32_16x16x32_bf16 v[42:45], v[188:191], v[224:227], v[42:45]
	v_mfma_f32_16x16x32_bf16 v[30:33], v[180:183], v[236:239], v[30:33]
	v_mfma_f32_16x16x32_bf16 v[26:29], v[188:191], v[236:239], v[26:29]
	v_mfma_f32_16x16x32_bf16 v[14:17], v[180:183], v[240:243], v[14:17]
	v_mfma_f32_16x16x32_bf16 v[10:13], v[188:191], v[240:243], v[10:13]
	s_setprio 0
	s_setprio 1
	v_mfma_f32_16x16x32_bf16 v[54:57], v[192:195], v[212:215], v[54:57]
	v_mfma_f32_16x16x32_bf16 v[50:53], v[204:207], v[212:215], v[50:53]
	v_mfma_f32_16x16x32_bf16 v[38:41], v[192:195], v[216:219], v[38:41]
	v_mfma_f32_16x16x32_bf16 v[34:37], v[204:207], v[216:219], v[34:37]
	v_mfma_f32_16x16x32_bf16 v[22:25], v[192:195], v[228:231], v[22:25]
	v_mfma_f32_16x16x32_bf16 v[18:21], v[204:207], v[228:231], v[18:21]
	v_mfma_f32_16x16x32_bf16 v[6:9], v[192:195], v[232:235], v[6:9]
	v_mfma_f32_16x16x32_bf16 v[2:5], v[204:207], v[232:235], v[2:5]
	v_mfma_f32_16x16x32_bf16 v[54:57], v[200:203], v[220:223], v[54:57]
	v_mfma_f32_16x16x32_bf16 v[50:53], v[208:211], v[220:223], v[50:53]
	v_mfma_f32_16x16x32_bf16 v[38:41], v[200:203], v[224:227], v[38:41]
	v_mfma_f32_16x16x32_bf16 v[34:37], v[208:211], v[224:227], v[34:37]
	v_mfma_f32_16x16x32_bf16 v[22:25], v[200:203], v[236:239], v[22:25]
	v_mfma_f32_16x16x32_bf16 v[18:21], v[208:211], v[236:239], v[18:21]
	v_mfma_f32_16x16x32_bf16 v[6:9], v[200:203], v[240:243], v[6:9]
	v_mfma_f32_16x16x32_bf16 v[2:5], v[208:211], v[240:243], v[2:5]
	s_setprio 0
	s_waitcnt vmcnt(8)
	s_barrier
	s_add_i32 s64, s64, 2
	s_add_u32 s62, s62, 0x8000
	s_addc_u32 s63, s63, 0
	s_add_u32 s4, s4, 0x100
	s_addc_u32 s5, s5, 0
	s_cmp_gt_u32 s64, 13
	s_cbranch_scc0 .LBB0_192
	s_and_b64 vcc, exec, s[12:13]
	s_cbranch_vccz .LBB0_195
	s_barrier

; #define PG8_STAGE(bufoff, gbase, voff) do { _Pragma("unroll") for (int _i = 0; _i < 2; ++_i) \
;         __builtin_amdgcn_global_load_lds((const unsigned*)((const char*)(gbase) + (voff)[_i]), (LAS unsigned*)(lds + (bufoff) + ldsw + _i * 8192), 16, 0, 0); } while (0)
; #define PG8_LDA(dst, b, h) do { _Pragma("unroll") for (int m = 0; m < 4; ++m) _Pragma("unroll") for (int k = 0; k < 2; ++k) dst[m][k] = *(const LAS bf16x8*)(lds + PG8_SA(b, h) + ((aoff ^ (k * 64)) + m * 2048)); } while (0)
; #define PG8_LDB(dst, b, h) do { _Pragma("unroll") for (int n = 0; n < 2; ++n) _Pragma("unroll") for (int k = 0; k < 2; ++k) dst[n][k] = *(const LAS bf16x8*)(lds + PG8_SB(b, h) + ((boff ^ (k * 64)) + n * 2048)); } while (0)
;     ...
;         for (int t = 0; t < nt; t += 2) {
;             const bool last = (t == nt - 2);
;             const char* a1 = cA + (size_t)(t + 1) * kstepA;
;             const char* a2 = last ? nA : cA + (size_t)(t + 2) * kstepA; const char* b2 = last ? nB : cB + (size_t)(t + 2) * kstepB;
;             const char* a3 = a2 + kstepA; const char* b3 = b2 + kstepB;
;             unsigned vs[2][2];
;             if constexpr (GATHER) {
;                 if (last && has_next) {
; #pragma unroll
;                     for (int hh = 0; hh < 2; ++hh)
; #pragma unroll
;                         for (int i = 0; i < 2; ++i) voffN[hh][i] = (unsigned)idxl[(ui + 1) * 256 + hh * HALF + sR[i]] * (unsigned)(K * 2) + (unsigned)sC[i] * 2u;
;                 }
; #pragma unroll
;                 for (int hh = 0; hh < 2; ++hh)
; #pragma unroll
;                     for (int i = 0; i < 2; ++i) vs[hh][i] = last ? voffN[hh][i] : voffA[hh][i];
;             } else {
; #pragma unroll
;                 for (int hh = 0; hh < 2; ++hh)
; #pragma unroll
;                     for (int i = 0; i < 2; ++i) vs[hh][i] = voffA[hh][i];
;             }
;             PG8_LDB(B0, 0, 0); PG8_LDB(B1, 0, 1); PG8_SCHED; PG8_LDA(At, 0, 0); PG8_STAGE(PG8_SA(1, 1), a1, voffA[1]);
;             PG8_WAIT_V(8); PG8_WAIT_L(0); PG8_BAR; if (do0) { PG8_MMA(0, 0, At, B0); PG8_MMA(0, 1, At, B1); } PG8_BAR; PG8_SCHED;
;             PG8_LDA(At, 0, 1); PG8_STAGE(PG8_SB(0, 0), b2, voffB); PG8_STAGE(PG8_SB(0, 1), b2 + hstep, voffB); PG8_STAGE(PG8_SA(0, 0), a2, vs[0]);
;             PG8_WAIT_V(8); PG8_WAIT_L(0); PG8_BAR; if (do1) { PG8_MMA(1, 0, At, B0); PG8_MMA(1, 1, At, B1); } PG8_BAR; PG8_SCHED;
.LBB0_212:
	ds_read_b128 v[168:171], v153
	ds_read_b128 v[172:175], v154
	ds_read_b128 v[176:179], v155
	ds_read_b128 v[180:183], v156
	ds_read_b128 v[184:187], v157
	ds_read_b128 v[188:191], v158
	ds_read_b128 v[192:195], v159
	ds_read_b128 v[200:203], v160
	s_add_u32 s30, s4, 0x4000
	s_addc_u32 s31, s5, 0
	s_cmp_eq_u32 s64, 12
	s_cselect_b32 s36, s29, s30
	s_cselect_b32 s37, s17, s31
	s_cselect_b32 s34, s61, s62
	s_cselect_b32 s35, s19, s63
	s_add_u32 s30, s36, 0x4000
	s_addc_u32 s31, s37, 0
	v_lshl_add_u64 v[196:197], s[4:5], 0, v[148:149]
	s_add_i32 m0, s27, 0xc000
	ds_read_b128 v[204:207], v161
	ds_read_b128 v[208:211], v161 offset:2048
	ds_read_b128 v[212:215], v162
	ds_read_b128 v[216:219], v162 offset:2048
	ds_read_b128 v[220:223], v161 offset:4096
	ds_read_b128 v[224:227], v161 offset:6144
	ds_read_b128 v[228:231], v162 offset:4096
	ds_read_b128 v[232:235], v162 offset:6144
	global_load_lds_dwordx4 v[196:197], off
	v_lshl_add_u64 v[196:197], s[4:5], 0, v[150:151]
	s_add_i32 m0, s27, 0xe000
	s_nop 0
	global_load_lds_dwordx4 v[196:197], off
	s_bitcmp1_b32 s0, 0
	s_cbranch_scc0 .Lwm_in0s_0
	s_waitcnt vmcnt(8)
.Lwm_in0s_0:
	s_waitcnt lgkmcnt(0)
	s_barrier
	s_setprio 1
	s_waitcnt lgkmcnt(0)
	v_mfma_f32_16x16x32_bf16 v[126:129], v[168:171], v[204:207], v[126:129]
	v_mfma_f32_16x16x32_bf16 v[122:125], v[176:179], v[204:207], v[122:125]
	v_mfma_f32_16x16x32_bf16 v[110:113], v[168:171], v[208:211], v[110:113]
	v_mfma_f32_16x16x32_bf16 v[106:109], v[176:179], v[208:211], v[106:109]
	v_mfma_f32_16x16x32_bf16 v[94:97], v[168:171], v[220:223], v[94:97]
	v_mfma_f32_16x16x32_bf16 v[90:93], v[176:179], v[220:223], v[90:93]
	v_mfma_f32_16x16x32_bf16 v[78:81], v[168:171], v[224:227], v[78:81]
	v_mfma_f32_16x16x32_bf16 v[74:77], v[176:179], v[224:227], v[74:77]
	v_mfma_f32_16x16x32_bf16 v[126:129], v[172:175], v[212:215], v[126:129]
	v_mfma_f32_16x16x32_bf16 v[122:125], v[180:183], v[212:215], v[122:125]
	v_mfma_f32_16x16x32_bf16 v[110:113], v[172:175], v[216:219], v[110:113]
	v_mfma_f32_16x16x32_bf16 v[106:109], v[180:183], v[216:219], v[106:109]
	v_mfma_f32_16x16x32_bf16 v[94:97], v[172:175], v[228:231], v[94:97]
	v_mfma_f32_16x16x32_bf16 v[90:93], v[180:183], v[228:231], v[90:93]
	v_mfma_f32_16x16x32_bf16 v[78:81], v[172:175], v[232:235], v[78:81]
	v_mfma_f32_16x16x32_bf16 v[74:77], v[180:183], v[232:235], v[74:77]
	s_setprio 0
	s_setprio 1
	v_mfma_f32_16x16x32_bf16 v[118:121], v[184:187], v[204:207], v[118:121]
	v_mfma_f32_16x16x32_bf16 v[114:117], v[192:195], v[204:207], v[114:117]
	v_mfma_f32_16x16x32_bf16 v[102:105], v[184:187], v[208:211], v[102:105]
	v_mfma_f32_16x16x32_bf16 v[98:101], v[192:195], v[208:211], v[98:101]
	v_mfma_f32_16x16x32_bf16 v[86:89], v[184:187], v[220:223], v[86:89]
	v_mfma_f32_16x16x32_bf16 v[82:85], v[192:195], v[220:223], v[82:85]
	v_mfma_f32_16x16x32_bf16 v[70:73], v[184:187], v[224:227], v[70:73]
	v_mfma_f32_16x16x32_bf16 v[66:69], v[192:195], v[224:227], v[66:69]
	v_mfma_f32_16x16x32_bf16 v[118:121], v[188:191], v[212:215], v[118:121]
	v_mfma_f32_16x16x32_bf16 v[114:117], v[200:203], v[212:215], v[114:117]
	v_mfma_f32_16x16x32_bf16 v[102:105], v[188:191], v[216:219], v[102:105]
	v_mfma_f32_16x16x32_bf16 v[98:101], v[200:203], v[216:219], v[98:101]
	v_mfma_f32_16x16x32_bf16 v[86:89], v[188:191], v[228:231], v[86:89]
	v_mfma_f32_16x16x32_bf16 v[82:85], v[200:203], v[228:231], v[82:85]
	v_mfma_f32_16x16x32_bf16 v[70:73], v[188:191], v[232:235], v[70:73]
	v_mfma_f32_16x16x32_bf16 v[66:69], v[200:203], v[232:235], v[66:69]
	s_setprio 0
	s_waitcnt vmcnt(8)
	s_barrier
	s_add_i32 s65, s58, s39
	v_lshl_add_u64 v[196:197], s[34:35], 0, v[132:133]
	s_mov_b32 m0, s65
	ds_read_b128 v[204:207], v161 offset:16384
	ds_read_b128 v[208:211], v161 offset:18432
	ds_read_b128 v[212:215], v162 offset:16384
	ds_read_b128 v[216:219], v162 offset:18432
	ds_read_b128 v[220:223], v161 offset:20480
	ds_read_b128 v[224:227], v161 offset:22528
	ds_read_b128 v[228:231], v162 offset:20480
	ds_read_b128 v[232:235], v162 offset:22528
	global_load_lds_dwordx4 v[196:197], off
	s_add_i32 m0, s65, 0x2000
	s_add_u32 s66, s34, 0x40000
	v_lshl_add_u64 v[236:237], s[34:35], 0, v[130:131]
	s_addc_u32 s67, s35, 0
	s_add_i32 s65, s59, s39
	global_load_lds_dwordx4 v[236:237], off
	v_lshl_add_u64 v[238:239], s[66:67], 0, v[132:133]
	s_mov_b32 m0, s65
	s_nop 0
	global_load_lds_dwordx4 v[238:239], off
	v_lshl_add_u64 v[238:239], s[66:67], 0, v[130:131]
	s_add_i32 m0, s65, 0x2000
	s_nop 0
	global_load_lds_dwordx4 v[238:239], off
	v_lshl_add_u64 v[238:239], s[36:37], 0, v[134:135]
	s_mov_b32 m0, s27
	s_nop 0
	global_load_lds_dwordx4 v[238:239], off
	v_lshl_add_u64 v[238:239], s[36:37], 0, v[136:137]
	s_mov_b32 m0, s48
	s_nop 0
	global_load_lds_dwordx4 v[238:239], off
	s_bitcmp1_b32 s0, 0
	s_cbranch_scc0 .Lwm_in0s_1
	s_waitcnt vmcnt(8)
; #define PG8_STAGE(bufoff, gbase, voff) do { _Pragma("unroll") for (int _i = 0; _i < 2; ++_i) \
;         __builtin_amdgcn_global_load_lds((const unsigned*)((const char*)(gbase) + (voff)[_i]), (LAS unsigned*)(lds + (bufoff) + ldsw + _i * 8192), 16, 0, 0); } while (0)
; #define PG8_LDA(dst, b, h) do { _Pragma("unroll") for (int m = 0; m < 4; ++m) _Pragma("unroll") for (int k = 0; k < 2; ++k) dst[m][k] = *(const LAS bf16x8*)(lds + PG8_SA(b, h) + ((aoff ^ (k * 64)) + m * 2048)); } while (0)
; #define PG8_LDB(dst, b, h) do { _Pragma("unroll") for (int n = 0; n < 2; ++n) _Pragma("unroll") for (int k = 0; k < 2; ++k) dst[n][k] = *(const LAS bf16x8*)(lds + PG8_SB(b, h) + ((boff ^ (k * 64)) + n * 2048)); } while (0)
; #define PG8_MMA(ai, bj, At, Bt) do { __builtin_amdgcn_s_setprio(1); _Pragma("unroll") for (int m = 0; m < 4; ++m) _Pragma("unroll") for (int n = 0; n < 2; ++n) _Pragma("unroll") for (int k = 0; k < 2; ++k) \
;         acc[ai][bj][m][n] = __builtin_amdgcn_mfma_f32_16x16x32_bf16(Bt[n][k], At[m][k], acc[ai][bj][m][n], 0, 0, 0); __builtin_amdgcn_s_setprio(0); } while (0)
; #define PG8_WAIT_V(n) asm volatile("s_waitcnt vmcnt(" #n ")" ::: "memory")
; #define PG8_WAIT_L(n) asm volatile("s_waitcnt lgkmcnt(" #n ")" ::: "memory")
; #define PG8_BAR __builtin_amdgcn_s_barrier()
; #define PG8_SCHED __builtin_amdgcn_sched_barrier(0)
;     ...
;             PG8_WAIT_V(8); PG8_WAIT_L(0); PG8_BAR; if (do1) { PG8_MMA(1, 0, At, B0); PG8_MMA(1, 1, At, B1); } PG8_BAR; PG8_SCHED;
;             PG8_LDB(B0, 1, 0); PG8_LDB(B1, 1, 1); PG8_SCHED; PG8_LDA(At, 1, 0); PG8_STAGE(PG8_SA(0, 1), a2, vs[1]);
;             PG8_WAIT_V(8); PG8_WAIT_L(0); PG8_BAR; if (do0) { PG8_MMA(0, 0, At, B0); PG8_MMA(0, 1, At, B1); } PG8_BAR; PG8_SCHED;
.Lwm_in0s_1:
	s_waitcnt lgkmcnt(0)
	s_barrier
	s_setprio 1
	s_waitcnt lgkmcnt(0)
	v_mfma_f32_16x16x32_bf16 v[62:65], v[168:171], v[204:207], v[62:65]
	v_mfma_f32_16x16x32_bf16 v[58:61], v[176:179], v[204:207], v[58:61]
	v_mfma_f32_16x16x32_bf16 v[46:49], v[168:171], v[208:211], v[46:49]
	v_mfma_f32_16x16x32_bf16 v[42:45], v[176:179], v[208:211], v[42:45]
	v_mfma_f32_16x16x32_bf16 v[30:33], v[168:171], v[220:223], v[30:33]
	v_mfma_f32_16x16x32_bf16 v[26:29], v[176:179], v[220:223], v[26:29]
	v_mfma_f32_16x16x32_bf16 v[14:17], v[168:171], v[224:227], v[14:17]
	v_mfma_f32_16x16x32_bf16 v[10:13], v[176:179], v[224:227], v[10:13]
	v_mfma_f32_16x16x32_bf16 v[62:65], v[172:175], v[212:215], v[62:65]
	v_mfma_f32_16x16x32_bf16 v[58:61], v[180:183], v[212:215], v[58:61]
	v_mfma_f32_16x16x32_bf16 v[46:49], v[172:175], v[216:219], v[46:49]
	v_mfma_f32_16x16x32_bf16 v[42:45], v[180:183], v[216:219], v[42:45]
	v_mfma_f32_16x16x32_bf16 v[30:33], v[172:175], v[228:231], v[30:33]
	v_mfma_f32_16x16x32_bf16 v[26:29], v[180:183], v[228:231], v[26:29]
	v_mfma_f32_16x16x32_bf16 v[14:17], v[172:175], v[232:235], v[14:17]
	v_mfma_f32_16x16x32_bf16 v[10:13], v[180:183], v[232:235], v[10:13]
	s_setprio 0
	s_setprio 1
	v_mfma_f32_16x16x32_bf16 v[54:57], v[184:187], v[204:207], v[54:57]
	v_mfma_f32_16x16x32_bf16 v[50:53], v[192:195], v[204:207], v[50:53]
	v_mfma_f32_16x16x32_bf16 v[38:41], v[184:187], v[208:211], v[38:41]
	v_mfma_f32_16x16x32_bf16 v[34:37], v[192:195], v[208:211], v[34:37]
	v_mfma_f32_16x16x32_bf16 v[22:25], v[184:187], v[220:223], v[22:25]
	v_mfma_f32_16x16x32_bf16 v[18:21], v[192:195], v[220:223], v[18:21]
	v_mfma_f32_16x16x32_bf16 v[6:9], v[184:187], v[224:227], v[6:9]
	v_mfma_f32_16x16x32_bf16 v[2:5], v[192:195], v[224:227], v[2:5]
	v_mfma_f32_16x16x32_bf16 v[54:57], v[188:191], v[212:215], v[54:57]
	v_mfma_f32_16x16x32_bf16 v[50:53], v[200:203], v[212:215], v[50:53]
	v_mfma_f32_16x16x32_bf16 v[38:41], v[188:191], v[216:219], v[38:41]
	v_mfma_f32_16x16x32_bf16 v[34:37], v[200:203], v[216:219], v[34:37]
	v_mfma_f32_16x16x32_bf16 v[22:25], v[188:191], v[228:231], v[22:25]
	v_mfma_f32_16x16x32_bf16 v[18:21], v[200:203], v[228:231], v[18:21]
	v_mfma_f32_16x16x32_bf16 v[6:9], v[188:191], v[232:235], v[6:9]
	v_mfma_f32_16x16x32_bf16 v[2:5], v[200:203], v[232:235], v[2:5]
	s_setprio 0
	s_waitcnt vmcnt(8)
	s_barrier
	s_add_i32 s65, 0, 0x18000
	v_add_u32_e32 v167, s65, v143
	v_add_u32_e32 v172, s65, v152
	s_add_i32 s66, 0, 0x1c000
	ds_read_b128 v[168:171], v167
	ds_read_b128 v[172:175], v172
	ds_read_b128 v[176:179], v163
	ds_read_b128 v[180:183], v164
	v_add_u32_e32 v167, s66, v143
	v_add_u32_e32 v188, s66, v152
	ds_read_b128 v[184:187], v167
	ds_read_b128 v[188:191], v188
	ds_read_b128 v[192:195], v165
	ds_read_b128 v[200:203], v166
	s_mov_b32 m0, s49
	v_lshl_add_u64 v[238:239], s[36:37], 0, v[138:139]
	ds_read_b128 v[204:207], v161 offset:32768
	ds_read_b128 v[208:211], v161 offset:34816
	ds_read_b128 v[212:215], v162 offset:32768
	ds_read_b128 v[216:219], v162 offset:34816
	ds_read_b128 v[220:223], v161 offset:36864
	ds_read_b128 v[224:227], v161 offset:38912
	ds_read_b128 v[228:231], v162 offset:36864
	ds_read_b128 v[232:235], v162 offset:38912
	global_load_lds_dwordx4 v[238:239], off
	v_lshl_add_u64 v[238:239], s[36:37], 0, v[140:141]
	s_mov_b32 m0, s50
	s_nop 0
	global_load_lds_dwordx4 v[238:239], off
	s_bitcmp1_b32 s0, 0
	s_cbranch_scc0 .Lwm_in0s_2
	s_waitcnt vmcnt(8)
; #define PG8_STAGE(bufoff, gbase, voff) do { _Pragma("unroll") for (int _i = 0; _i < 2; ++_i) \
;         __builtin_amdgcn_global_load_lds((const unsigned*)((const char*)(gbase) + (voff)[_i]), (LAS unsigned*)(lds + (bufoff) + ldsw + _i * 8192), 16, 0, 0); } while (0)
; #define PG8_LDA(dst, b, h) do { _Pragma("unroll") for (int m = 0; m < 4; ++m) _Pragma("unroll") for (int k = 0; k < 2; ++k) dst[m][k] = *(const LAS bf16x8*)(lds + PG8_SA(b, h) + ((aoff ^ (k * 64)) + m * 2048)); } while (0)
; #define PG8_MMA(ai, bj, At, Bt) do { __builtin_amdgcn_s_setprio(1); _Pragma("unroll") for (int m = 0; m < 4; ++m) _Pragma("unroll") for (int n = 0; n < 2; ++n) _Pragma("unroll") for (int k = 0; k < 2; ++k) \
;         acc[ai][bj][m][n] = __builtin_amdgcn_mfma_f32_16x16x32_bf16(Bt[n][k], At[m][k], acc[ai][bj][m][n], 0, 0, 0); __builtin_amdgcn_s_setprio(0); } while (0)
; #define PG8_WAIT_V(n) asm volatile("s_waitcnt vmcnt(" #n ")" ::: "memory")
; #define PG8_WAIT_L(n) asm volatile("s_waitcnt lgkmcnt(" #n ")" ::: "memory")
; #define PG8_BAR __builtin_amdgcn_s_barrier()
; #define PG8_SCHED __builtin_amdgcn_sched_barrier(0)
;     ...
;             PG8_WAIT_V(8); PG8_WAIT_L(0); PG8_BAR; if (do0) { PG8_MMA(0, 0, At, B0); PG8_MMA(0, 1, At, B1); } PG8_BAR; PG8_SCHED;
;             PG8_LDA(At, 1, 1); PG8_STAGE(PG8_SB(1, 0), b3, voffB); PG8_STAGE(PG8_SB(1, 1), b3 + hstep, voffB); PG8_STAGE(PG8_SA(1, 0), a3, vs[0]);
;             PG8_WAIT_V(8); PG8_WAIT_L(0); PG8_BAR; if (do1) { PG8_MMA(1, 0, At, B0); PG8_MMA(1, 1, At, B1); } PG8_BAR; PG8_SCHED;
;         }
.Lwm_in0s_2:
	s_waitcnt lgkmcnt(0)
	s_barrier
	s_setprio 1
	s_waitcnt lgkmcnt(0)
	v_mfma_f32_16x16x32_bf16 v[126:129], v[168:171], v[204:207], v[126:129]
	v_mfma_f32_16x16x32_bf16 v[122:125], v[176:179], v[204:207], v[122:125]
	v_mfma_f32_16x16x32_bf16 v[110:113], v[168:171], v[208:211], v[110:113]
	v_mfma_f32_16x16x32_bf16 v[106:109], v[176:179], v[208:211], v[106:109]
	v_mfma_f32_16x16x32_bf16 v[94:97], v[168:171], v[220:223], v[94:97]
	v_mfma_f32_16x16x32_bf16 v[90:93], v[176:179], v[220:223], v[90:93]
	v_mfma_f32_16x16x32_bf16 v[78:81], v[168:171], v[224:227], v[78:81]
	v_mfma_f32_16x16x32_bf16 v[74:77], v[176:179], v[224:227], v[74:77]
	v_mfma_f32_16x16x32_bf16 v[126:129], v[172:175], v[212:215], v[126:129]
	v_mfma_f32_16x16x32_bf16 v[122:125], v[180:183], v[212:215], v[122:125]
	v_mfma_f32_16x16x32_bf16 v[110:113], v[172:175], v[216:219], v[110:113]
	v_mfma_f32_16x16x32_bf16 v[106:109], v[180:183], v[216:219], v[106:109]
	v_mfma_f32_16x16x32_bf16 v[94:97], v[172:175], v[228:231], v[94:97]
	v_mfma_f32_16x16x32_bf16 v[90:93], v[180:183], v[228:231], v[90:93]
	v_mfma_f32_16x16x32_bf16 v[78:81], v[172:175], v[232:235], v[78:81]
	v_mfma_f32_16x16x32_bf16 v[74:77], v[180:183], v[232:235], v[74:77]
	s_setprio 0
	s_setprio 1
	v_mfma_f32_16x16x32_bf16 v[118:121], v[184:187], v[204:207], v[118:121]
	v_mfma_f32_16x16x32_bf16 v[114:117], v[192:195], v[204:207], v[114:117]
	v_mfma_f32_16x16x32_bf16 v[102:105], v[184:187], v[208:211], v[102:105]
	v_mfma_f32_16x16x32_bf16 v[98:101], v[192:195], v[208:211], v[98:101]
	v_mfma_f32_16x16x32_bf16 v[86:89], v[184:187], v[220:223], v[86:89]
	v_mfma_f32_16x16x32_bf16 v[82:85], v[192:195], v[220:223], v[82:85]
	v_mfma_f32_16x16x32_bf16 v[70:73], v[184:187], v[224:227], v[70:73]
	v_mfma_f32_16x16x32_bf16 v[66:69], v[192:195], v[224:227], v[66:69]
	v_mfma_f32_16x16x32_bf16 v[118:121], v[188:191], v[212:215], v[118:121]
	v_mfma_f32_16x16x32_bf16 v[114:117], v[200:203], v[212:215], v[114:117]
	v_mfma_f32_16x16x32_bf16 v[102:105], v[188:191], v[216:219], v[102:105]
	v_mfma_f32_16x16x32_bf16 v[98:101], v[200:203], v[216:219], v[98:101]
	v_mfma_f32_16x16x32_bf16 v[86:89], v[188:191], v[228:231], v[86:89]
	v_mfma_f32_16x16x32_bf16 v[82:85], v[200:203], v[228:231], v[82:85]
	v_mfma_f32_16x16x32_bf16 v[70:73], v[188:191], v[232:235], v[70:73]
	v_mfma_f32_16x16x32_bf16 v[66:69], v[200:203], v[232:235], v[66:69]
	s_setprio 0
	s_waitcnt vmcnt(8)
	s_barrier
	s_add_i32 s36, s65, s39
	v_lshl_add_u64 v[196:197], v[196:197], 0, s[12:13]
	s_mov_b32 m0, s36
	ds_read_b128 v[204:207], v161 offset:49152
	ds_read_b128 v[208:211], v161 offset:51200
	ds_read_b128 v[212:215], v162 offset:49152
	ds_read_b128 v[216:219], v162 offset:51200
	ds_read_b128 v[220:223], v161 offset:53248
	ds_read_b128 v[224:227], v161 offset:55296
	ds_read_b128 v[228:231], v162 offset:53248
	ds_read_b128 v[232:235], v162 offset:55296
	global_load_lds_dwordx4 v[196:197], off
	s_add_i32 m0, s36, 0x2000
	s_add_u32 s34, s34, 0x40080
	v_lshl_add_u64 v[196:197], v[236:237], 0, s[12:13]
	s_addc_u32 s35, s35, 0
	s_add_i32 s36, s66, s39
	global_load_lds_dwordx4 v[196:197], off
	v_lshl_add_u64 v[196:197], s[34:35], 0, v[132:133]
	s_mov_b32 m0, s36
	s_nop 0
	global_load_lds_dwordx4 v[196:197], off
	v_lshl_add_u64 v[196:197], s[34:35], 0, v[130:131]
	s_add_i32 m0, s36, 0x2000
	s_nop 0
	global_load_lds_dwordx4 v[196:197], off
	v_lshl_add_u64 v[196:197], s[30:31], 0, v[134:135]
	s_mov_b32 m0, s55
	s_nop 0
	global_load_lds_dwordx4 v[196:197], off
	v_lshl_add_u64 v[196:197], s[30:31], 0, v[136:137]
	s_mov_b32 m0, s56
	s_nop 0
	global_load_lds_dwordx4 v[196:197], off
	s_bitcmp1_b32 s0, 0
	s_cbranch_scc0 .Lwm_in0s_3
	s_waitcnt vmcnt(8)
.Lwm_in0s_3:
	s_waitcnt lgkmcnt(0)
	s_barrier
	s_setprio 1
	s_waitcnt lgkmcnt(0)
	v_mfma_f32_16x16x32_bf16 v[62:65], v[168:171], v[204:207], v[62:65]
	v_mfma_f32_16x16x32_bf16 v[58:61], v[176:179], v[204:207], v[58:61]
	v_mfma_f32_16x16x32_bf16 v[46:49], v[168:171], v[208:211], v[46:49]
	v_mfma_f32_16x16x32_bf16 v[42:45], v[176:179], v[208:211], v[42:45]
	v_mfma_f32_16x16x32_bf16 v[30:33], v[168:171], v[220:223], v[30:33]
	v_mfma_f32_16x16x32_bf16 v[26:29], v[176:179], v[220:223], v[26:29]
	v_mfma_f32_16x16x32_bf16 v[14:17], v[168:171], v[224:227], v[14:17]
	v_mfma_f32_16x16x32_bf16 v[10:13], v[176:179], v[224:227], v[10:13]
	v_mfma_f32_16x16x32_bf16 v[62:65], v[172:175], v[212:215], v[62:65]
	v_mfma_f32_16x16x32_bf16 v[58:61], v[180:183], v[212:215], v[58:61]
	v_mfma_f32_16x16x32_bf16 v[46:49], v[172:175], v[216:219], v[46:49]
	v_mfma_f32_16x16x32_bf16 v[42:45], v[180:183], v[216:219], v[42:45]
	v_mfma_f32_16x16x32_bf16 v[30:33], v[172:175], v[228:231], v[30:33]
	v_mfma_f32_16x16x32_bf16 v[26:29], v[180:183], v[228:231], v[26:29]
	v_mfma_f32_16x16x32_bf16 v[14:17], v[172:175], v[232:235], v[14:17]
	v_mfma_f32_16x16x32_bf16 v[10:13], v[180:183], v[232:235], v[10:13]
	s_setprio 0
	s_setprio 1
	v_mfma_f32_16x16x32_bf16 v[54:57], v[184:187], v[204:207], v[54:57]
	v_mfma_f32_16x16x32_bf16 v[50:53], v[192:195], v[204:207], v[50:53]
	v_mfma_f32_16x16x32_bf16 v[38:41], v[184:187], v[208:211], v[38:41]
	v_mfma_f32_16x16x32_bf16 v[34:37], v[192:195], v[208:211], v[34:37]
	v_mfma_f32_16x16x32_bf16 v[22:25], v[184:187], v[220:223], v[22:25]
	v_mfma_f32_16x16x32_bf16 v[18:21], v[192:195], v[220:223], v[18:21]
	v_mfma_f32_16x16x32_bf16 v[6:9], v[184:187], v[224:227], v[6:9]
	v_mfma_f32_16x16x32_bf16 v[2:5], v[192:195], v[224:227], v[2:5]
	v_mfma_f32_16x16x32_bf16 v[54:57], v[188:191], v[212:215], v[54:57]
	v_mfma_f32_16x16x32_bf16 v[50:53], v[200:203], v[212:215], v[50:53]
	v_mfma_f32_16x16x32_bf16 v[38:41], v[188:191], v[216:219], v[38:41]
	v_mfma_f32_16x16x32_bf16 v[34:37], v[200:203], v[216:219], v[34:37]
	v_mfma_f32_16x16x32_bf16 v[22:25], v[188:191], v[228:231], v[22:25]
	v_mfma_f32_16x16x32_bf16 v[18:21], v[200:203], v[228:231], v[18:21]
	v_mfma_f32_16x16x32_bf16 v[6:9], v[188:191], v[232:235], v[6:9]
	v_mfma_f32_16x16x32_bf16 v[2:5], v[200:203], v[232:235], v[2:5]
	s_setprio 0
	s_waitcnt vmcnt(8)
	s_barrier
	s_add_i32 s64, s64, 2
	s_add_u32 s62, s62, 0x100
	s_addc_u32 s63, s63, 0
	s_add_u32 s4, s4, 0x8000
	s_addc_u32 s5, s5, 0
	s_cmp_gt_u32 s64, 13
	s_cbranch_scc0 .LBB0_212
	s_and_b64 vcc, exec, s[14:15]
	s_cbranch_vccz .LBB0_215
	s_barrier

; #define PG8_MMA(ai, bj, At, Bt) do { __builtin_amdgcn_s_setprio(1); _Pragma("unroll") for (int m = 0; m < 4; ++m) _Pragma("unroll") for (int n = 0; n < 2; ++n) _Pragma("unroll") for (int k = 0; k < 2; ++k) \
;         acc[ai][bj][m][n] = __builtin_amdgcn_mfma_f32_16x16x32_bf16(Bt[n][k], At[m][k], acc[ai][bj][m][n], 0, 0, 0); __builtin_amdgcn_s_setprio(0); } while (0)
; #define PG8_WAIT_V(n) asm volatile("s_waitcnt vmcnt(" #n ")" ::: "memory")
; #define PG8_WAIT_L(n) asm volatile("s_waitcnt lgkmcnt(" #n ")" ::: "memory")
; #define PG8_BAR __builtin_amdgcn_s_barrier()
; #define PG8_SCHED __builtin_amdgcn_sched_barrier(0)
;     ...
;             PG8_WAIT_V(8); PG8_WAIT_L(0); PG8_BAR; if (do1) { PG8_MMA(1, 0, At, B0); PG8_MMA(1, 1, At, B1); } PG8_BAR; PG8_SCHED;
;         }
.LBB0_1005:
	s_waitcnt vmcnt(8)
	s_barrier
	s_add_i32 s65, s65, 2
	s_add_u32 s19, s19, 0x8000
	s_addc_u32 s64, s64, 0
	s_add_u32 s28, s28, 0x100
	s_addc_u32 s29, s29, 0
	s_cmp_gt_u32 s65, 13
	s_cbranch_scc1 .LBB0_1016

; #define PG8_STAGE(bufoff, gbase, voff) do { _Pragma("unroll") for (int _i = 0; _i < 2; ++_i) \
;         __builtin_amdgcn_global_load_lds((const unsigned*)((const char*)(gbase) + (voff)[_i]), (LAS unsigned*)(lds + (bufoff) + ldsw + _i * 8192), 16, 0, 0); } while (0)
; #define PG8_LDA(dst, b, h) do { _Pragma("unroll") for (int m = 0; m < 4; ++m) _Pragma("unroll") for (int k = 0; k < 2; ++k) dst[m][k] = *(const LAS bf16x8*)(lds + PG8_SA(b, h) + ((aoff ^ (k * 64)) + m * 2048)); } while (0)
; #define PG8_LDB(dst, b, h) do { _Pragma("unroll") for (int n = 0; n < 2; ++n) _Pragma("unroll") for (int k = 0; k < 2; ++k) dst[n][k] = *(const LAS bf16x8*)(lds + PG8_SB(b, h) + ((boff ^ (k * 64)) + n * 2048)); } while (0)
; #define PG8_BAR __builtin_amdgcn_s_barrier()
;     ...
;             const bool last = (t == nt - 2);
;             const char* a1 = cA + (size_t)(t + 1) * kstepA;
;             const char* a2 = last ? nA : cA + (size_t)(t + 2) * kstepA; const char* b2 = last ? nB : cB + (size_t)(t + 2) * kstepB;
;             const char* a3 = a2 + kstepA; const char* b3 = b2 + kstepB;
;             unsigned vs[2][2];
;             if constexpr (GATHER) {
;                 if (last && has_next) {
; #pragma unroll
;                     for (int hh = 0; hh < 2; ++hh)
; #pragma unroll
;                         for (int i = 0; i < 2; ++i) voffN[hh][i] = (unsigned)idxl[(ui + 1) * 256 + hh * HALF + sR[i]] * (unsigned)(K * 2) + (unsigned)sC[i] * 2u;
;                 }
; #pragma unroll
;                 for (int hh = 0; hh < 2; ++hh)
; #pragma unroll
;                     for (int i = 0; i < 2; ++i) vs[hh][i] = last ? voffN[hh][i] : voffA[hh][i];
;             } else {
; #pragma unroll
;                 for (int hh = 0; hh < 2; ++hh)
; #pragma unroll
;                     for (int i = 0; i < 2; ++i) vs[hh][i] = voffA[hh][i];
;             }
;             PG8_LDB(B0, 0, 0); PG8_LDB(B1, 0, 1); PG8_SCHED; PG8_LDA(At, 0, 0); PG8_STAGE(PG8_SA(1, 1), a1, voffA[1]);
;             PG8_WAIT_V(8); PG8_WAIT_L(0); PG8_BAR; if (do0) { PG8_MMA(0, 0, At, B0); PG8_MMA(0, 1, At, B1); } PG8_BAR; PG8_SCHED;
;             PG8_LDA(At, 0, 1); PG8_STAGE(PG8_SB(0, 0), b2, voffB); PG8_STAGE(PG8_SB(0, 1), b2 + hstep, voffB); PG8_STAGE(PG8_SA(0, 0), a2, vs[0]);
;             PG8_WAIT_V(8); PG8_WAIT_L(0); PG8_BAR; if (do1) { PG8_MMA(1, 0, At, B0); PG8_MMA(1, 1, At, B1); } PG8_BAR; PG8_SCHED;
.LBB0_1008:
	v_add_u32_e32 v2, s54, v226
	v_add_u32_e32 v134, s54, v227
	ds_read_b128 v[150:153], v2
	ds_read_b128 v[154:157], v134
	v_add_u32_e32 v2, s55, v226
	v_add_u32_e32 v134, s55, v227
	ds_read_b128 v[158:161], v2
	ds_read_b128 v[162:165], v134
	v_add_u32_e32 v2, s56, v226
	v_add_u32_e32 v138, s56, v227
	ds_read_b128 v[134:137], v2
	ds_read_b128 v[138:141], v138
	v_add_u32_e32 v2, s57, v226
	v_add_u32_e32 v146, s57, v227
	ds_read_b128 v[142:145], v2
	ds_read_b128 v[146:149], v146
	v_lshl_add_u64 v[224:225], v[222:223], 0, s[28:29]
	s_add_i32 m0, s23, 0xc000
	s_waitcnt lgkmcnt(0)
	ds_read_b128 v[190:193], v228
	ds_read_b128 v[178:181], v228 offset:2048
	ds_read_b128 v[194:197], v229
	ds_read_b128 v[182:185], v229 offset:2048
	ds_read_b128 v[174:177], v228 offset:4096
	ds_read_b128 v[166:169], v228 offset:6144
	ds_read_b128 v[186:189], v229 offset:4096
	ds_read_b128 v[170:173], v229 offset:6144
	global_load_lds_dwordx4 v[224:225], off
	v_lshl_add_u64 v[224:225], v[220:221], 0, s[28:29]
	s_add_i32 m0, s23, 0xe000
	v_cndmask_b32_e64 v2, 0, 1, s[26:27]
	global_load_lds_dwordx4 v[224:225], off
	s_bitcmp1_b32 s2, 0
	s_cbranch_scc0 .Lwm_guL0_0
	s_waitcnt vmcnt(8)
.Lwm_guL0_0:
	s_waitcnt lgkmcnt(0)
	v_cmp_ne_u32_e64 s[8:9], 1, v2
	s_andn2_b64 vcc, exec, s[26:27]
	s_barrier
	s_cbranch_vccnz .LBB0_1010
	s_setprio 1
	s_waitcnt lgkmcnt(0)
	v_mfma_f32_16x16x32_bf16 v[130:133], v[150:153], v[190:193], v[130:133]
	v_mfma_f32_16x16x32_bf16 v[126:129], v[158:161], v[190:193], v[126:129]
	v_mfma_f32_16x16x32_bf16 v[114:117], v[150:153], v[178:181], v[114:117]
	v_mfma_f32_16x16x32_bf16 v[110:113], v[158:161], v[178:181], v[110:113]
	v_mfma_f32_16x16x32_bf16 v[98:101], v[150:153], v[174:177], v[98:101]
	v_mfma_f32_16x16x32_bf16 v[94:97], v[158:161], v[174:177], v[94:97]
	v_mfma_f32_16x16x32_bf16 v[82:85], v[150:153], v[166:169], v[82:85]
	v_mfma_f32_16x16x32_bf16 v[78:81], v[158:161], v[166:169], v[78:81]
	v_mfma_f32_16x16x32_bf16 v[130:133], v[154:157], v[194:197], v[130:133]
	v_mfma_f32_16x16x32_bf16 v[126:129], v[162:165], v[194:197], v[126:129]
	v_mfma_f32_16x16x32_bf16 v[114:117], v[154:157], v[182:185], v[114:117]
	v_mfma_f32_16x16x32_bf16 v[110:113], v[162:165], v[182:185], v[110:113]
	v_mfma_f32_16x16x32_bf16 v[98:101], v[154:157], v[186:189], v[98:101]
	v_mfma_f32_16x16x32_bf16 v[94:97], v[162:165], v[186:189], v[94:97]
	v_mfma_f32_16x16x32_bf16 v[82:85], v[154:157], v[170:173], v[82:85]
	v_mfma_f32_16x16x32_bf16 v[78:81], v[162:165], v[170:173], v[78:81]
	s_setprio 0
	s_setprio 1
	v_mfma_f32_16x16x32_bf16 v[122:125], v[134:137], v[190:193], v[122:125]
	v_mfma_f32_16x16x32_bf16 v[118:121], v[142:145], v[190:193], v[118:121]
	v_mfma_f32_16x16x32_bf16 v[106:109], v[134:137], v[178:181], v[106:109]
	v_mfma_f32_16x16x32_bf16 v[102:105], v[142:145], v[178:181], v[102:105]
	v_mfma_f32_16x16x32_bf16 v[90:93], v[134:137], v[174:177], v[90:93]
	v_mfma_f32_16x16x32_bf16 v[86:89], v[142:145], v[174:177], v[86:89]
	v_mfma_f32_16x16x32_bf16 v[74:77], v[134:137], v[166:169], v[74:77]
	v_mfma_f32_16x16x32_bf16 v[70:73], v[142:145], v[166:169], v[70:73]
	v_mfma_f32_16x16x32_bf16 v[122:125], v[138:141], v[194:197], v[122:125]
	v_mfma_f32_16x16x32_bf16 v[118:121], v[146:149], v[194:197], v[118:121]
	v_mfma_f32_16x16x32_bf16 v[106:109], v[138:141], v[182:185], v[106:109]
	v_mfma_f32_16x16x32_bf16 v[102:105], v[146:149], v[182:185], v[102:105]
	v_mfma_f32_16x16x32_bf16 v[90:93], v[138:141], v[186:189], v[90:93]
	v_mfma_f32_16x16x32_bf16 v[86:89], v[146:149], v[186:189], v[86:89]
	v_mfma_f32_16x16x32_bf16 v[74:77], v[138:141], v[170:173], v[74:77]
	v_mfma_f32_16x16x32_bf16 v[70:73], v[146:149], v[170:173], v[70:73]
	s_setprio 0
.LBB0_1010:
	s_add_u32 s10, s90, s28
	s_addc_u32 s11, s91, s29
	s_add_u32 s30, s10, 0x4213700
	s_addc_u32 s31, s11, 0
	s_and_b64 s[10:11], s[6:7], exec
	v_cndmask_b32_e64 v2, v218, v4, s[6:7]
	v_cndmask_b32_e64 v224, v219, v5, s[6:7]
	s_cselect_b32 s35, s83, s31
	s_cselect_b32 s34, s82, s30
	s_cselect_b32 s31, s21, s64
	s_cselect_b32 s30, s20, s19
	s_waitcnt vmcnt(8)
	s_barrier
	s_mov_b32 m0, s37
	v_lshl_add_u64 v[232:233], s[30:31], 0, v[202:203]
	s_add_u32 s10, s30, 0x40000
	s_waitcnt lgkmcnt(0)
	ds_read_b128 v[190:193], v228 offset:16384
	ds_read_b128 v[178:181], v228 offset:18432
	ds_read_b128 v[194:197], v229 offset:16384
	ds_read_b128 v[182:185], v229 offset:18432
	ds_read_b128 v[174:177], v228 offset:20480
	ds_read_b128 v[166:169], v228 offset:22528
	ds_read_b128 v[186:189], v229 offset:20480
	ds_read_b128 v[170:173], v229 offset:22528
	global_load_lds_dwordx4 v[232:233], off
	v_lshl_add_u64 v[232:233], s[30:31], 0, v[204:205]
	s_mov_b32 m0, s38
	s_addc_u32 s11, s31, 0
	global_load_lds_dwordx4 v[232:233], off
	v_lshl_add_u64 v[232:233], s[10:11], 0, v[202:203]
	s_mov_b32 m0, s39
	v_cndmask_b32_e64 v213, 0, 1, s[24:25]
	global_load_lds_dwordx4 v[232:233], off
	v_lshl_add_u64 v[232:233], s[10:11], 0, v[204:205]
	s_mov_b32 m0, s40
	v_cmp_ne_u32_e64 s[10:11], 1, v213
	global_load_lds_dwordx4 v[232:233], off
	s_mov_b32 m0, s23
	s_andn2_b64 vcc, exec, s[24:25]
	global_load_lds_dwordx4 v2, s[34:35]
	s_mov_b32 m0, s41
	s_nop 0
	global_load_lds_dwordx4 v224, s[34:35]
	s_bitcmp1_b32 s2, 0
	s_cbranch_scc0 .Lwm_guL0_1
	s_waitcnt vmcnt(8)
; #define PG8_STAGE(bufoff, gbase, voff) do { _Pragma("unroll") for (int _i = 0; _i < 2; ++_i) \
;         __builtin_amdgcn_global_load_lds((const unsigned*)((const char*)(gbase) + (voff)[_i]), (LAS unsigned*)(lds + (bufoff) + ldsw + _i * 8192), 16, 0, 0); } while (0)
; #define PG8_LDA(dst, b, h) do { _Pragma("unroll") for (int m = 0; m < 4; ++m) _Pragma("unroll") for (int k = 0; k < 2; ++k) dst[m][k] = *(const LAS bf16x8*)(lds + PG8_SA(b, h) + ((aoff ^ (k * 64)) + m * 2048)); } while (0)
; #define PG8_LDB(dst, b, h) do { _Pragma("unroll") for (int n = 0; n < 2; ++n) _Pragma("unroll") for (int k = 0; k < 2; ++k) dst[n][k] = *(const LAS bf16x8*)(lds + PG8_SB(b, h) + ((boff ^ (k * 64)) + n * 2048)); } while (0)
; #define PG8_MMA(ai, bj, At, Bt) do { __builtin_amdgcn_s_setprio(1); _Pragma("unroll") for (int m = 0; m < 4; ++m) _Pragma("unroll") for (int n = 0; n < 2; ++n) _Pragma("unroll") for (int k = 0; k < 2; ++k) \
;         acc[ai][bj][m][n] = __builtin_amdgcn_mfma_f32_16x16x32_bf16(Bt[n][k], At[m][k], acc[ai][bj][m][n], 0, 0, 0); __builtin_amdgcn_s_setprio(0); } while (0)
; #define PG8_WAIT_V(n) asm volatile("s_waitcnt vmcnt(" #n ")" ::: "memory")
; #define PG8_WAIT_L(n) asm volatile("s_waitcnt lgkmcnt(" #n ")" ::: "memory")
; #define PG8_BAR __builtin_amdgcn_s_barrier()
;     ...
;                     for (int i = 0; i < 2; ++i) vs[hh][i] = last ? voffN[hh][i] : voffA[hh][i];
;             } else {
; #pragma unroll
;                 for (int hh = 0; hh < 2; ++hh)
; #pragma unroll
;                     for (int i = 0; i < 2; ++i) vs[hh][i] = voffA[hh][i];
;             }
;             PG8_LDB(B0, 0, 0); PG8_LDB(B1, 0, 1); PG8_SCHED; PG8_LDA(At, 0, 0); PG8_STAGE(PG8_SA(1, 1), a1, voffA[1]);
;             PG8_WAIT_V(8); PG8_WAIT_L(0); PG8_BAR; if (do0) { PG8_MMA(0, 0, At, B0); PG8_MMA(0, 1, At, B1); } PG8_BAR; PG8_SCHED;
;             PG8_LDA(At, 0, 1); PG8_STAGE(PG8_SB(0, 0), b2, voffB); PG8_STAGE(PG8_SB(0, 1), b2 + hstep, voffB); PG8_STAGE(PG8_SA(0, 0), a2, vs[0]);
;             PG8_WAIT_V(8); PG8_WAIT_L(0); PG8_BAR; if (do1) { PG8_MMA(1, 0, At, B0); PG8_MMA(1, 1, At, B1); } PG8_BAR; PG8_SCHED;
;             PG8_LDB(B0, 1, 0); PG8_LDB(B1, 1, 1); PG8_SCHED; PG8_LDA(At, 1, 0); PG8_STAGE(PG8_SA(0, 1), a2, vs[1]);
;             PG8_WAIT_V(8); PG8_WAIT_L(0); PG8_BAR; if (do0) { PG8_MMA(0, 0, At, B0); PG8_MMA(0, 1, At, B1); } PG8_BAR; PG8_SCHED;
.Lwm_guL0_1:
	s_waitcnt lgkmcnt(0)
	s_barrier
	s_cbranch_vccnz .LBB0_1012
	s_setprio 1
	s_waitcnt lgkmcnt(0)
	v_mfma_f32_16x16x32_bf16 v[66:69], v[150:153], v[190:193], v[66:69]
	v_mfma_f32_16x16x32_bf16 v[62:65], v[158:161], v[190:193], v[62:65]
	v_mfma_f32_16x16x32_bf16 v[50:53], v[150:153], v[178:181], v[50:53]
	v_mfma_f32_16x16x32_bf16 v[46:49], v[158:161], v[178:181], v[46:49]
	v_mfma_f32_16x16x32_bf16 v[34:37], v[150:153], v[174:177], v[34:37]
	v_mfma_f32_16x16x32_bf16 v[30:33], v[158:161], v[174:177], v[30:33]
	v_mfma_f32_16x16x32_bf16 v[18:21], v[150:153], v[166:169], v[18:21]
	v_mfma_f32_16x16x32_bf16 v[14:17], v[158:161], v[166:169], v[14:17]
	v_mfma_f32_16x16x32_bf16 v[66:69], v[154:157], v[194:197], v[66:69]
	v_mfma_f32_16x16x32_bf16 v[62:65], v[162:165], v[194:197], v[62:65]
	v_mfma_f32_16x16x32_bf16 v[50:53], v[154:157], v[182:185], v[50:53]
	v_mfma_f32_16x16x32_bf16 v[46:49], v[162:165], v[182:185], v[46:49]
	v_mfma_f32_16x16x32_bf16 v[34:37], v[154:157], v[186:189], v[34:37]
	v_mfma_f32_16x16x32_bf16 v[30:33], v[162:165], v[186:189], v[30:33]
	v_mfma_f32_16x16x32_bf16 v[18:21], v[154:157], v[170:173], v[18:21]
	v_mfma_f32_16x16x32_bf16 v[14:17], v[162:165], v[170:173], v[14:17]
	s_setprio 0
	s_setprio 1
	v_mfma_f32_16x16x32_bf16 v[58:61], v[134:137], v[190:193], v[58:61]
	v_mfma_f32_16x16x32_bf16 v[54:57], v[142:145], v[190:193], v[54:57]
	v_mfma_f32_16x16x32_bf16 v[42:45], v[134:137], v[178:181], v[42:45]
	v_mfma_f32_16x16x32_bf16 v[38:41], v[142:145], v[178:181], v[38:41]
	v_mfma_f32_16x16x32_bf16 v[26:29], v[134:137], v[174:177], v[26:29]
	v_mfma_f32_16x16x32_bf16 v[22:25], v[142:145], v[174:177], v[22:25]
	v_mfma_f32_16x16x32_bf16 v[10:13], v[134:137], v[166:169], v[10:13]
	v_mfma_f32_16x16x32_bf16 v[6:9], v[142:145], v[166:169], v[6:9]
	v_mfma_f32_16x16x32_bf16 v[58:61], v[138:141], v[194:197], v[58:61]
	v_mfma_f32_16x16x32_bf16 v[54:57], v[146:149], v[194:197], v[54:57]
	v_mfma_f32_16x16x32_bf16 v[42:45], v[138:141], v[182:185], v[42:45]
	v_mfma_f32_16x16x32_bf16 v[38:41], v[146:149], v[182:185], v[38:41]
	v_mfma_f32_16x16x32_bf16 v[26:29], v[138:141], v[186:189], v[26:29]
	v_mfma_f32_16x16x32_bf16 v[22:25], v[146:149], v[186:189], v[22:25]
	v_mfma_f32_16x16x32_bf16 v[10:13], v[138:141], v[170:173], v[10:13]
	v_mfma_f32_16x16x32_bf16 v[6:9], v[146:149], v[170:173], v[6:9]
	s_setprio 0
.LBB0_1012:
	v_cndmask_b32_e64 v213, v214, v215, s[6:7]
	v_cndmask_b32_e64 v225, v216, v217, s[6:7]
	s_waitcnt vmcnt(8)
	s_barrier
	s_add_i32 s6, 0, 0x18000
	v_add_u32_e32 v134, s6, v226
	v_add_u32_e32 v135, s6, v227
	ds_read_b128 v[150:153], v134
	ds_read_b128 v[154:157], v135
	v_add_u32_e32 v134, s58, v226
	s_add_i32 s6, 0, 0x1c000
	v_add_u32_e32 v135, s58, v227
	ds_read_b128 v[158:161], v134
	ds_read_b128 v[162:165], v135
	v_add_u32_e32 v134, s6, v226
	v_add_u32_e32 v138, s6, v227
	v_add_u32_e32 v142, s59, v226
	v_add_u32_e32 v146, s59, v227
	ds_read_b128 v[134:137], v134
	ds_read_b128 v[138:141], v138
	ds_read_b128 v[142:145], v142
	ds_read_b128 v[146:149], v146
	s_mov_b32 m0, s42
	s_waitcnt lgkmcnt(0)
	ds_read_b128 v[190:193], v228 offset:32768
	ds_read_b128 v[178:181], v228 offset:34816
	ds_read_b128 v[194:197], v229 offset:32768
	ds_read_b128 v[182:185], v229 offset:34816
	ds_read_b128 v[174:177], v228 offset:36864
	ds_read_b128 v[166:169], v228 offset:38912
	ds_read_b128 v[186:189], v229 offset:36864
	ds_read_b128 v[170:173], v229 offset:38912
	global_load_lds_dwordx4 v213, s[34:35]
	s_mov_b32 m0, s43
	s_and_b64 vcc, exec, s[8:9]
	global_load_lds_dwordx4 v225, s[34:35]
	s_bitcmp1_b32 s2, 0
	s_cbranch_scc0 .Lwm_guL0_2
	s_waitcnt vmcnt(8)
.Lwm_guL0_2:
	s_waitcnt lgkmcnt(0)
	s_barrier
	s_cbranch_vccnz .LBB0_1014
	s_setprio 1
	s_waitcnt lgkmcnt(0)
	v_mfma_f32_16x16x32_bf16 v[130:133], v[150:153], v[190:193], v[130:133]
	v_mfma_f32_16x16x32_bf16 v[126:129], v[158:161], v[190:193], v[126:129]
	v_mfma_f32_16x16x32_bf16 v[114:117], v[150:153], v[178:181], v[114:117]
	v_mfma_f32_16x16x32_bf16 v[110:113], v[158:161], v[178:181], v[110:113]
	v_mfma_f32_16x16x32_bf16 v[98:101], v[150:153], v[174:177], v[98:101]
	v_mfma_f32_16x16x32_bf16 v[94:97], v[158:161], v[174:177], v[94:97]
	v_mfma_f32_16x16x32_bf16 v[82:85], v[150:153], v[166:169], v[82:85]
	v_mfma_f32_16x16x32_bf16 v[78:81], v[158:161], v[166:169], v[78:81]
	v_mfma_f32_16x16x32_bf16 v[130:133], v[154:157], v[194:197], v[130:133]
	v_mfma_f32_16x16x32_bf16 v[126:129], v[162:165], v[194:197], v[126:129]
	v_mfma_f32_16x16x32_bf16 v[114:117], v[154:157], v[182:185], v[114:117]
	v_mfma_f32_16x16x32_bf16 v[110:113], v[162:165], v[182:185], v[110:113]
	v_mfma_f32_16x16x32_bf16 v[98:101], v[154:157], v[186:189], v[98:101]
	v_mfma_f32_16x16x32_bf16 v[94:97], v[162:165], v[186:189], v[94:97]
	v_mfma_f32_16x16x32_bf16 v[82:85], v[154:157], v[170:173], v[82:85]
	v_mfma_f32_16x16x32_bf16 v[78:81], v[162:165], v[170:173], v[78:81]
	s_setprio 0
	s_setprio 1
	v_mfma_f32_16x16x32_bf16 v[122:125], v[134:137], v[190:193], v[122:125]
	v_mfma_f32_16x16x32_bf16 v[118:121], v[142:145], v[190:193], v[118:121]
	v_mfma_f32_16x16x32_bf16 v[106:109], v[134:137], v[178:181], v[106:109]
	v_mfma_f32_16x16x32_bf16 v[102:105], v[142:145], v[178:181], v[102:105]
	v_mfma_f32_16x16x32_bf16 v[90:93], v[134:137], v[174:177], v[90:93]
	v_mfma_f32_16x16x32_bf16 v[86:89], v[142:145], v[174:177], v[86:89]
	v_mfma_f32_16x16x32_bf16 v[74:77], v[134:137], v[166:169], v[74:77]
	v_mfma_f32_16x16x32_bf16 v[70:73], v[142:145], v[166:169], v[70:73]
	v_mfma_f32_16x16x32_bf16 v[122:125], v[138:141], v[194:197], v[122:125]
	v_mfma_f32_16x16x32_bf16 v[118:121], v[146:149], v[194:197], v[118:121]
	v_mfma_f32_16x16x32_bf16 v[106:109], v[138:141], v[182:185], v[106:109]
	v_mfma_f32_16x16x32_bf16 v[102:105], v[146:149], v[182:185], v[102:105]
	v_mfma_f32_16x16x32_bf16 v[90:93], v[138:141], v[186:189], v[90:93]
	v_mfma_f32_16x16x32_bf16 v[86:89], v[146:149], v[186:189], v[86:89]
	v_mfma_f32_16x16x32_bf16 v[74:77], v[138:141], v[170:173], v[74:77]
	v_mfma_f32_16x16x32_bf16 v[70:73], v[146:149], v[170:173], v[70:73]
	s_setprio 0
; #define PG8_STAGE(bufoff, gbase, voff) do { _Pragma("unroll") for (int _i = 0; _i < 2; ++_i) \
;         __builtin_amdgcn_global_load_lds((const unsigned*)((const char*)(gbase) + (voff)[_i]), (LAS unsigned*)(lds + (bufoff) + ldsw + _i * 8192), 16, 0, 0); } while (0)
; #define PG8_LDA(dst, b, h) do { _Pragma("unroll") for (int m = 0; m < 4; ++m) _Pragma("unroll") for (int k = 0; k < 2; ++k) dst[m][k] = *(const LAS bf16x8*)(lds + PG8_SA(b, h) + ((aoff ^ (k * 64)) + m * 2048)); } while (0)
; #define PG8_MMA(ai, bj, At, Bt) do { __builtin_amdgcn_s_setprio(1); _Pragma("unroll") for (int m = 0; m < 4; ++m) _Pragma("unroll") for (int n = 0; n < 2; ++n) _Pragma("unroll") for (int k = 0; k < 2; ++k) \
;         acc[ai][bj][m][n] = __builtin_amdgcn_mfma_f32_16x16x32_bf16(Bt[n][k], At[m][k], acc[ai][bj][m][n], 0, 0, 0); __builtin_amdgcn_s_setprio(0); } while (0)
; #define PG8_WAIT_V(n) asm volatile("s_waitcnt vmcnt(" #n ")" ::: "memory")
; #define PG8_WAIT_L(n) asm volatile("s_waitcnt lgkmcnt(" #n ")" ::: "memory")
; #define PG8_BAR __builtin_amdgcn_s_barrier()
; #define PG8_SCHED __builtin_amdgcn_sched_barrier(0)
;     ...
;             PG8_LDA(At, 1, 1); PG8_STAGE(PG8_SB(1, 0), b3, voffB); PG8_STAGE(PG8_SB(1, 1), b3 + hstep, voffB); PG8_STAGE(PG8_SA(1, 0), a3, vs[0]);
;             PG8_WAIT_V(8); PG8_WAIT_L(0); PG8_BAR; if (do1) { PG8_MMA(1, 0, At, B0); PG8_MMA(1, 1, At, B1); } PG8_BAR; PG8_SCHED;
.LBB0_1014:
	v_mov_b32_e32 v225, v3
	s_add_u32 s6, s30, 0x4000
	v_lshl_add_u64 v[232:233], s[34:35], 0, v[2:3]
	v_lshl_add_u64 v[224:225], s[34:35], 0, v[224:225]
	s_addc_u32 s7, s31, 0
	s_waitcnt vmcnt(8)
	s_barrier
	s_mov_b32 m0, s47
	v_lshl_add_u64 v[234:235], s[6:7], 0, v[202:203]
	s_waitcnt lgkmcnt(0)
	ds_read_b128 v[190:193], v228 offset:49152
	ds_read_b128 v[178:181], v228 offset:51200
	ds_read_b128 v[194:197], v229 offset:49152
	ds_read_b128 v[182:185], v229 offset:51200
	ds_read_b128 v[174:177], v228 offset:53248
	ds_read_b128 v[166:169], v228 offset:55296
	ds_read_b128 v[186:189], v229 offset:53248
	ds_read_b128 v[170:173], v229 offset:55296
	global_load_lds_dwordx4 v[234:235], off
	v_lshl_add_u64 v[234:235], s[6:7], 0, v[204:205]
	s_add_u32 s6, s30, 0x44000
	s_mov_b32 m0, s48
	s_addc_u32 s7, s31, 0
	global_load_lds_dwordx4 v[234:235], off
	v_lshl_add_u64 v[234:235], s[6:7], 0, v[202:203]
	s_mov_b32 m0, s51
	v_lshl_add_u64 v[232:233], v[232:233], 0, s[16:17]
	global_load_lds_dwordx4 v[234:235], off
	v_lshl_add_u64 v[234:235], s[6:7], 0, v[204:205]
	s_mov_b32 m0, s52
	v_lshl_add_u64 v[224:225], v[224:225], 0, s[16:17]
	global_load_lds_dwordx4 v[234:235], off
	s_mov_b32 m0, s49
	s_and_b64 vcc, exec, s[10:11]
	global_load_lds_dwordx4 v[232:233], off
	s_mov_b32 m0, s50
	s_nop 0
	global_load_lds_dwordx4 v[224:225], off
	s_bitcmp1_b32 s2, 0
	s_cbranch_scc0 .Lwm_guL0_3
	s_waitcnt vmcnt(8)
.Lwm_guL0_3:
	s_waitcnt lgkmcnt(0)
	s_barrier
	s_cbranch_vccnz .LBB0_1005
	s_setprio 1
	s_waitcnt lgkmcnt(0)
	v_mfma_f32_16x16x32_bf16 v[66:69], v[150:153], v[190:193], v[66:69]
	v_mfma_f32_16x16x32_bf16 v[62:65], v[158:161], v[190:193], v[62:65]
	v_mfma_f32_16x16x32_bf16 v[50:53], v[150:153], v[178:181], v[50:53]
	v_mfma_f32_16x16x32_bf16 v[46:49], v[158:161], v[178:181], v[46:49]
	v_mfma_f32_16x16x32_bf16 v[34:37], v[150:153], v[174:177], v[34:37]
	v_mfma_f32_16x16x32_bf16 v[30:33], v[158:161], v[174:177], v[30:33]
	v_mfma_f32_16x16x32_bf16 v[18:21], v[150:153], v[166:169], v[18:21]
	v_mfma_f32_16x16x32_bf16 v[14:17], v[158:161], v[166:169], v[14:17]
	v_mfma_f32_16x16x32_bf16 v[66:69], v[154:157], v[194:197], v[66:69]
	v_mfma_f32_16x16x32_bf16 v[62:65], v[162:165], v[194:197], v[62:65]
	v_mfma_f32_16x16x32_bf16 v[50:53], v[154:157], v[182:185], v[50:53]
	v_mfma_f32_16x16x32_bf16 v[46:49], v[162:165], v[182:185], v[46:49]
	v_mfma_f32_16x16x32_bf16 v[34:37], v[154:157], v[186:189], v[34:37]
	v_mfma_f32_16x16x32_bf16 v[30:33], v[162:165], v[186:189], v[30:33]
	v_mfma_f32_16x16x32_bf16 v[18:21], v[154:157], v[170:173], v[18:21]
	v_mfma_f32_16x16x32_bf16 v[14:17], v[162:165], v[170:173], v[14:17]
	s_setprio 0
	s_setprio 1
	v_mfma_f32_16x16x32_bf16 v[58:61], v[134:137], v[190:193], v[58:61]
	v_mfma_f32_16x16x32_bf16 v[54:57], v[142:145], v[190:193], v[54:57]
	v_mfma_f32_16x16x32_bf16 v[42:45], v[134:137], v[178:181], v[42:45]
	v_mfma_f32_16x16x32_bf16 v[38:41], v[142:145], v[178:181], v[38:41]
	v_mfma_f32_16x16x32_bf16 v[26:29], v[134:137], v[174:177], v[26:29]
	v_mfma_f32_16x16x32_bf16 v[22:25], v[142:145], v[174:177], v[22:25]
	v_mfma_f32_16x16x32_bf16 v[10:13], v[134:137], v[166:169], v[10:13]
	v_mfma_f32_16x16x32_bf16 v[6:9], v[142:145], v[166:169], v[6:9]
	v_mfma_f32_16x16x32_bf16 v[58:61], v[138:141], v[194:197], v[58:61]
	v_mfma_f32_16x16x32_bf16 v[54:57], v[146:149], v[194:197], v[54:57]
	v_mfma_f32_16x16x32_bf16 v[42:45], v[138:141], v[182:185], v[42:45]
	v_mfma_f32_16x16x32_bf16 v[38:41], v[146:149], v[182:185], v[38:41]
	v_mfma_f32_16x16x32_bf16 v[26:29], v[138:141], v[186:189], v[26:29]
	v_mfma_f32_16x16x32_bf16 v[22:25], v[146:149], v[186:189], v[22:25]
	v_mfma_f32_16x16x32_bf16 v[10:13], v[138:141], v[170:173], v[10:13]
	v_mfma_f32_16x16x32_bf16 v[6:9], v[146:149], v[170:173], v[6:9]
	s_setprio 0
	s_branch .LBB0_1005

; #define PG8_STAGE(bufoff, gbase, voff) do { _Pragma("unroll") for (int _i = 0; _i < 2; ++_i) \
;         __builtin_amdgcn_global_load_lds((const unsigned*)((const char*)(gbase) + (voff)[_i]), (LAS unsigned*)(lds + (bufoff) + ldsw + _i * 8192), 16, 0, 0); } while (0)
; #define PG8_LDA(dst, b, h) do { _Pragma("unroll") for (int m = 0; m < 4; ++m) _Pragma("unroll") for (int k = 0; k < 2; ++k) dst[m][k] = *(const LAS bf16x8*)(lds + PG8_SA(b, h) + ((aoff ^ (k * 64)) + m * 2048)); } while (0)
; #define PG8_LDB(dst, b, h) do { _Pragma("unroll") for (int n = 0; n < 2; ++n) _Pragma("unroll") for (int k = 0; k < 2; ++k) dst[n][k] = *(const LAS bf16x8*)(lds + PG8_SB(b, h) + ((boff ^ (k * 64)) + n * 2048)); } while (0)
;     ...
;         for (int t = 0; t < nt; t += 2) {
;             const bool last = (t == nt - 2);
;             const char* a1 = cA + (size_t)(t + 1) * kstepA;
;             const char* a2 = last ? nA : cA + (size_t)(t + 2) * kstepA; const char* b2 = last ? nB : cB + (size_t)(t + 2) * kstepB;
;             const char* a3 = a2 + kstepA; const char* b3 = b2 + kstepB;
;             unsigned vs[2][2];
;             if constexpr (GATHER) {
;                 if (last && has_next) {
; #pragma unroll
;                     for (int hh = 0; hh < 2; ++hh)
; #pragma unroll
;                         for (int i = 0; i < 2; ++i) voffN[hh][i] = (unsigned)idxl[(ui + 1) * 256 + hh * HALF + sR[i]] * (unsigned)(K * 2) + (unsigned)sC[i] * 2u;
;                 }
; #pragma unroll
;                 for (int hh = 0; hh < 2; ++hh)
; #pragma unroll
;                     for (int i = 0; i < 2; ++i) vs[hh][i] = last ? voffN[hh][i] : voffA[hh][i];
;             } else {
; #pragma unroll
;                 for (int hh = 0; hh < 2; ++hh)
; #pragma unroll
;                     for (int i = 0; i < 2; ++i) vs[hh][i] = voffA[hh][i];
;             }
;             PG8_LDB(B0, 0, 0); PG8_LDB(B1, 0, 1); PG8_SCHED; PG8_LDA(At, 0, 0); PG8_STAGE(PG8_SA(1, 1), a1, voffA[1]);
;             PG8_WAIT_V(8); PG8_WAIT_L(0); PG8_BAR; if (do0) { PG8_MMA(0, 0, At, B0); PG8_MMA(0, 1, At, B1); } PG8_BAR; PG8_SCHED;
;             PG8_LDA(At, 0, 1); PG8_STAGE(PG8_SB(0, 0), b2, voffB); PG8_STAGE(PG8_SB(0, 1), b2 + hstep, voffB); PG8_STAGE(PG8_SA(0, 0), a2, vs[0]);
;             PG8_WAIT_V(8); PG8_WAIT_L(0); PG8_BAR; if (do1) { PG8_MMA(1, 0, At, B0); PG8_MMA(1, 1, At, B1); } PG8_BAR; PG8_SCHED;
.LBB0_1099:
	s_add_i32 s59, s59, 2
	s_waitcnt vmcnt(8)
	s_barrier
	s_add_u32 s22, s22, 0x8000
	s_addc_u32 s23, s23, 0
	s_add_u32 s62, s62, 0x8000
	s_addc_u32 s63, s63, 0
	s_cmp_ge_u32 s59, s60
	s_cbranch_scc1 .LBB0_1108
.LBB0_1100:
	ds_read_b128 v[150:153], v218
	ds_read_b128 v[154:157], v219
	ds_read_b128 v[158:161], v220
	ds_read_b128 v[162:165], v221
	ds_read_b128 v[134:137], v222
	ds_read_b128 v[138:141], v223
	ds_read_b128 v[142:145], v224
	ds_read_b128 v[146:149], v225
	v_lshl_add_u64 v[4:5], s[22:23], 0, v[212:213]
	s_add_i32 m0, s28, 0xc000
	s_waitcnt lgkmcnt(0)
	ds_read_b128 v[190:193], v226
	ds_read_b128 v[178:181], v226 offset:2048
	ds_read_b128 v[194:197], v227
	ds_read_b128 v[182:185], v227 offset:2048
	ds_read_b128 v[174:177], v226 offset:4096
	ds_read_b128 v[166:169], v226 offset:6144
	ds_read_b128 v[186:189], v227 offset:4096
	ds_read_b128 v[170:173], v227 offset:6144
	global_load_lds_dwordx4 v[4:5], off
	v_lshl_add_u64 v[4:5], s[22:23], 0, v[214:215]
	s_add_i32 m0, s28, 0xe000
	v_cmp_ne_u32_e64 s[6:7], 1, v228
	global_load_lds_dwordx4 v[4:5], off
	s_bitcmp1_b32 s2, 0
	s_cbranch_scc0 .Lwm_dnL0_0
	s_waitcnt vmcnt(8)
.Lwm_dnL0_0:
	s_waitcnt lgkmcnt(0)
	s_andn2_b64 vcc, exec, s[20:21]
	s_barrier
	s_cbranch_vccnz .LBB0_1102
	s_setprio 1
	s_waitcnt lgkmcnt(0)
	v_mfma_f32_16x16x32_bf16 v[66:69], v[150:153], v[190:193], v[66:69]
	v_mfma_f32_16x16x32_bf16 v[62:65], v[158:161], v[190:193], v[62:65]
	v_mfma_f32_16x16x32_bf16 v[50:53], v[150:153], v[178:181], v[50:53]
	v_mfma_f32_16x16x32_bf16 v[46:49], v[158:161], v[178:181], v[46:49]
	v_mfma_f32_16x16x32_bf16 v[34:37], v[150:153], v[174:177], v[34:37]
	v_mfma_f32_16x16x32_bf16 v[30:33], v[158:161], v[174:177], v[30:33]
	v_mfma_f32_16x16x32_bf16 v[18:21], v[150:153], v[166:169], v[18:21]
	v_mfma_f32_16x16x32_bf16 v[14:17], v[158:161], v[166:169], v[14:17]
	v_mfma_f32_16x16x32_bf16 v[66:69], v[154:157], v[194:197], v[66:69]
	v_mfma_f32_16x16x32_bf16 v[62:65], v[162:165], v[194:197], v[62:65]
	v_mfma_f32_16x16x32_bf16 v[50:53], v[154:157], v[182:185], v[50:53]
	v_mfma_f32_16x16x32_bf16 v[46:49], v[162:165], v[182:185], v[46:49]
	v_mfma_f32_16x16x32_bf16 v[34:37], v[154:157], v[186:189], v[34:37]
	v_mfma_f32_16x16x32_bf16 v[30:33], v[162:165], v[186:189], v[30:33]
	v_mfma_f32_16x16x32_bf16 v[18:21], v[154:157], v[170:173], v[18:21]
	v_mfma_f32_16x16x32_bf16 v[14:17], v[162:165], v[170:173], v[14:17]
	s_setprio 0
	s_setprio 1
	v_mfma_f32_16x16x32_bf16 v[58:61], v[134:137], v[190:193], v[58:61]
	v_mfma_f32_16x16x32_bf16 v[54:57], v[142:145], v[190:193], v[54:57]
	v_mfma_f32_16x16x32_bf16 v[42:45], v[134:137], v[178:181], v[42:45]
	v_mfma_f32_16x16x32_bf16 v[38:41], v[142:145], v[178:181], v[38:41]
	v_mfma_f32_16x16x32_bf16 v[26:29], v[134:137], v[174:177], v[26:29]
	v_mfma_f32_16x16x32_bf16 v[22:25], v[142:145], v[174:177], v[22:25]
	v_mfma_f32_16x16x32_bf16 v[10:13], v[134:137], v[166:169], v[10:13]
	v_mfma_f32_16x16x32_bf16 v[4:7], v[142:145], v[166:169], v[6:9]
	v_mfma_f32_16x16x32_bf16 v[58:61], v[138:141], v[194:197], v[58:61]
	v_mfma_f32_16x16x32_bf16 v[54:57], v[146:149], v[194:197], v[54:57]
	v_mfma_f32_16x16x32_bf16 v[42:45], v[138:141], v[182:185], v[42:45]
	v_mfma_f32_16x16x32_bf16 v[38:41], v[146:149], v[182:185], v[38:41]
	v_mfma_f32_16x16x32_bf16 v[26:29], v[138:141], v[186:189], v[26:29]
	v_mfma_f32_16x16x32_bf16 v[22:25], v[146:149], v[186:189], v[22:25]
	v_mfma_f32_16x16x32_bf16 v[10:13], v[138:141], v[170:173], v[10:13]
	v_mfma_f32_16x16x32_bf16 v[6:9], v[146:149], v[170:173], v[4:7]
	s_setprio 0
.LBB0_1102:
	s_add_u32 s8, s22, 0x4000
	s_addc_u32 s9, s23, 0
	s_cmp_eq_u32 s61, s59
	s_cselect_b32 s27, s15, s9
	s_cselect_b32 s26, s14, s8
	s_cselect_b32 s25, s17, s63
	s_cselect_b32 s24, s16, s62
	s_waitcnt vmcnt(8)
	s_barrier
	s_mov_b32 m0, s29
	v_lshl_add_u64 v[4:5], s[24:25], 0, v[208:209]
	s_add_u32 s8, s24, 0xb0000
	s_waitcnt lgkmcnt(0)
	ds_read_b128 v[190:193], v226 offset:16384
	ds_read_b128 v[178:181], v226 offset:18432
	ds_read_b128 v[194:197], v227 offset:16384
	ds_read_b128 v[182:185], v227 offset:18432
	ds_read_b128 v[174:177], v226 offset:20480
	ds_read_b128 v[166:169], v226 offset:22528
	ds_read_b128 v[186:189], v227 offset:20480
	ds_read_b128 v[170:173], v227 offset:22528
	global_load_lds_dwordx4 v[4:5], off
	v_lshl_add_u64 v[4:5], s[24:25], 0, v[210:211]
	s_mov_b32 m0, s30
	s_addc_u32 s9, s25, 0
	global_load_lds_dwordx4 v[4:5], off
	v_lshl_add_u64 v[4:5], s[8:9], 0, v[208:209]
	s_mov_b32 m0, s31
	v_cndmask_b32_e64 v3, 0, 1, s[18:19]
	global_load_lds_dwordx4 v[4:5], off
	v_lshl_add_u64 v[4:5], s[8:9], 0, v[210:211]
	s_mov_b32 m0, s34
	v_cmp_ne_u32_e64 s[8:9], 1, v3
	global_load_lds_dwordx4 v[4:5], off
	v_lshl_add_u64 v[4:5], s[26:27], 0, v[200:201]
	s_mov_b32 m0, s28
	s_andn2_b64 vcc, exec, s[18:19]
	global_load_lds_dwordx4 v[4:5], off
	v_lshl_add_u64 v[4:5], s[26:27], 0, v[202:203]
	s_mov_b32 m0, s35
	s_nop 0
	global_load_lds_dwordx4 v[4:5], off
	s_bitcmp1_b32 s2, 0
	s_cbranch_scc0 .Lwm_dnL0_1
	s_waitcnt vmcnt(8)

; #define PG8_STAGE(bufoff, gbase, voff) do { _Pragma("unroll") for (int _i = 0; _i < 2; ++_i) \
;         __builtin_amdgcn_global_load_lds((const unsigned*)((const char*)(gbase) + (voff)[_i]), (LAS unsigned*)(lds + (bufoff) + ldsw + _i * 8192), 16, 0, 0); } while (0)
; #define PG8_LDA(dst, b, h) do { _Pragma("unroll") for (int m = 0; m < 4; ++m) _Pragma("unroll") for (int k = 0; k < 2; ++k) dst[m][k] = *(const LAS bf16x8*)(lds + PG8_SA(b, h) + ((aoff ^ (k * 64)) + m * 2048)); } while (0)
; #define PG8_LDB(dst, b, h) do { _Pragma("unroll") for (int n = 0; n < 2; ++n) _Pragma("unroll") for (int k = 0; k < 2; ++k) dst[n][k] = *(const LAS bf16x8*)(lds + PG8_SB(b, h) + ((boff ^ (k * 64)) + n * 2048)); } while (0)
; #define PG8_MMA(ai, bj, At, Bt) do { __builtin_amdgcn_s_setprio(1); _Pragma("unroll") for (int m = 0; m < 4; ++m) _Pragma("unroll") for (int n = 0; n < 2; ++n) _Pragma("unroll") for (int k = 0; k < 2; ++k) \
;         acc[ai][bj][m][n] = __builtin_amdgcn_mfma_f32_16x16x32_bf16(Bt[n][k], At[m][k], acc[ai][bj][m][n], 0, 0, 0); __builtin_amdgcn_s_setprio(0); } while (0)
; #define PG8_WAIT_V(n) asm volatile("s_waitcnt vmcnt(" #n ")" ::: "memory")
; #define PG8_WAIT_L(n) asm volatile("s_waitcnt lgkmcnt(" #n ")" ::: "memory")
; #define PG8_BAR __builtin_amdgcn_s_barrier()
; #define PG8_SCHED __builtin_amdgcn_sched_barrier(0)
;     ...
;             PG8_LDB(B0, 1, 0); PG8_LDB(B1, 1, 1); PG8_SCHED; PG8_LDA(At, 1, 0); PG8_STAGE(PG8_SA(0, 1), a2, vs[1]);
;             PG8_WAIT_V(8); PG8_WAIT_L(0); PG8_BAR; if (do0) { PG8_MMA(0, 0, At, B0); PG8_MMA(0, 1, At, B1); } PG8_BAR; PG8_SCHED;
.LBB0_1104:
	s_waitcnt vmcnt(8)
	s_barrier
	s_add_i32 s64, 0, 0x18000
	v_add_u32_e32 v3, s64, v199
	v_add_u32_e32 v4, s64, v216
	ds_read_b128 v[150:153], v3
	ds_read_b128 v[154:157], v4
	v_add_u32_e32 v3, s48, v199
	s_add_i32 s64, 0, 0x1c000
	v_add_u32_e32 v4, s48, v216
	ds_read_b128 v[158:161], v3
	ds_read_b128 v[162:165], v4
	v_add_u32_e32 v3, s64, v199
	v_add_u32_e32 v4, s64, v216
	ds_read_b128 v[134:137], v3
	ds_read_b128 v[138:141], v4
	v_add_u32_e32 v3, s49, v199
	v_add_u32_e32 v4, s49, v216
	ds_read_b128 v[142:145], v3
	ds_read_b128 v[146:149], v4
	s_mov_b32 m0, s36
	v_lshl_add_u64 v[4:5], s[26:27], 0, v[204:205]
	s_waitcnt lgkmcnt(0)
	ds_read_b128 v[190:193], v226 offset:32768
	ds_read_b128 v[178:181], v226 offset:34816
	ds_read_b128 v[194:197], v227 offset:32768
	ds_read_b128 v[182:185], v227 offset:34816
	ds_read_b128 v[174:177], v226 offset:36864
	ds_read_b128 v[166:169], v226 offset:38912
	ds_read_b128 v[186:189], v227 offset:36864
	ds_read_b128 v[170:173], v227 offset:38912
	global_load_lds_dwordx4 v[4:5], off
	v_lshl_add_u64 v[4:5], s[26:27], 0, v[206:207]
	s_mov_b32 m0, s37
	s_and_b64 vcc, exec, s[6:7]
	global_load_lds_dwordx4 v[4:5], off
	s_bitcmp1_b32 s2, 0
	s_cbranch_scc0 .Lwm_dnL0_2
	s_waitcnt vmcnt(8)
.Lwm_dnL0_2:
	s_waitcnt lgkmcnt(0)
	s_barrier
	s_cbranch_vccnz .LBB0_1106
	s_setprio 1
	s_waitcnt lgkmcnt(0)
	v_mfma_f32_16x16x32_bf16 v[66:69], v[150:153], v[190:193], v[66:69]
	v_mfma_f32_16x16x32_bf16 v[62:65], v[158:161], v[190:193], v[62:65]
	v_mfma_f32_16x16x32_bf16 v[50:53], v[150:153], v[178:181], v[50:53]
	v_mfma_f32_16x16x32_bf16 v[46:49], v[158:161], v[178:181], v[46:49]
	v_mfma_f32_16x16x32_bf16 v[34:37], v[150:153], v[174:177], v[34:37]
	v_mfma_f32_16x16x32_bf16 v[30:33], v[158:161], v[174:177], v[30:33]
	v_mfma_f32_16x16x32_bf16 v[18:21], v[150:153], v[166:169], v[18:21]
	v_mfma_f32_16x16x32_bf16 v[14:17], v[158:161], v[166:169], v[14:17]
	v_mfma_f32_16x16x32_bf16 v[66:69], v[154:157], v[194:197], v[66:69]
	v_mfma_f32_16x16x32_bf16 v[62:65], v[162:165], v[194:197], v[62:65]
	v_mfma_f32_16x16x32_bf16 v[50:53], v[154:157], v[182:185], v[50:53]
	v_mfma_f32_16x16x32_bf16 v[46:49], v[162:165], v[182:185], v[46:49]
	v_mfma_f32_16x16x32_bf16 v[34:37], v[154:157], v[186:189], v[34:37]
	v_mfma_f32_16x16x32_bf16 v[30:33], v[162:165], v[186:189], v[30:33]
	v_mfma_f32_16x16x32_bf16 v[18:21], v[154:157], v[170:173], v[18:21]
	v_mfma_f32_16x16x32_bf16 v[14:17], v[162:165], v[170:173], v[14:17]
	s_setprio 0
	s_setprio 1
	v_mfma_f32_16x16x32_bf16 v[58:61], v[134:137], v[190:193], v[58:61]
	v_mfma_f32_16x16x32_bf16 v[54:57], v[142:145], v[190:193], v[54:57]
	v_mfma_f32_16x16x32_bf16 v[42:45], v[134:137], v[178:181], v[42:45]
	v_mfma_f32_16x16x32_bf16 v[38:41], v[142:145], v[178:181], v[38:41]
	v_mfma_f32_16x16x32_bf16 v[26:29], v[134:137], v[174:177], v[26:29]
	v_mfma_f32_16x16x32_bf16 v[22:25], v[142:145], v[174:177], v[22:25]
	v_mfma_f32_16x16x32_bf16 v[10:13], v[134:137], v[166:169], v[10:13]
	v_mfma_f32_16x16x32_bf16 v[4:7], v[142:145], v[166:169], v[6:9]
	v_mfma_f32_16x16x32_bf16 v[58:61], v[138:141], v[194:197], v[58:61]
	v_mfma_f32_16x16x32_bf16 v[54:57], v[146:149], v[194:197], v[54:57]
	v_mfma_f32_16x16x32_bf16 v[42:45], v[138:141], v[182:185], v[42:45]
	v_mfma_f32_16x16x32_bf16 v[38:41], v[146:149], v[182:185], v[38:41]
	v_mfma_f32_16x16x32_bf16 v[26:29], v[138:141], v[186:189], v[26:29]
	v_mfma_f32_16x16x32_bf16 v[22:25], v[146:149], v[186:189], v[22:25]
	v_mfma_f32_16x16x32_bf16 v[10:13], v[138:141], v[170:173], v[10:13]
	v_mfma_f32_16x16x32_bf16 v[6:9], v[146:149], v[170:173], v[4:7]
	s_setprio 0
; #define PG8_STAGE(bufoff, gbase, voff) do { _Pragma("unroll") for (int _i = 0; _i < 2; ++_i) \
;         __builtin_amdgcn_global_load_lds((const unsigned*)((const char*)(gbase) + (voff)[_i]), (LAS unsigned*)(lds + (bufoff) + ldsw + _i * 8192), 16, 0, 0); } while (0)
; #define PG8_LDA(dst, b, h) do { _Pragma("unroll") for (int m = 0; m < 4; ++m) _Pragma("unroll") for (int k = 0; k < 2; ++k) dst[m][k] = *(const LAS bf16x8*)(lds + PG8_SA(b, h) + ((aoff ^ (k * 64)) + m * 2048)); } while (0)
; #define PG8_MMA(ai, bj, At, Bt) do { __builtin_amdgcn_s_setprio(1); _Pragma("unroll") for (int m = 0; m < 4; ++m) _Pragma("unroll") for (int n = 0; n < 2; ++n) _Pragma("unroll") for (int k = 0; k < 2; ++k) \
;         acc[ai][bj][m][n] = __builtin_amdgcn_mfma_f32_16x16x32_bf16(Bt[n][k], At[m][k], acc[ai][bj][m][n], 0, 0, 0); __builtin_amdgcn_s_setprio(0); } while (0)
; #define PG8_WAIT_V(n) asm volatile("s_waitcnt vmcnt(" #n ")" ::: "memory")
; #define PG8_WAIT_L(n) asm volatile("s_waitcnt lgkmcnt(" #n ")" ::: "memory")
; #define PG8_BAR __builtin_amdgcn_s_barrier()
; #define PG8_SCHED __builtin_amdgcn_sched_barrier(0)
;     ...
;             PG8_LDA(At, 1, 1); PG8_STAGE(PG8_SB(1, 0), b3, voffB); PG8_STAGE(PG8_SB(1, 1), b3 + hstep, voffB); PG8_STAGE(PG8_SA(1, 0), a3, vs[0]);
;             PG8_WAIT_V(8); PG8_WAIT_L(0); PG8_BAR; if (do1) { PG8_MMA(1, 0, At, B0); PG8_MMA(1, 1, At, B1); } PG8_BAR; PG8_SCHED;
.LBB0_1106:
	s_add_u32 s6, s26, 0x4000
	s_addc_u32 s7, s27, 0
	s_add_u32 s26, s24, 0x4000
	s_addc_u32 s27, s25, 0
	s_waitcnt vmcnt(8)
	s_barrier
	s_mov_b32 m0, s39
	v_lshl_add_u64 v[4:5], s[26:27], 0, v[208:209]
	s_add_u32 s24, s24, 0xb4000
	s_waitcnt lgkmcnt(0)
	ds_read_b128 v[190:193], v226 offset:49152
	ds_read_b128 v[178:181], v226 offset:51200
	ds_read_b128 v[194:197], v227 offset:49152
	ds_read_b128 v[182:185], v227 offset:51200
	ds_read_b128 v[174:177], v226 offset:53248
	ds_read_b128 v[166:169], v226 offset:55296
	ds_read_b128 v[186:189], v227 offset:53248
	ds_read_b128 v[170:173], v227 offset:55296
	global_load_lds_dwordx4 v[4:5], off
	v_lshl_add_u64 v[4:5], s[26:27], 0, v[210:211]
	s_mov_b32 m0, s40
	s_addc_u32 s25, s25, 0
	global_load_lds_dwordx4 v[4:5], off
	v_lshl_add_u64 v[4:5], s[24:25], 0, v[208:209]
	s_mov_b32 m0, s43
	s_and_b64 vcc, exec, s[8:9]
	global_load_lds_dwordx4 v[4:5], off
	v_lshl_add_u64 v[4:5], s[24:25], 0, v[210:211]
	s_mov_b32 m0, s44
	s_nop 0
	global_load_lds_dwordx4 v[4:5], off
	v_lshl_add_u64 v[4:5], s[6:7], 0, v[200:201]
	s_mov_b32 m0, s41
	s_nop 0
	global_load_lds_dwordx4 v[4:5], off
	v_lshl_add_u64 v[4:5], s[6:7], 0, v[202:203]
	s_mov_b32 m0, s42
	s_nop 0
	global_load_lds_dwordx4 v[4:5], off
	s_bitcmp1_b32 s2, 0
	s_cbranch_scc0 .Lwm_dnL0_3
	s_waitcnt vmcnt(8)
.Lwm_dnL0_3:
	s_waitcnt lgkmcnt(0)
	s_barrier
	s_cbranch_vccnz .LBB0_1099
	s_setprio 1
	s_waitcnt lgkmcnt(0)
	v_mfma_f32_16x16x32_bf16 v[130:133], v[150:153], v[190:193], v[130:133]
	v_mfma_f32_16x16x32_bf16 v[126:129], v[158:161], v[190:193], v[126:129]
	v_mfma_f32_16x16x32_bf16 v[114:117], v[150:153], v[178:181], v[114:117]
	v_mfma_f32_16x16x32_bf16 v[110:113], v[158:161], v[178:181], v[110:113]
	v_mfma_f32_16x16x32_bf16 v[98:101], v[150:153], v[174:177], v[98:101]
	v_mfma_f32_16x16x32_bf16 v[94:97], v[158:161], v[174:177], v[94:97]
	v_mfma_f32_16x16x32_bf16 v[82:85], v[150:153], v[166:169], v[82:85]
	v_mfma_f32_16x16x32_bf16 v[78:81], v[158:161], v[166:169], v[78:81]
	v_mfma_f32_16x16x32_bf16 v[130:133], v[154:157], v[194:197], v[130:133]
	v_mfma_f32_16x16x32_bf16 v[126:129], v[162:165], v[194:197], v[126:129]
	v_mfma_f32_16x16x32_bf16 v[114:117], v[154:157], v[182:185], v[114:117]
	v_mfma_f32_16x16x32_bf16 v[110:113], v[162:165], v[182:185], v[110:113]
	v_mfma_f32_16x16x32_bf16 v[98:101], v[154:157], v[186:189], v[98:101]
	v_mfma_f32_16x16x32_bf16 v[94:97], v[162:165], v[186:189], v[94:97]
	v_mfma_f32_16x16x32_bf16 v[82:85], v[154:157], v[170:173], v[82:85]
	v_mfma_f32_16x16x32_bf16 v[78:81], v[162:165], v[170:173], v[78:81]
	s_setprio 0
	s_setprio 1
	v_mfma_f32_16x16x32_bf16 v[122:125], v[134:137], v[190:193], v[122:125]
	v_mfma_f32_16x16x32_bf16 v[118:121], v[142:145], v[190:193], v[118:121]
	v_mfma_f32_16x16x32_bf16 v[106:109], v[134:137], v[178:181], v[106:109]
	v_mfma_f32_16x16x32_bf16 v[102:105], v[142:145], v[178:181], v[102:105]
	v_mfma_f32_16x16x32_bf16 v[90:93], v[134:137], v[174:177], v[90:93]
	v_mfma_f32_16x16x32_bf16 v[86:89], v[142:145], v[174:177], v[86:89]
	v_mfma_f32_16x16x32_bf16 v[74:77], v[134:137], v[166:169], v[74:77]
	v_mfma_f32_16x16x32_bf16 v[70:73], v[142:145], v[166:169], v[70:73]
	v_mfma_f32_16x16x32_bf16 v[122:125], v[138:141], v[194:197], v[122:125]
	v_mfma_f32_16x16x32_bf16 v[118:121], v[146:149], v[194:197], v[118:121]
	v_mfma_f32_16x16x32_bf16 v[106:109], v[138:141], v[182:185], v[106:109]
	v_mfma_f32_16x16x32_bf16 v[102:105], v[146:149], v[182:185], v[102:105]
	v_mfma_f32_16x16x32_bf16 v[90:93], v[138:141], v[186:189], v[90:93]
	v_mfma_f32_16x16x32_bf16 v[86:89], v[146:149], v[186:189], v[86:89]
	v_mfma_f32_16x16x32_bf16 v[74:77], v[138:141], v[170:173], v[74:77]
	v_mfma_f32_16x16x32_bf16 v[70:73], v[146:149], v[170:173], v[70:73]
	s_setprio 0
	s_branch .LBB0_1099

; #define PG8_STAGE(bufoff, gbase, voff) do { _Pragma("unroll") for (int _i = 0; _i < 2; ++_i) \
;         __builtin_amdgcn_global_load_lds((const unsigned*)((const char*)(gbase) + (voff)[_i]), (LAS unsigned*)(lds + (bufoff) + ldsw + _i * 8192), 16, 0, 0); } while (0)
; #define PG8_LDA(dst, b, h) do { _Pragma("unroll") for (int m = 0; m < 4; ++m) _Pragma("unroll") for (int k = 0; k < 2; ++k) dst[m][k] = *(const LAS bf16x8*)(lds + PG8_SA(b, h) + ((aoff ^ (k * 64)) + m * 2048)); } while (0)
; #define PG8_LDB(dst, b, h) do { _Pragma("unroll") for (int n = 0; n < 2; ++n) _Pragma("unroll") for (int k = 0; k < 2; ++k) dst[n][k] = *(const LAS bf16x8*)(lds + PG8_SB(b, h) + ((boff ^ (k * 64)) + n * 2048)); } while (0)
;     ...
;         for (int t = 0; t < nt; t += 2) {
;             const bool last = (t == nt - 2);
;             const char* a1 = cA + (size_t)(t + 1) * kstepA;
;             const char* a2 = last ? nA : cA + (size_t)(t + 2) * kstepA; const char* b2 = last ? nB : cB + (size_t)(t + 2) * kstepB;
;             const char* a3 = a2 + kstepA; const char* b3 = b2 + kstepB;
;             unsigned vs[2][2];
;             if constexpr (GATHER) {
;                 if (last && has_next) {
; #pragma unroll
;                     for (int hh = 0; hh < 2; ++hh)
; #pragma unroll
;                         for (int i = 0; i < 2; ++i) voffN[hh][i] = (unsigned)idxl[(ui + 1) * 256 + hh * HALF + sR[i]] * (unsigned)(K * 2) + (unsigned)sC[i] * 2u;
;                 }
; #pragma unroll
;                 for (int hh = 0; hh < 2; ++hh)
; #pragma unroll
;                     for (int i = 0; i < 2; ++i) vs[hh][i] = last ? voffN[hh][i] : voffA[hh][i];
;             } else {
; #pragma unroll
;                 for (int hh = 0; hh < 2; ++hh)
; #pragma unroll
;                     for (int i = 0; i < 2; ++i) vs[hh][i] = voffA[hh][i];
;             }
;             PG8_LDB(B0, 0, 0); PG8_LDB(B1, 0, 1); PG8_SCHED; PG8_LDA(At, 0, 0); PG8_STAGE(PG8_SA(1, 1), a1, voffA[1]);
;             PG8_WAIT_V(8); PG8_WAIT_L(0); PG8_BAR; if (do0) { PG8_MMA(0, 0, At, B0); PG8_MMA(0, 1, At, B1); } PG8_BAR; PG8_SCHED;
;             PG8_LDA(At, 0, 1); PG8_STAGE(PG8_SB(0, 0), b2, voffB); PG8_STAGE(PG8_SB(0, 1), b2 + hstep, voffB); PG8_STAGE(PG8_SA(0, 0), a2, vs[0]);
;             PG8_WAIT_V(8); PG8_WAIT_L(0); PG8_BAR; if (do1) { PG8_MMA(1, 0, At, B0); PG8_MMA(1, 1, At, B1); } PG8_BAR; PG8_SCHED;
.LBB0_1257:
	ds_read_b128 v[156:159], v176
	ds_read_b128 v[160:163], v177
	ds_read_b128 v[164:167], v178
	ds_read_b128 v[192:195], v179
	ds_read_b128 v[200:203], v180
	ds_read_b128 v[204:207], v181
	ds_read_b128 v[208:211], v182
	ds_read_b128 v[212:215], v183
	s_add_u32 s40, s38, 0x80
	s_addc_u32 s41, s39, 0
	s_cmp_eq_u32 s63, 12
	s_cselect_b32 s45, s3, s41
	s_cselect_b32 s44, s11, s40
	s_cselect_b32 s41, s12, s62
	s_cselect_b32 s40, s29, s31
	v_lshl_add_u64 v[168:169], s[38:39], 0, v[150:151]
	s_add_i32 m0, s47, 0xc000
	ds_read_b128 v[216:219], v184
	ds_read_b128 v[220:223], v184 offset:2048
	ds_read_b128 v[224:227], v185
	ds_read_b128 v[228:231], v185 offset:2048
	ds_read_b128 v[232:235], v184 offset:4096
	ds_read_b128 v[236:239], v184 offset:6144
	ds_read_b128 v[240:243], v185 offset:4096
	ds_read_b128 v[244:247], v185 offset:6144
	global_load_lds_dwordx4 v[168:169], off
	v_lshl_add_u64 v[168:169], s[38:39], 0, v[148:149]
	s_add_i32 m0, s47, 0xe000
	s_add_u32 s42, s40, 0x4000
	global_load_lds_dwordx4 v[168:169], off
	s_mov_b64 vcc, s[18:19]
	s_cbranch_vccz .Lwm_in1n_0
	s_waitcnt vmcnt(8)
.Lwm_in1n_0:
	s_waitcnt lgkmcnt(0)
	s_addc_u32 s43, s41, 0
	s_barrier
	s_setprio 1
	s_waitcnt lgkmcnt(0)
	v_mfma_f32_16x16x32_bf16 v[126:129], v[156:159], v[216:219], v[126:129]
	v_mfma_f32_16x16x32_bf16 v[118:121], v[164:167], v[216:219], v[118:121]
	v_mfma_f32_16x16x32_bf16 v[110:113], v[156:159], v[220:223], v[110:113]
	v_mfma_f32_16x16x32_bf16 v[102:105], v[164:167], v[220:223], v[102:105]
	v_mfma_f32_16x16x32_bf16 v[94:97], v[156:159], v[232:235], v[94:97]
	v_mfma_f32_16x16x32_bf16 v[86:89], v[164:167], v[232:235], v[86:89]
	v_mfma_f32_16x16x32_bf16 v[78:81], v[156:159], v[236:239], v[78:81]
	v_mfma_f32_16x16x32_bf16 v[70:73], v[164:167], v[236:239], v[70:73]
	v_mfma_f32_16x16x32_bf16 v[126:129], v[160:163], v[224:227], v[126:129]
	v_mfma_f32_16x16x32_bf16 v[118:121], v[192:195], v[224:227], v[118:121]
	v_mfma_f32_16x16x32_bf16 v[110:113], v[160:163], v[228:231], v[110:113]
	v_mfma_f32_16x16x32_bf16 v[102:105], v[192:195], v[228:231], v[102:105]
	v_mfma_f32_16x16x32_bf16 v[94:97], v[160:163], v[240:243], v[94:97]
	v_mfma_f32_16x16x32_bf16 v[86:89], v[192:195], v[240:243], v[86:89]
	v_mfma_f32_16x16x32_bf16 v[78:81], v[160:163], v[244:247], v[78:81]
	v_mfma_f32_16x16x32_bf16 v[70:73], v[192:195], v[244:247], v[70:73]
	s_setprio 0
	s_setprio 1
	v_mfma_f32_16x16x32_bf16 v[122:125], v[200:203], v[216:219], v[122:125]
	v_mfma_f32_16x16x32_bf16 v[114:117], v[208:211], v[216:219], v[114:117]
	v_mfma_f32_16x16x32_bf16 v[106:109], v[200:203], v[220:223], v[106:109]
	v_mfma_f32_16x16x32_bf16 v[98:101], v[208:211], v[220:223], v[98:101]
	v_mfma_f32_16x16x32_bf16 v[90:93], v[200:203], v[232:235], v[90:93]
	v_mfma_f32_16x16x32_bf16 v[82:85], v[208:211], v[232:235], v[82:85]
	v_mfma_f32_16x16x32_bf16 v[74:77], v[200:203], v[236:239], v[74:77]
	v_mfma_f32_16x16x32_bf16 v[66:69], v[208:211], v[236:239], v[66:69]
	v_mfma_f32_16x16x32_bf16 v[122:125], v[204:207], v[224:227], v[122:125]
	v_mfma_f32_16x16x32_bf16 v[114:117], v[212:215], v[224:227], v[114:117]
	v_mfma_f32_16x16x32_bf16 v[106:109], v[204:207], v[228:231], v[106:109]
	v_mfma_f32_16x16x32_bf16 v[98:101], v[212:215], v[228:231], v[98:101]
	v_mfma_f32_16x16x32_bf16 v[90:93], v[204:207], v[240:243], v[90:93]
	v_mfma_f32_16x16x32_bf16 v[82:85], v[212:215], v[240:243], v[82:85]
	v_mfma_f32_16x16x32_bf16 v[74:77], v[204:207], v[244:247], v[74:77]
	v_mfma_f32_16x16x32_bf16 v[66:69], v[212:215], v[244:247], v[66:69]
	s_setprio 0
	s_waitcnt vmcnt(8)
	s_barrier
	s_add_i32 s64, s56, s46
	v_lshl_add_u64 v[168:169], s[40:41], 0, v[130:131]
	s_mov_b32 m0, s64
	ds_read_b128 v[216:219], v184 offset:16384
	ds_read_b128 v[220:223], v184 offset:18432
	ds_read_b128 v[224:227], v185 offset:16384
	ds_read_b128 v[228:231], v185 offset:18432
	ds_read_b128 v[232:235], v184 offset:20480
	ds_read_b128 v[236:239], v184 offset:22528
	ds_read_b128 v[240:243], v185 offset:20480
	ds_read_b128 v[244:247], v185 offset:22528
	global_load_lds_dwordx4 v[168:169], off
	s_add_i32 m0, s64, 0x2000
	s_add_u32 s64, s40, 0x40000
	v_lshl_add_u64 v[168:169], s[40:41], 0, v[132:133]
	s_addc_u32 s65, s41, 0
	s_add_i32 s66, s57, s46
	global_load_lds_dwordx4 v[168:169], off
	v_lshl_add_u64 v[168:169], s[64:65], 0, v[130:131]
	s_mov_b32 m0, s66
	v_lshl_add_u64 v[196:197], s[44:45], 0, v[136:137]
	global_load_lds_dwordx4 v[168:169], off
	v_lshl_add_u64 v[168:169], s[64:65], 0, v[132:133]
	s_add_i32 m0, s66, 0x2000
	s_nop 0
	global_load_lds_dwordx4 v[168:169], off
	v_lshl_add_u64 v[168:169], s[44:45], 0, v[134:135]
	s_mov_b32 m0, s47
	s_nop 0
	global_load_lds_dwordx4 v[168:169], off
	s_mov_b32 m0, s48
	s_nop 0
	global_load_lds_dwordx4 v[196:197], off
	s_bitcmp1_b32 s18, 0
	s_cbranch_scc0 .Lwm_in1n_1
	s_waitcnt vmcnt(8)
; #define PG8_STAGE(bufoff, gbase, voff) do { _Pragma("unroll") for (int _i = 0; _i < 2; ++_i) \
;         __builtin_amdgcn_global_load_lds((const unsigned*)((const char*)(gbase) + (voff)[_i]), (LAS unsigned*)(lds + (bufoff) + ldsw + _i * 8192), 16, 0, 0); } while (0)
; #define PG8_LDA(dst, b, h) do { _Pragma("unroll") for (int m = 0; m < 4; ++m) _Pragma("unroll") for (int k = 0; k < 2; ++k) dst[m][k] = *(const LAS bf16x8*)(lds + PG8_SA(b, h) + ((aoff ^ (k * 64)) + m * 2048)); } while (0)
; #define PG8_LDB(dst, b, h) do { _Pragma("unroll") for (int n = 0; n < 2; ++n) _Pragma("unroll") for (int k = 0; k < 2; ++k) dst[n][k] = *(const LAS bf16x8*)(lds + PG8_SB(b, h) + ((boff ^ (k * 64)) + n * 2048)); } while (0)
; #define PG8_MMA(ai, bj, At, Bt) do { __builtin_amdgcn_s_setprio(1); _Pragma("unroll") for (int m = 0; m < 4; ++m) _Pragma("unroll") for (int n = 0; n < 2; ++n) _Pragma("unroll") for (int k = 0; k < 2; ++k) \
;         acc[ai][bj][m][n] = __builtin_amdgcn_mfma_f32_16x16x32_bf16(Bt[n][k], At[m][k], acc[ai][bj][m][n], 0, 0, 0); __builtin_amdgcn_s_setprio(0); } while (0)
; #define PG8_WAIT_V(n) asm volatile("s_waitcnt vmcnt(" #n ")" ::: "memory")
; #define PG8_WAIT_L(n) asm volatile("s_waitcnt lgkmcnt(" #n ")" ::: "memory")
; #define PG8_BAR __builtin_amdgcn_s_barrier()
; #define PG8_SCHED __builtin_amdgcn_sched_barrier(0)
;     ...
;             PG8_WAIT_V(8); PG8_WAIT_L(0); PG8_BAR; if (do1) { PG8_MMA(1, 0, At, B0); PG8_MMA(1, 1, At, B1); } PG8_BAR; PG8_SCHED;
;             PG8_LDB(B0, 1, 0); PG8_LDB(B1, 1, 1); PG8_SCHED; PG8_LDA(At, 1, 0); PG8_STAGE(PG8_SA(0, 1), a2, vs[1]);
;             PG8_WAIT_V(8); PG8_WAIT_L(0); PG8_BAR; if (do0) { PG8_MMA(0, 0, At, B0); PG8_MMA(0, 1, At, B1); } PG8_BAR; PG8_SCHED;
.Lwm_in1n_1:
	s_waitcnt lgkmcnt(0)
	s_barrier
	s_setprio 1
	s_waitcnt lgkmcnt(0)
	v_mfma_f32_16x16x32_bf16 v[62:65], v[156:159], v[216:219], v[62:65]
	v_mfma_f32_16x16x32_bf16 v[54:57], v[164:167], v[216:219], v[54:57]
	v_mfma_f32_16x16x32_bf16 v[46:49], v[156:159], v[220:223], v[46:49]
	v_mfma_f32_16x16x32_bf16 v[38:41], v[164:167], v[220:223], v[38:41]
	v_mfma_f32_16x16x32_bf16 v[30:33], v[156:159], v[232:235], v[30:33]
	v_mfma_f32_16x16x32_bf16 v[22:25], v[164:167], v[232:235], v[22:25]
	v_mfma_f32_16x16x32_bf16 v[14:17], v[156:159], v[236:239], v[14:17]
	v_mfma_f32_16x16x32_bf16 v[6:9], v[164:167], v[236:239], v[6:9]
	v_mfma_f32_16x16x32_bf16 v[62:65], v[160:163], v[224:227], v[62:65]
	v_mfma_f32_16x16x32_bf16 v[54:57], v[192:195], v[224:227], v[54:57]
	v_mfma_f32_16x16x32_bf16 v[46:49], v[160:163], v[228:231], v[46:49]
	v_mfma_f32_16x16x32_bf16 v[38:41], v[192:195], v[228:231], v[38:41]
	v_mfma_f32_16x16x32_bf16 v[30:33], v[160:163], v[240:243], v[30:33]
	v_mfma_f32_16x16x32_bf16 v[22:25], v[192:195], v[240:243], v[22:25]
	v_mfma_f32_16x16x32_bf16 v[14:17], v[160:163], v[244:247], v[14:17]
	v_mfma_f32_16x16x32_bf16 v[6:9], v[192:195], v[244:247], v[6:9]
	s_setprio 0
	s_setprio 1
	v_mfma_f32_16x16x32_bf16 v[58:61], v[200:203], v[216:219], v[58:61]
	v_mfma_f32_16x16x32_bf16 v[50:53], v[208:211], v[216:219], v[50:53]
	v_mfma_f32_16x16x32_bf16 v[42:45], v[200:203], v[220:223], v[42:45]
	v_mfma_f32_16x16x32_bf16 v[34:37], v[208:211], v[220:223], v[34:37]
	v_mfma_f32_16x16x32_bf16 v[26:29], v[200:203], v[232:235], v[26:29]
	v_mfma_f32_16x16x32_bf16 v[18:21], v[208:211], v[232:235], v[18:21]
	v_mfma_f32_16x16x32_bf16 v[10:13], v[200:203], v[236:239], v[10:13]
	v_mfma_f32_16x16x32_bf16 v[2:5], v[208:211], v[236:239], v[2:5]
	v_mfma_f32_16x16x32_bf16 v[58:61], v[204:207], v[224:227], v[58:61]
	v_mfma_f32_16x16x32_bf16 v[50:53], v[212:215], v[224:227], v[50:53]
	v_mfma_f32_16x16x32_bf16 v[42:45], v[204:207], v[228:231], v[42:45]
	v_mfma_f32_16x16x32_bf16 v[34:37], v[212:215], v[228:231], v[34:37]
	v_mfma_f32_16x16x32_bf16 v[26:29], v[204:207], v[240:243], v[26:29]
	v_mfma_f32_16x16x32_bf16 v[18:21], v[212:215], v[240:243], v[18:21]
	v_mfma_f32_16x16x32_bf16 v[10:13], v[204:207], v[244:247], v[10:13]
	v_mfma_f32_16x16x32_bf16 v[2:5], v[212:215], v[244:247], v[2:5]
	s_setprio 0
	s_waitcnt vmcnt(8)
	s_barrier
	s_add_i32 s64, 0, 0x18000
	v_add_u32_e32 v142, s64, v170
	v_add_u32_e32 v160, s64, v174
	s_add_i32 s65, 0, 0x1c000
	ds_read_b128 v[156:159], v142
	ds_read_b128 v[160:163], v160
	ds_read_b128 v[164:167], v186
	ds_read_b128 v[192:195], v187
	v_add_u32_e32 v142, s65, v170
	v_add_u32_e32 v191, s65, v174
	ds_read_b128 v[200:203], v142
	ds_read_b128 v[204:207], v191
	ds_read_b128 v[208:211], v188
	ds_read_b128 v[212:215], v189
	s_mov_b32 m0, s49
	v_lshl_add_u64 v[248:249], s[44:45], 0, v[138:139]
	ds_read_b128 v[216:219], v184 offset:32768
	ds_read_b128 v[220:223], v184 offset:34816
	ds_read_b128 v[224:227], v185 offset:32768
	ds_read_b128 v[228:231], v185 offset:34816
	ds_read_b128 v[232:235], v184 offset:36864
	ds_read_b128 v[236:239], v184 offset:38912
	ds_read_b128 v[240:243], v185 offset:36864
	ds_read_b128 v[244:247], v185 offset:38912
	global_load_lds_dwordx4 v[248:249], off
	v_lshl_add_u64 v[248:249], s[44:45], 0, v[140:141]
	s_mov_b32 m0, s50
	s_nop 0
	global_load_lds_dwordx4 v[248:249], off
	s_bitcmp1_b32 s18, 0
	s_cbranch_scc0 .Lwm_in1n_2
	s_waitcnt vmcnt(8)
; #define PG8_STAGE(bufoff, gbase, voff) do { _Pragma("unroll") for (int _i = 0; _i < 2; ++_i) \
;         __builtin_amdgcn_global_load_lds((const unsigned*)((const char*)(gbase) + (voff)[_i]), (LAS unsigned*)(lds + (bufoff) + ldsw + _i * 8192), 16, 0, 0); } while (0)
; #define PG8_LDA(dst, b, h) do { _Pragma("unroll") for (int m = 0; m < 4; ++m) _Pragma("unroll") for (int k = 0; k < 2; ++k) dst[m][k] = *(const LAS bf16x8*)(lds + PG8_SA(b, h) + ((aoff ^ (k * 64)) + m * 2048)); } while (0)
; #define PG8_MMA(ai, bj, At, Bt) do { __builtin_amdgcn_s_setprio(1); _Pragma("unroll") for (int m = 0; m < 4; ++m) _Pragma("unroll") for (int n = 0; n < 2; ++n) _Pragma("unroll") for (int k = 0; k < 2; ++k) \
;         acc[ai][bj][m][n] = __builtin_amdgcn_mfma_f32_16x16x32_bf16(Bt[n][k], At[m][k], acc[ai][bj][m][n], 0, 0, 0); __builtin_amdgcn_s_setprio(0); } while (0)
; #define PG8_WAIT_V(n) asm volatile("s_waitcnt vmcnt(" #n ")" ::: "memory")
; #define PG8_WAIT_L(n) asm volatile("s_waitcnt lgkmcnt(" #n ")" ::: "memory")
; #define PG8_BAR __builtin_amdgcn_s_barrier()
; #define PG8_SCHED __builtin_amdgcn_sched_barrier(0)
;     ...
;             PG8_WAIT_V(8); PG8_WAIT_L(0); PG8_BAR; if (do0) { PG8_MMA(0, 0, At, B0); PG8_MMA(0, 1, At, B1); } PG8_BAR; PG8_SCHED;
;             PG8_LDA(At, 1, 1); PG8_STAGE(PG8_SB(1, 0), b3, voffB); PG8_STAGE(PG8_SB(1, 1), b3 + hstep, voffB); PG8_STAGE(PG8_SA(1, 0), a3, vs[0]);
;             PG8_WAIT_V(8); PG8_WAIT_L(0); PG8_BAR; if (do1) { PG8_MMA(1, 0, At, B0); PG8_MMA(1, 1, At, B1); } PG8_BAR; PG8_SCHED;
;         }
.Lwm_in1n_2:
	s_waitcnt lgkmcnt(0)
	s_barrier
	s_setprio 1
	s_waitcnt lgkmcnt(0)
	v_mfma_f32_16x16x32_bf16 v[126:129], v[156:159], v[216:219], v[126:129]
	v_mfma_f32_16x16x32_bf16 v[118:121], v[164:167], v[216:219], v[118:121]
	v_mfma_f32_16x16x32_bf16 v[110:113], v[156:159], v[220:223], v[110:113]
	v_mfma_f32_16x16x32_bf16 v[102:105], v[164:167], v[220:223], v[102:105]
	v_mfma_f32_16x16x32_bf16 v[94:97], v[156:159], v[232:235], v[94:97]
	v_mfma_f32_16x16x32_bf16 v[86:89], v[164:167], v[232:235], v[86:89]
	v_mfma_f32_16x16x32_bf16 v[78:81], v[156:159], v[236:239], v[78:81]
	v_mfma_f32_16x16x32_bf16 v[70:73], v[164:167], v[236:239], v[70:73]
	v_mfma_f32_16x16x32_bf16 v[126:129], v[160:163], v[224:227], v[126:129]
	v_mfma_f32_16x16x32_bf16 v[118:121], v[192:195], v[224:227], v[118:121]
	v_mfma_f32_16x16x32_bf16 v[110:113], v[160:163], v[228:231], v[110:113]
	v_mfma_f32_16x16x32_bf16 v[102:105], v[192:195], v[228:231], v[102:105]
	v_mfma_f32_16x16x32_bf16 v[94:97], v[160:163], v[240:243], v[94:97]
	v_mfma_f32_16x16x32_bf16 v[86:89], v[192:195], v[240:243], v[86:89]
	v_mfma_f32_16x16x32_bf16 v[78:81], v[160:163], v[244:247], v[78:81]
	v_mfma_f32_16x16x32_bf16 v[70:73], v[192:195], v[244:247], v[70:73]
	s_setprio 0
	s_setprio 1
	v_mfma_f32_16x16x32_bf16 v[122:125], v[200:203], v[216:219], v[122:125]
	v_mfma_f32_16x16x32_bf16 v[114:117], v[208:211], v[216:219], v[114:117]
	v_mfma_f32_16x16x32_bf16 v[106:109], v[200:203], v[220:223], v[106:109]
	v_mfma_f32_16x16x32_bf16 v[98:101], v[208:211], v[220:223], v[98:101]
	v_mfma_f32_16x16x32_bf16 v[90:93], v[200:203], v[232:235], v[90:93]
	v_mfma_f32_16x16x32_bf16 v[82:85], v[208:211], v[232:235], v[82:85]
	v_mfma_f32_16x16x32_bf16 v[74:77], v[200:203], v[236:239], v[74:77]
	v_mfma_f32_16x16x32_bf16 v[66:69], v[208:211], v[236:239], v[66:69]
	v_mfma_f32_16x16x32_bf16 v[122:125], v[204:207], v[224:227], v[122:125]
	v_mfma_f32_16x16x32_bf16 v[114:117], v[212:215], v[224:227], v[114:117]
	v_mfma_f32_16x16x32_bf16 v[106:109], v[204:207], v[228:231], v[106:109]
	v_mfma_f32_16x16x32_bf16 v[98:101], v[212:215], v[228:231], v[98:101]
	v_mfma_f32_16x16x32_bf16 v[90:93], v[204:207], v[240:243], v[90:93]
	v_mfma_f32_16x16x32_bf16 v[82:85], v[212:215], v[240:243], v[82:85]
	v_mfma_f32_16x16x32_bf16 v[74:77], v[204:207], v[244:247], v[74:77]
	v_mfma_f32_16x16x32_bf16 v[66:69], v[212:215], v[244:247], v[66:69]
	s_setprio 0
	s_waitcnt vmcnt(8)
	s_barrier
	s_add_i32 s44, s64, s46
	v_lshl_add_u64 v[248:249], s[42:43], 0, v[130:131]
	s_mov_b32 m0, s44
	ds_read_b128 v[216:219], v184 offset:49152
	ds_read_b128 v[220:223], v184 offset:51200
	ds_read_b128 v[224:227], v185 offset:49152
	ds_read_b128 v[228:231], v185 offset:51200
	ds_read_b128 v[232:235], v184 offset:53248
	ds_read_b128 v[236:239], v184 offset:55296
	ds_read_b128 v[240:243], v185 offset:53248
	ds_read_b128 v[244:247], v185 offset:55296
	global_load_lds_dwordx4 v[248:249], off
	s_add_i32 m0, s44, 0x2000
	s_add_u32 s40, s40, 0x44000
	v_lshl_add_u64 v[248:249], s[42:43], 0, v[132:133]
	s_addc_u32 s41, s41, 0
	s_add_i32 s42, s65, s46
	global_load_lds_dwordx4 v[248:249], off
	v_lshl_add_u64 v[248:249], s[40:41], 0, v[130:131]
	s_mov_b32 m0, s42
	v_lshl_add_u64 v[168:169], v[168:169], 0, s[20:21]
	global_load_lds_dwordx4 v[248:249], off
	v_lshl_add_u64 v[248:249], s[40:41], 0, v[132:133]
	s_add_i32 m0, s42, 0x2000
	s_nop 0
	global_load_lds_dwordx4 v[248:249], off
	s_mov_b32 m0, s52
	s_nop 0
	global_load_lds_dwordx4 v[168:169], off
	v_lshl_add_u64 v[168:169], v[196:197], 0, s[20:21]
	s_mov_b32 m0, s53
	s_nop 0
	global_load_lds_dwordx4 v[168:169], off
	s_bitcmp1_b32 s18, 0
	s_cbranch_scc0 .Lwm_in1n_3
	s_waitcnt vmcnt(8)
.Lwm_in1n_3:
	s_waitcnt lgkmcnt(0)
	s_barrier
	s_setprio 1
	s_waitcnt lgkmcnt(0)
	v_mfma_f32_16x16x32_bf16 v[62:65], v[156:159], v[216:219], v[62:65]
	v_mfma_f32_16x16x32_bf16 v[54:57], v[164:167], v[216:219], v[54:57]
	v_mfma_f32_16x16x32_bf16 v[46:49], v[156:159], v[220:223], v[46:49]
	v_mfma_f32_16x16x32_bf16 v[38:41], v[164:167], v[220:223], v[38:41]
	v_mfma_f32_16x16x32_bf16 v[30:33], v[156:159], v[232:235], v[30:33]
	v_mfma_f32_16x16x32_bf16 v[22:25], v[164:167], v[232:235], v[22:25]
	v_mfma_f32_16x16x32_bf16 v[14:17], v[156:159], v[236:239], v[14:17]
	v_mfma_f32_16x16x32_bf16 v[6:9], v[164:167], v[236:239], v[6:9]
	v_mfma_f32_16x16x32_bf16 v[62:65], v[160:163], v[224:227], v[62:65]
	v_mfma_f32_16x16x32_bf16 v[54:57], v[192:195], v[224:227], v[54:57]
	v_mfma_f32_16x16x32_bf16 v[46:49], v[160:163], v[228:231], v[46:49]
	v_mfma_f32_16x16x32_bf16 v[38:41], v[192:195], v[228:231], v[38:41]
	v_mfma_f32_16x16x32_bf16 v[30:33], v[160:163], v[240:243], v[30:33]
	v_mfma_f32_16x16x32_bf16 v[22:25], v[192:195], v[240:243], v[22:25]
	v_mfma_f32_16x16x32_bf16 v[14:17], v[160:163], v[244:247], v[14:17]
	v_mfma_f32_16x16x32_bf16 v[6:9], v[192:195], v[244:247], v[6:9]
	s_setprio 0
	s_setprio 1
	v_mfma_f32_16x16x32_bf16 v[58:61], v[200:203], v[216:219], v[58:61]
	v_mfma_f32_16x16x32_bf16 v[50:53], v[208:211], v[216:219], v[50:53]
	v_mfma_f32_16x16x32_bf16 v[42:45], v[200:203], v[220:223], v[42:45]
	v_mfma_f32_16x16x32_bf16 v[34:37], v[208:211], v[220:223], v[34:37]
	v_mfma_f32_16x16x32_bf16 v[26:29], v[200:203], v[232:235], v[26:29]
	v_mfma_f32_16x16x32_bf16 v[18:21], v[208:211], v[232:235], v[18:21]
	v_mfma_f32_16x16x32_bf16 v[10:13], v[200:203], v[236:239], v[10:13]
	v_mfma_f32_16x16x32_bf16 v[2:5], v[208:211], v[236:239], v[2:5]
	v_mfma_f32_16x16x32_bf16 v[58:61], v[204:207], v[224:227], v[58:61]
	v_mfma_f32_16x16x32_bf16 v[50:53], v[212:215], v[224:227], v[50:53]
	v_mfma_f32_16x16x32_bf16 v[42:45], v[204:207], v[228:231], v[42:45]
	v_mfma_f32_16x16x32_bf16 v[34:37], v[212:215], v[228:231], v[34:37]
	v_mfma_f32_16x16x32_bf16 v[26:29], v[204:207], v[240:243], v[26:29]
	v_mfma_f32_16x16x32_bf16 v[18:21], v[212:215], v[240:243], v[18:21]
	v_mfma_f32_16x16x32_bf16 v[10:13], v[204:207], v[244:247], v[10:13]
	v_mfma_f32_16x16x32_bf16 v[2:5], v[212:215], v[244:247], v[2:5]
	s_setprio 0
	s_waitcnt vmcnt(8)
	s_barrier
	s_add_i32 s63, s63, 2
	s_add_u32 s31, s31, 0x8000
	s_addc_u32 s62, s62, 0
	s_add_u32 s38, s38, 0x100
	s_addc_u32 s39, s39, 0
	s_cmp_gt_u32 s63, 13
	s_cbranch_scc0 .LBB0_1257
	s_and_b64 vcc, exec, s[22:23]
	s_cbranch_vccz .LBB0_1260
	s_barrier

; #define PG8_STAGE(bufoff, gbase, voff) do { _Pragma("unroll") for (int _i = 0; _i < 2; ++_i) \
;         __builtin_amdgcn_global_load_lds((const unsigned*)((const char*)(gbase) + (voff)[_i]), (LAS unsigned*)(lds + (bufoff) + ldsw + _i * 8192), 16, 0, 0); } while (0)
; #define PG8_LDA(dst, b, h) do { _Pragma("unroll") for (int m = 0; m < 4; ++m) _Pragma("unroll") for (int k = 0; k < 2; ++k) dst[m][k] = *(const LAS bf16x8*)(lds + PG8_SA(b, h) + ((aoff ^ (k * 64)) + m * 2048)); } while (0)
; #define PG8_LDB(dst, b, h) do { _Pragma("unroll") for (int n = 0; n < 2; ++n) _Pragma("unroll") for (int k = 0; k < 2; ++k) dst[n][k] = *(const LAS bf16x8*)(lds + PG8_SB(b, h) + ((boff ^ (k * 64)) + n * 2048)); } while (0)
;     ...
;         for (int t = 0; t < nt; t += 2) {
;             const bool last = (t == nt - 2);
;             const char* a1 = cA + (size_t)(t + 1) * kstepA;
;             const char* a2 = last ? nA : cA + (size_t)(t + 2) * kstepA; const char* b2 = last ? nB : cB + (size_t)(t + 2) * kstepB;
;             const char* a3 = a2 + kstepA; const char* b3 = b2 + kstepB;
;             unsigned vs[2][2];
;             if constexpr (GATHER) {
;                 if (last && has_next) {
; #pragma unroll
;                     for (int hh = 0; hh < 2; ++hh)
; #pragma unroll
;                         for (int i = 0; i < 2; ++i) voffN[hh][i] = (unsigned)idxl[(ui + 1) * 256 + hh * HALF + sR[i]] * (unsigned)(K * 2) + (unsigned)sC[i] * 2u;
;                 }
; #pragma unroll
;                 for (int hh = 0; hh < 2; ++hh)
; #pragma unroll
;                     for (int i = 0; i < 2; ++i) vs[hh][i] = last ? voffN[hh][i] : voffA[hh][i];
;             } else {
; #pragma unroll
;                 for (int hh = 0; hh < 2; ++hh)
; #pragma unroll
;                     for (int i = 0; i < 2; ++i) vs[hh][i] = voffA[hh][i];
;             }
;             PG8_LDB(B0, 0, 0); PG8_LDB(B1, 0, 1); PG8_SCHED; PG8_LDA(At, 0, 0); PG8_STAGE(PG8_SA(1, 1), a1, voffA[1]);
;             PG8_WAIT_V(8); PG8_WAIT_L(0); PG8_BAR; if (do0) { PG8_MMA(0, 0, At, B0); PG8_MMA(0, 1, At, B1); } PG8_BAR; PG8_SCHED;
;             PG8_LDA(At, 0, 1); PG8_STAGE(PG8_SB(0, 0), b2, voffB); PG8_STAGE(PG8_SB(0, 1), b2 + hstep, voffB); PG8_STAGE(PG8_SA(0, 0), a2, vs[0]);
;             PG8_WAIT_V(8); PG8_WAIT_L(0); PG8_BAR; if (do1) { PG8_MMA(1, 0, At, B0); PG8_MMA(1, 1, At, B1); } PG8_BAR; PG8_SCHED;
.LBB0_1343:
	v_add_u32_e32 v130, s92, v161
	v_add_u32_e32 v134, s92, v188
	v_add_u32_e32 v138, s93, v161
	v_add_u32_e32 v142, s93, v188
	v_add_u32_e32 v158, s62, v161
	ds_read_b128 v[130:133], v130
	ds_read_b128 v[134:137], v134
	ds_read_b128 v[138:141], v138
	ds_read_b128 v[142:145], v142
	v_add_u32_e32 v184, s62, v188
	ds_read_b128 v[180:183], v158
	ds_read_b128 v[200:203], v184
	v_add_u32_e32 v158, s63, v161
	s_add_u32 s56, s0, 0x4000
	v_add_u32_e32 v184, s63, v188
	ds_read_b128 v[204:207], v158
	ds_read_b128 v[208:211], v184
	s_addc_u32 s57, s1, 0
	s_cmp_eq_u32 s95, 12
	s_cselect_b32 s60, s23, s56
	s_cselect_b32 s61, s3, s57
	s_cselect_b32 s58, s47, s74
	s_cselect_b32 s59, s45, s94
	s_add_u32 s56, s60, 0x4000
	s_addc_u32 s57, s61, 0
	v_lshl_add_u64 v[184:185], s[0:1], 0, v[176:177]
	s_add_i32 m0, s55, 0xc000
	ds_read_b128 v[212:215], v193
	ds_read_b128 v[216:219], v193 offset:2048
	ds_read_b128 v[220:223], v194
	ds_read_b128 v[224:227], v194 offset:2048
	ds_read_b128 v[228:231], v193 offset:4096
	ds_read_b128 v[232:235], v193 offset:6144
	ds_read_b128 v[236:239], v194 offset:4096
	ds_read_b128 v[240:243], v194 offset:6144
	global_load_lds_dwordx4 v[184:185], off
	v_lshl_add_u64 v[184:185], s[0:1], 0, v[178:179]
	s_add_i32 m0, s55, 0xe000
	s_nop 0
	global_load_lds_dwordx4 v[184:185], off
	s_bitcmp1_b32 s8, 0
	s_cbranch_scc0 .Lwm_in1s_0
	s_waitcnt vmcnt(8)
.Lwm_in1s_0:
	s_waitcnt lgkmcnt(0)
	s_barrier
	s_setprio 1
	s_waitcnt lgkmcnt(0)
	v_mfma_f32_16x16x32_bf16 v[126:129], v[130:133], v[212:215], v[126:129]
	v_mfma_f32_16x16x32_bf16 v[122:125], v[138:141], v[212:215], v[122:125]
	v_mfma_f32_16x16x32_bf16 v[94:97], v[130:133], v[216:219], v[94:97]
	v_mfma_f32_16x16x32_bf16 v[90:93], v[138:141], v[216:219], v[90:93]
	v_mfma_f32_16x16x32_bf16 v[62:65], v[130:133], v[228:231], v[62:65]
	v_mfma_f32_16x16x32_bf16 v[58:61], v[138:141], v[228:231], v[58:61]
	v_mfma_f32_16x16x32_bf16 v[30:33], v[130:133], v[232:235], v[30:33]
	v_mfma_f32_16x16x32_bf16 v[26:29], v[138:141], v[232:235], v[26:29]
	v_mfma_f32_16x16x32_bf16 v[126:129], v[134:137], v[220:223], v[126:129]
	v_mfma_f32_16x16x32_bf16 v[122:125], v[142:145], v[220:223], v[122:125]
	v_mfma_f32_16x16x32_bf16 v[94:97], v[134:137], v[224:227], v[94:97]
	v_mfma_f32_16x16x32_bf16 v[90:93], v[142:145], v[224:227], v[90:93]
	v_mfma_f32_16x16x32_bf16 v[62:65], v[134:137], v[236:239], v[62:65]
	v_mfma_f32_16x16x32_bf16 v[58:61], v[142:145], v[236:239], v[58:61]
	v_mfma_f32_16x16x32_bf16 v[30:33], v[134:137], v[240:243], v[30:33]
	v_mfma_f32_16x16x32_bf16 v[26:29], v[142:145], v[240:243], v[26:29]
	s_setprio 0
	s_setprio 1
	v_mfma_f32_16x16x32_bf16 v[110:113], v[180:183], v[212:215], v[110:113]
	v_mfma_f32_16x16x32_bf16 v[106:109], v[204:207], v[212:215], v[106:109]
	v_mfma_f32_16x16x32_bf16 v[78:81], v[180:183], v[216:219], v[78:81]
	v_mfma_f32_16x16x32_bf16 v[74:77], v[204:207], v[216:219], v[74:77]
	v_mfma_f32_16x16x32_bf16 v[46:49], v[180:183], v[228:231], v[46:49]
	v_mfma_f32_16x16x32_bf16 v[42:45], v[204:207], v[228:231], v[42:45]
	v_mfma_f32_16x16x32_bf16 v[14:17], v[180:183], v[232:235], v[14:17]
	v_mfma_f32_16x16x32_bf16 v[10:13], v[204:207], v[232:235], v[10:13]
	v_mfma_f32_16x16x32_bf16 v[110:113], v[200:203], v[220:223], v[110:113]
	v_mfma_f32_16x16x32_bf16 v[106:109], v[208:211], v[220:223], v[106:109]
	v_mfma_f32_16x16x32_bf16 v[78:81], v[200:203], v[224:227], v[78:81]
	v_mfma_f32_16x16x32_bf16 v[74:77], v[208:211], v[224:227], v[74:77]
	v_mfma_f32_16x16x32_bf16 v[46:49], v[200:203], v[236:239], v[46:49]
	v_mfma_f32_16x16x32_bf16 v[42:45], v[208:211], v[236:239], v[42:45]
	v_mfma_f32_16x16x32_bf16 v[14:17], v[200:203], v[240:243], v[14:17]
	v_mfma_f32_16x16x32_bf16 v[10:13], v[208:211], v[240:243], v[10:13]
	s_setprio 0
	s_waitcnt vmcnt(8)
	s_barrier
	s_add_i32 vcc_lo, s92, s64
	v_lshl_add_u64 v[184:185], s[58:59], 0, v[146:147]
	s_mov_b32 m0, vcc_lo
	ds_read_b128 v[212:215], v193 offset:16384
	ds_read_b128 v[216:219], v193 offset:18432
	ds_read_b128 v[220:223], v194 offset:16384
	ds_read_b128 v[224:227], v194 offset:18432
	ds_read_b128 v[228:231], v193 offset:20480
	ds_read_b128 v[232:235], v193 offset:22528
	ds_read_b128 v[236:239], v194 offset:20480
	ds_read_b128 v[240:243], v194 offset:22528
	global_load_lds_dwordx4 v[184:185], off
	s_add_i32 m0, vcc_lo, 0x2000
	s_add_u32 vcc_lo, s58, 0x40000
	v_lshl_add_u64 v[196:197], s[58:59], 0, v[148:149]
	s_addc_u32 vcc_hi, s59, 0
	s_add_i32 s18, s62, s64
	global_load_lds_dwordx4 v[196:197], off
	v_lshl_add_u64 v[244:245], vcc, 0, v[146:147]
	s_mov_b32 m0, s18
	s_nop 0
	global_load_lds_dwordx4 v[244:245], off
	v_lshl_add_u64 v[244:245], vcc, 0, v[148:149]
	s_add_i32 m0, s18, 0x2000
	s_nop 0
	global_load_lds_dwordx4 v[244:245], off
	v_lshl_add_u64 v[244:245], s[60:61], 0, v[150:151]
	s_mov_b32 m0, s55
	s_nop 0
	global_load_lds_dwordx4 v[244:245], off
	v_lshl_add_u64 v[244:245], s[60:61], 0, v[152:153]
	s_mov_b32 m0, s65
	s_nop 0
	global_load_lds_dwordx4 v[244:245], off
	s_bitcmp1_b32 s8, 0
	s_cbranch_scc0 .Lwm_in1s_1
	s_waitcnt vmcnt(8)
; #define PG8_STAGE(bufoff, gbase, voff) do { _Pragma("unroll") for (int _i = 0; _i < 2; ++_i) \
;         __builtin_amdgcn_global_load_lds((const unsigned*)((const char*)(gbase) + (voff)[_i]), (LAS unsigned*)(lds + (bufoff) + ldsw + _i * 8192), 16, 0, 0); } while (0)
; #define PG8_LDA(dst, b, h) do { _Pragma("unroll") for (int m = 0; m < 4; ++m) _Pragma("unroll") for (int k = 0; k < 2; ++k) dst[m][k] = *(const LAS bf16x8*)(lds + PG8_SA(b, h) + ((aoff ^ (k * 64)) + m * 2048)); } while (0)
; #define PG8_LDB(dst, b, h) do { _Pragma("unroll") for (int n = 0; n < 2; ++n) _Pragma("unroll") for (int k = 0; k < 2; ++k) dst[n][k] = *(const LAS bf16x8*)(lds + PG8_SB(b, h) + ((boff ^ (k * 64)) + n * 2048)); } while (0)
; #define PG8_MMA(ai, bj, At, Bt) do { __builtin_amdgcn_s_setprio(1); _Pragma("unroll") for (int m = 0; m < 4; ++m) _Pragma("unroll") for (int n = 0; n < 2; ++n) _Pragma("unroll") for (int k = 0; k < 2; ++k) \
;         acc[ai][bj][m][n] = __builtin_amdgcn_mfma_f32_16x16x32_bf16(Bt[n][k], At[m][k], acc[ai][bj][m][n], 0, 0, 0); __builtin_amdgcn_s_setprio(0); } while (0)
; #define PG8_WAIT_V(n) asm volatile("s_waitcnt vmcnt(" #n ")" ::: "memory")
; #define PG8_WAIT_L(n) asm volatile("s_waitcnt lgkmcnt(" #n ")" ::: "memory")
; #define PG8_BAR __builtin_amdgcn_s_barrier()
; #define PG8_SCHED __builtin_amdgcn_sched_barrier(0)
;     ...
;             PG8_WAIT_V(8); PG8_WAIT_L(0); PG8_BAR; if (do1) { PG8_MMA(1, 0, At, B0); PG8_MMA(1, 1, At, B1); } PG8_BAR; PG8_SCHED;
;             PG8_LDB(B0, 1, 0); PG8_LDB(B1, 1, 1); PG8_SCHED; PG8_LDA(At, 1, 0); PG8_STAGE(PG8_SA(0, 1), a2, vs[1]);
;             PG8_WAIT_V(8); PG8_WAIT_L(0); PG8_BAR; if (do0) { PG8_MMA(0, 0, At, B0); PG8_MMA(0, 1, At, B1); } PG8_BAR; PG8_SCHED;
.Lwm_in1s_1:
	s_waitcnt lgkmcnt(0)
	s_barrier
	s_setprio 1
	s_waitcnt lgkmcnt(0)
	v_mfma_f32_16x16x32_bf16 v[118:121], v[130:133], v[212:215], v[118:121]
	v_mfma_f32_16x16x32_bf16 v[114:117], v[138:141], v[212:215], v[114:117]
	v_mfma_f32_16x16x32_bf16 v[86:89], v[130:133], v[216:219], v[86:89]
	v_mfma_f32_16x16x32_bf16 v[82:85], v[138:141], v[216:219], v[82:85]
	v_mfma_f32_16x16x32_bf16 v[54:57], v[130:133], v[228:231], v[54:57]
	v_mfma_f32_16x16x32_bf16 v[50:53], v[138:141], v[228:231], v[50:53]
	v_mfma_f32_16x16x32_bf16 v[22:25], v[130:133], v[232:235], v[22:25]
	v_mfma_f32_16x16x32_bf16 v[18:21], v[138:141], v[232:235], v[18:21]
	v_mfma_f32_16x16x32_bf16 v[118:121], v[134:137], v[220:223], v[118:121]
	v_mfma_f32_16x16x32_bf16 v[114:117], v[142:145], v[220:223], v[114:117]
	v_mfma_f32_16x16x32_bf16 v[86:89], v[134:137], v[224:227], v[86:89]
	v_mfma_f32_16x16x32_bf16 v[82:85], v[142:145], v[224:227], v[82:85]
	v_mfma_f32_16x16x32_bf16 v[54:57], v[134:137], v[236:239], v[54:57]
	v_mfma_f32_16x16x32_bf16 v[50:53], v[142:145], v[236:239], v[50:53]
	v_mfma_f32_16x16x32_bf16 v[22:25], v[134:137], v[240:243], v[22:25]
	v_mfma_f32_16x16x32_bf16 v[18:21], v[142:145], v[240:243], v[18:21]
	s_setprio 0
	s_setprio 1
	v_mfma_f32_16x16x32_bf16 v[102:105], v[180:183], v[212:215], v[102:105]
	v_mfma_f32_16x16x32_bf16 v[98:101], v[204:207], v[212:215], v[98:101]
	v_mfma_f32_16x16x32_bf16 v[70:73], v[180:183], v[216:219], v[70:73]
	v_mfma_f32_16x16x32_bf16 v[66:69], v[204:207], v[216:219], v[66:69]
	v_mfma_f32_16x16x32_bf16 v[38:41], v[180:183], v[228:231], v[38:41]
	v_mfma_f32_16x16x32_bf16 v[34:37], v[204:207], v[228:231], v[34:37]
	v_mfma_f32_16x16x32_bf16 v[6:9], v[180:183], v[232:235], v[6:9]
	v_mfma_f32_16x16x32_bf16 v[2:5], v[204:207], v[232:235], v[2:5]
	v_mfma_f32_16x16x32_bf16 v[102:105], v[200:203], v[220:223], v[102:105]
	v_mfma_f32_16x16x32_bf16 v[98:101], v[208:211], v[220:223], v[98:101]
	v_mfma_f32_16x16x32_bf16 v[70:73], v[200:203], v[224:227], v[70:73]
	v_mfma_f32_16x16x32_bf16 v[66:69], v[208:211], v[224:227], v[66:69]
	v_mfma_f32_16x16x32_bf16 v[38:41], v[200:203], v[236:239], v[38:41]
	v_mfma_f32_16x16x32_bf16 v[34:37], v[208:211], v[236:239], v[34:37]
	v_mfma_f32_16x16x32_bf16 v[6:9], v[200:203], v[240:243], v[6:9]
	v_mfma_f32_16x16x32_bf16 v[2:5], v[208:211], v[240:243], v[2:5]
	s_setprio 0
	s_waitcnt vmcnt(8)
	s_barrier
	s_add_i32 s18, 0, 0x18000
	s_add_i32 s19, 0, 0x1c000
	v_add_u32_e32 v130, s18, v161
	v_add_u32_e32 v134, s18, v188
	v_add_u32_e32 v138, s72, v161
	v_add_u32_e32 v142, s72, v188
	v_add_u32_e32 v158, s19, v161
	ds_read_b128 v[130:133], v130
	ds_read_b128 v[134:137], v134
	ds_read_b128 v[138:141], v138
	ds_read_b128 v[142:145], v142
	v_add_u32_e32 v195, s19, v188
	ds_read_b128 v[180:183], v158
	ds_read_b128 v[200:203], v195
	v_add_u32_e32 v158, s73, v161
	v_add_u32_e32 v195, s73, v188
	ds_read_b128 v[204:207], v158
	ds_read_b128 v[208:211], v195
	s_mov_b32 m0, s66
	v_lshl_add_u64 v[244:245], s[60:61], 0, v[154:155]
	ds_read_b128 v[212:215], v193 offset:32768
	ds_read_b128 v[216:219], v193 offset:34816
	ds_read_b128 v[220:223], v194 offset:32768
	ds_read_b128 v[224:227], v194 offset:34816
	ds_read_b128 v[228:231], v193 offset:36864
	ds_read_b128 v[232:235], v193 offset:38912
	ds_read_b128 v[236:239], v194 offset:36864
	ds_read_b128 v[240:243], v194 offset:38912
	global_load_lds_dwordx4 v[244:245], off
	v_lshl_add_u64 v[244:245], s[60:61], 0, v[156:157]
	s_mov_b32 m0, s67
	s_nop 0
	global_load_lds_dwordx4 v[244:245], off
	s_bitcmp1_b32 s8, 0
	s_cbranch_scc0 .Lwm_in1s_2
	s_waitcnt vmcnt(8)
; #define PG8_STAGE(bufoff, gbase, voff) do { _Pragma("unroll") for (int _i = 0; _i < 2; ++_i) \
;         __builtin_amdgcn_global_load_lds((const unsigned*)((const char*)(gbase) + (voff)[_i]), (LAS unsigned*)(lds + (bufoff) + ldsw + _i * 8192), 16, 0, 0); } while (0)
; #define PG8_LDA(dst, b, h) do { _Pragma("unroll") for (int m = 0; m < 4; ++m) _Pragma("unroll") for (int k = 0; k < 2; ++k) dst[m][k] = *(const LAS bf16x8*)(lds + PG8_SA(b, h) + ((aoff ^ (k * 64)) + m * 2048)); } while (0)
; #define PG8_MMA(ai, bj, At, Bt) do { __builtin_amdgcn_s_setprio(1); _Pragma("unroll") for (int m = 0; m < 4; ++m) _Pragma("unroll") for (int n = 0; n < 2; ++n) _Pragma("unroll") for (int k = 0; k < 2; ++k) \
;         acc[ai][bj][m][n] = __builtin_amdgcn_mfma_f32_16x16x32_bf16(Bt[n][k], At[m][k], acc[ai][bj][m][n], 0, 0, 0); __builtin_amdgcn_s_setprio(0); } while (0)
; #define PG8_WAIT_V(n) asm volatile("s_waitcnt vmcnt(" #n ")" ::: "memory")
; #define PG8_WAIT_L(n) asm volatile("s_waitcnt lgkmcnt(" #n ")" ::: "memory")
; #define PG8_BAR __builtin_amdgcn_s_barrier()
; #define PG8_SCHED __builtin_amdgcn_sched_barrier(0)
;     ...
;             PG8_WAIT_V(8); PG8_WAIT_L(0); PG8_BAR; if (do0) { PG8_MMA(0, 0, At, B0); PG8_MMA(0, 1, At, B1); } PG8_BAR; PG8_SCHED;
;             PG8_LDA(At, 1, 1); PG8_STAGE(PG8_SB(1, 0), b3, voffB); PG8_STAGE(PG8_SB(1, 1), b3 + hstep, voffB); PG8_STAGE(PG8_SA(1, 0), a3, vs[0]);
;             PG8_WAIT_V(8); PG8_WAIT_L(0); PG8_BAR; if (do1) { PG8_MMA(1, 0, At, B0); PG8_MMA(1, 1, At, B1); } PG8_BAR; PG8_SCHED;
;         }
.Lwm_in1s_2:
	s_waitcnt lgkmcnt(0)
	s_barrier
	s_setprio 1
	s_waitcnt lgkmcnt(0)
	v_mfma_f32_16x16x32_bf16 v[126:129], v[130:133], v[212:215], v[126:129]
	v_mfma_f32_16x16x32_bf16 v[122:125], v[138:141], v[212:215], v[122:125]
	v_mfma_f32_16x16x32_bf16 v[94:97], v[130:133], v[216:219], v[94:97]
	v_mfma_f32_16x16x32_bf16 v[90:93], v[138:141], v[216:219], v[90:93]
	v_mfma_f32_16x16x32_bf16 v[62:65], v[130:133], v[228:231], v[62:65]
	v_mfma_f32_16x16x32_bf16 v[58:61], v[138:141], v[228:231], v[58:61]
	v_mfma_f32_16x16x32_bf16 v[30:33], v[130:133], v[232:235], v[30:33]
	v_mfma_f32_16x16x32_bf16 v[26:29], v[138:141], v[232:235], v[26:29]
	v_mfma_f32_16x16x32_bf16 v[126:129], v[134:137], v[220:223], v[126:129]
	v_mfma_f32_16x16x32_bf16 v[122:125], v[142:145], v[220:223], v[122:125]
	v_mfma_f32_16x16x32_bf16 v[94:97], v[134:137], v[224:227], v[94:97]
	v_mfma_f32_16x16x32_bf16 v[90:93], v[142:145], v[224:227], v[90:93]
	v_mfma_f32_16x16x32_bf16 v[62:65], v[134:137], v[236:239], v[62:65]
	v_mfma_f32_16x16x32_bf16 v[58:61], v[142:145], v[236:239], v[58:61]
	v_mfma_f32_16x16x32_bf16 v[30:33], v[134:137], v[240:243], v[30:33]
	v_mfma_f32_16x16x32_bf16 v[26:29], v[142:145], v[240:243], v[26:29]
	s_setprio 0
	s_setprio 1
	v_mfma_f32_16x16x32_bf16 v[110:113], v[180:183], v[212:215], v[110:113]
	v_mfma_f32_16x16x32_bf16 v[106:109], v[204:207], v[212:215], v[106:109]
	v_mfma_f32_16x16x32_bf16 v[78:81], v[180:183], v[216:219], v[78:81]
	v_mfma_f32_16x16x32_bf16 v[74:77], v[204:207], v[216:219], v[74:77]
	v_mfma_f32_16x16x32_bf16 v[46:49], v[180:183], v[228:231], v[46:49]
	v_mfma_f32_16x16x32_bf16 v[42:45], v[204:207], v[228:231], v[42:45]
	v_mfma_f32_16x16x32_bf16 v[14:17], v[180:183], v[232:235], v[14:17]
	v_mfma_f32_16x16x32_bf16 v[10:13], v[204:207], v[232:235], v[10:13]
	v_mfma_f32_16x16x32_bf16 v[110:113], v[200:203], v[220:223], v[110:113]
	v_mfma_f32_16x16x32_bf16 v[106:109], v[208:211], v[220:223], v[106:109]
	v_mfma_f32_16x16x32_bf16 v[78:81], v[200:203], v[224:227], v[78:81]
	v_mfma_f32_16x16x32_bf16 v[74:77], v[208:211], v[224:227], v[74:77]
	v_mfma_f32_16x16x32_bf16 v[46:49], v[200:203], v[236:239], v[46:49]
	v_mfma_f32_16x16x32_bf16 v[42:45], v[208:211], v[236:239], v[42:45]
	v_mfma_f32_16x16x32_bf16 v[14:17], v[200:203], v[240:243], v[14:17]
	v_mfma_f32_16x16x32_bf16 v[10:13], v[208:211], v[240:243], v[10:13]
	s_setprio 0
	s_waitcnt vmcnt(8)
	s_barrier
	s_add_i32 s18, s18, s64
	v_lshl_add_u64 v[184:185], v[184:185], 0, s[10:11]
	s_mov_b32 m0, s18
	ds_read_b128 v[212:215], v193 offset:49152
	ds_read_b128 v[216:219], v193 offset:51200
	ds_read_b128 v[220:223], v194 offset:49152
	ds_read_b128 v[224:227], v194 offset:51200
	ds_read_b128 v[228:231], v193 offset:53248
	ds_read_b128 v[232:235], v193 offset:55296
	ds_read_b128 v[236:239], v194 offset:53248
	ds_read_b128 v[240:243], v194 offset:55296
	global_load_lds_dwordx4 v[184:185], off
	s_add_i32 m0, s18, 0x2000
	s_add_u32 s58, s58, 0x40080
	v_lshl_add_u64 v[184:185], v[196:197], 0, s[10:11]
	s_addc_u32 s59, s59, 0
	s_add_i32 s18, s19, s64
	global_load_lds_dwordx4 v[184:185], off
	v_lshl_add_u64 v[184:185], s[58:59], 0, v[146:147]
	s_mov_b32 m0, s18
	s_nop 0
	global_load_lds_dwordx4 v[184:185], off
	v_lshl_add_u64 v[184:185], s[58:59], 0, v[148:149]
	s_add_i32 m0, s18, 0x2000
	s_nop 0
	global_load_lds_dwordx4 v[184:185], off
	v_lshl_add_u64 v[184:185], s[56:57], 0, v[150:151]
	s_mov_b32 m0, s70
	s_nop 0
	global_load_lds_dwordx4 v[184:185], off
	v_lshl_add_u64 v[184:185], s[56:57], 0, v[152:153]
	s_mov_b32 m0, s71
	s_nop 0
	global_load_lds_dwordx4 v[184:185], off
	s_bitcmp1_b32 s8, 0
	s_cbranch_scc0 .Lwm_in1s_3
	s_waitcnt vmcnt(8)
.Lwm_in1s_3:
	s_waitcnt lgkmcnt(0)
	s_barrier
	s_setprio 1
	s_waitcnt lgkmcnt(0)
	v_mfma_f32_16x16x32_bf16 v[118:121], v[130:133], v[212:215], v[118:121]
	v_mfma_f32_16x16x32_bf16 v[114:117], v[138:141], v[212:215], v[114:117]
	v_mfma_f32_16x16x32_bf16 v[86:89], v[130:133], v[216:219], v[86:89]
	v_mfma_f32_16x16x32_bf16 v[82:85], v[138:141], v[216:219], v[82:85]
	v_mfma_f32_16x16x32_bf16 v[54:57], v[130:133], v[228:231], v[54:57]
	v_mfma_f32_16x16x32_bf16 v[50:53], v[138:141], v[228:231], v[50:53]
	v_mfma_f32_16x16x32_bf16 v[22:25], v[130:133], v[232:235], v[22:25]
	v_mfma_f32_16x16x32_bf16 v[18:21], v[138:141], v[232:235], v[18:21]
	v_mfma_f32_16x16x32_bf16 v[118:121], v[134:137], v[220:223], v[118:121]
	v_mfma_f32_16x16x32_bf16 v[114:117], v[142:145], v[220:223], v[114:117]
	v_mfma_f32_16x16x32_bf16 v[86:89], v[134:137], v[224:227], v[86:89]
	v_mfma_f32_16x16x32_bf16 v[82:85], v[142:145], v[224:227], v[82:85]
	v_mfma_f32_16x16x32_bf16 v[54:57], v[134:137], v[236:239], v[54:57]
	v_mfma_f32_16x16x32_bf16 v[50:53], v[142:145], v[236:239], v[50:53]
	v_mfma_f32_16x16x32_bf16 v[22:25], v[134:137], v[240:243], v[22:25]
	v_mfma_f32_16x16x32_bf16 v[18:21], v[142:145], v[240:243], v[18:21]
	s_setprio 0
	s_setprio 1
	v_mfma_f32_16x16x32_bf16 v[102:105], v[180:183], v[212:215], v[102:105]
	v_mfma_f32_16x16x32_bf16 v[98:101], v[204:207], v[212:215], v[98:101]
	v_mfma_f32_16x16x32_bf16 v[70:73], v[180:183], v[216:219], v[70:73]
	v_mfma_f32_16x16x32_bf16 v[66:69], v[204:207], v[216:219], v[66:69]
	v_mfma_f32_16x16x32_bf16 v[38:41], v[180:183], v[228:231], v[38:41]
	v_mfma_f32_16x16x32_bf16 v[34:37], v[204:207], v[228:231], v[34:37]
	v_mfma_f32_16x16x32_bf16 v[6:9], v[180:183], v[232:235], v[6:9]
	v_mfma_f32_16x16x32_bf16 v[2:5], v[204:207], v[232:235], v[2:5]
	v_mfma_f32_16x16x32_bf16 v[102:105], v[200:203], v[220:223], v[102:105]
	v_mfma_f32_16x16x32_bf16 v[98:101], v[208:211], v[220:223], v[98:101]
	v_mfma_f32_16x16x32_bf16 v[70:73], v[200:203], v[224:227], v[70:73]
	v_mfma_f32_16x16x32_bf16 v[66:69], v[208:211], v[224:227], v[66:69]
	v_mfma_f32_16x16x32_bf16 v[38:41], v[200:203], v[236:239], v[38:41]
	v_mfma_f32_16x16x32_bf16 v[34:37], v[208:211], v[236:239], v[34:37]
	v_mfma_f32_16x16x32_bf16 v[6:9], v[200:203], v[240:243], v[6:9]
	v_mfma_f32_16x16x32_bf16 v[2:5], v[208:211], v[240:243], v[2:5]
	s_setprio 0
	s_waitcnt vmcnt(8)
	s_barrier
	s_add_i32 s95, s95, 2
	s_add_u32 s74, s74, 0x100
	s_addc_u32 s94, s94, 0
	s_add_u32 s0, s0, 0x8000
	s_addc_u32 s1, s1, 0
	s_cmp_gt_u32 s95, 13
	s_cbranch_scc0 .LBB0_1343
	s_and_b64 vcc, exec, s[12:13]
	s_cbranch_vccz .LBB0_1346
	s_barrier

; #define PG8_STAGE(bufoff, gbase, voff) do { _Pragma("unroll") for (int _i = 0; _i < 2; ++_i) \
;         __builtin_amdgcn_global_load_lds((const unsigned*)((const char*)(gbase) + (voff)[_i]), (LAS unsigned*)(lds + (bufoff) + ldsw + _i * 8192), 16, 0, 0); } while (0)
; #define PG8_LDA(dst, b, h) do { _Pragma("unroll") for (int m = 0; m < 4; ++m) _Pragma("unroll") for (int k = 0; k < 2; ++k) dst[m][k] = *(const LAS bf16x8*)(lds + PG8_SA(b, h) + ((aoff ^ (k * 64)) + m * 2048)); } while (0)
; #define PG8_LDB(dst, b, h) do { _Pragma("unroll") for (int n = 0; n < 2; ++n) _Pragma("unroll") for (int k = 0; k < 2; ++k) dst[n][k] = *(const LAS bf16x8*)(lds + PG8_SB(b, h) + ((boff ^ (k * 64)) + n * 2048)); } while (0)
;     ...
;         for (int t = 0; t < nt; t += 2) {
;             const bool last = (t == nt - 2);
;             const char* a1 = cA + (size_t)(t + 1) * kstepA;
;             const char* a2 = last ? nA : cA + (size_t)(t + 2) * kstepA; const char* b2 = last ? nB : cB + (size_t)(t + 2) * kstepB;
;             const char* a3 = a2 + kstepA; const char* b3 = b2 + kstepB;
;             unsigned vs[2][2];
;             if constexpr (GATHER) {
;                 if (last && has_next) {
; #pragma unroll
;                     for (int hh = 0; hh < 2; ++hh)
; #pragma unroll
;                         for (int i = 0; i < 2; ++i) voffN[hh][i] = (unsigned)idxl[(ui + 1) * 256 + hh * HALF + sR[i]] * (unsigned)(K * 2) + (unsigned)sC[i] * 2u;
;                 }
; #pragma unroll
;                 for (int hh = 0; hh < 2; ++hh)
; #pragma unroll
;                     for (int i = 0; i < 2; ++i) vs[hh][i] = last ? voffN[hh][i] : voffA[hh][i];
;             } else {
; #pragma unroll
;                 for (int hh = 0; hh < 2; ++hh)
; #pragma unroll
;                     for (int i = 0; i < 2; ++i) vs[hh][i] = voffA[hh][i];
;             }
;             PG8_LDB(B0, 0, 0); PG8_LDB(B1, 0, 1); PG8_SCHED; PG8_LDA(At, 0, 0); PG8_STAGE(PG8_SA(1, 1), a1, voffA[1]);
;             PG8_WAIT_V(8); PG8_WAIT_L(0); PG8_BAR; if (do0) { PG8_MMA(0, 0, At, B0); PG8_MMA(0, 1, At, B1); } PG8_BAR; PG8_SCHED;
;             PG8_LDA(At, 0, 1); PG8_STAGE(PG8_SB(0, 0), b2, voffB); PG8_STAGE(PG8_SB(0, 1), b2 + hstep, voffB); PG8_STAGE(PG8_SA(0, 0), a2, vs[0]);
;             PG8_WAIT_V(8); PG8_WAIT_L(0); PG8_BAR; if (do1) { PG8_MMA(1, 0, At, B0); PG8_MMA(1, 1, At, B1); } PG8_BAR; PG8_SCHED;
.LBB0_1934:
	ds_read_b128 v[74:77], v191
	ds_read_b128 v[78:81], v192
	ds_read_b128 v[102:105], v193
	ds_read_b128 v[106:109], v194
	ds_read_b128 v[168:171], v195
	ds_read_b128 v[172:175], v196
	ds_read_b128 v[176:179], v197
	ds_read_b128 v[180:183], v199
	s_add_u32 s38, s0, 0x80
	s_addc_u32 s39, s1, 0
	s_cmp_eq_u32 s45, 28
	s_cselect_b32 s43, s7, s39
	s_cselect_b32 s42, s8, s38
	s_cselect_b32 s39, s27, s44
	s_cselect_b32 s38, s29, s37
	v_lshl_add_u64 v[184:185], s[0:1], 0, v[162:163]
	s_add_i32 m0, s52, 0xc000
	ds_read_b128 v[210:213], v200
	ds_read_b128 v[214:217], v200 offset:2048
	ds_read_b128 v[218:221], v201
	ds_read_b128 v[222:225], v201 offset:2048
	ds_read_b128 v[226:229], v200 offset:4096
	ds_read_b128 v[230:233], v200 offset:6144
	ds_read_b128 v[234:237], v201 offset:4096
	ds_read_b128 v[238:241], v201 offset:6144
	global_load_lds_dwordx4 v[184:185], off
	v_lshl_add_u64 v[184:185], s[0:1], 0, v[160:161]
	s_add_i32 m0, s52, 0xe000
	s_add_u32 s40, s38, 0x4000
	global_load_lds_dwordx4 v[184:185], off
	s_mov_b64 vcc, s[10:11]
	s_cbranch_vccz .Lwm_out1_0
	s_waitcnt vmcnt(8)
.Lwm_out1_0:
	s_waitcnt lgkmcnt(0)
	s_addc_u32 s41, s39, 0
	s_barrier
	s_setprio 1
	s_waitcnt lgkmcnt(0)
	v_mfma_f32_16x16x32_bf16 v[142:145], v[74:77], v[210:213], v[142:145]
	v_mfma_f32_16x16x32_bf16 v[10:13], v[102:105], v[210:213], v[10:13]
	v_mfma_f32_16x16x32_bf16 v[134:137], v[74:77], v[214:217], v[134:137]
	v_mfma_f32_16x16x32_bf16 v[18:21], v[102:105], v[214:217], v[18:21]
	v_mfma_f32_16x16x32_bf16 v[126:129], v[74:77], v[226:229], v[126:129]
	v_mfma_f32_16x16x32_bf16 v[22:25], v[102:105], v[226:229], v[22:25]
	v_mfma_f32_16x16x32_bf16 v[118:121], v[74:77], v[230:233], v[118:121]
	v_mfma_f32_16x16x32_bf16 v[34:37], v[102:105], v[230:233], v[34:37]
	v_mfma_f32_16x16x32_bf16 v[142:145], v[78:81], v[218:221], v[142:145]
	v_mfma_f32_16x16x32_bf16 v[10:13], v[106:109], v[218:221], v[10:13]
	v_mfma_f32_16x16x32_bf16 v[134:137], v[78:81], v[222:225], v[134:137]
	v_mfma_f32_16x16x32_bf16 v[18:21], v[106:109], v[222:225], v[18:21]
	v_mfma_f32_16x16x32_bf16 v[126:129], v[78:81], v[234:237], v[126:129]
	v_mfma_f32_16x16x32_bf16 v[22:25], v[106:109], v[234:237], v[22:25]
	v_mfma_f32_16x16x32_bf16 v[118:121], v[78:81], v[238:241], v[118:121]
	v_mfma_f32_16x16x32_bf16 v[34:37], v[106:109], v[238:241], v[34:37]
	s_setprio 0
	s_setprio 1
	v_mfma_f32_16x16x32_bf16 v[138:141], v[168:171], v[210:213], v[138:141]
	v_mfma_f32_16x16x32_bf16 v[14:17], v[176:179], v[210:213], v[14:17]
	v_mfma_f32_16x16x32_bf16 v[130:133], v[168:171], v[214:217], v[130:133]
	v_mfma_f32_16x16x32_bf16 v[30:33], v[176:179], v[214:217], v[30:33]
	v_mfma_f32_16x16x32_bf16 v[122:125], v[168:171], v[226:229], v[122:125]
	v_mfma_f32_16x16x32_bf16 v[26:29], v[176:179], v[226:229], v[26:29]
	v_mfma_f32_16x16x32_bf16 v[114:117], v[168:171], v[230:233], v[114:117]
	v_mfma_f32_16x16x32_bf16 v[46:49], v[176:179], v[230:233], v[46:49]
	v_mfma_f32_16x16x32_bf16 v[138:141], v[172:175], v[218:221], v[138:141]
	v_mfma_f32_16x16x32_bf16 v[14:17], v[180:183], v[218:221], v[14:17]
	v_mfma_f32_16x16x32_bf16 v[130:133], v[172:175], v[222:225], v[130:133]
	v_mfma_f32_16x16x32_bf16 v[30:33], v[180:183], v[222:225], v[30:33]
	v_mfma_f32_16x16x32_bf16 v[122:125], v[172:175], v[234:237], v[122:125]
	v_mfma_f32_16x16x32_bf16 v[26:29], v[180:183], v[234:237], v[26:29]
	v_mfma_f32_16x16x32_bf16 v[114:117], v[172:175], v[238:241], v[114:117]
	v_mfma_f32_16x16x32_bf16 v[46:49], v[180:183], v[238:241], v[46:49]
	s_setprio 0
	s_waitcnt vmcnt(8)
	s_barrier
	s_add_i32 s46, s67, s51
	v_lshl_add_u64 v[184:185], s[38:39], 0, v[146:147]
	s_mov_b32 m0, s46
	ds_read_b128 v[210:213], v200 offset:16384
	ds_read_b128 v[214:217], v200 offset:18432
	ds_read_b128 v[218:221], v201 offset:16384
	ds_read_b128 v[222:225], v201 offset:18432
	ds_read_b128 v[226:229], v200 offset:20480
	ds_read_b128 v[230:233], v200 offset:22528
	ds_read_b128 v[234:237], v201 offset:20480
	ds_read_b128 v[238:241], v201 offset:22528
	global_load_lds_dwordx4 v[184:185], off
	s_add_i32 m0, s46, 0x2000
	s_add_u32 s46, s38, 0x80000
	v_lshl_add_u64 v[184:185], s[38:39], 0, v[148:149]
	s_addc_u32 s47, s39, 0
	s_add_i32 s72, s68, s51
	global_load_lds_dwordx4 v[184:185], off
	v_lshl_add_u64 v[184:185], s[46:47], 0, v[146:147]
	s_mov_b32 m0, s72
	v_lshl_add_u64 v[242:243], s[42:43], 0, v[152:153]
	global_load_lds_dwordx4 v[184:185], off
	v_lshl_add_u64 v[184:185], s[46:47], 0, v[148:149]
	s_add_i32 m0, s72, 0x2000
	s_nop 0
	global_load_lds_dwordx4 v[184:185], off
	v_lshl_add_u64 v[184:185], s[42:43], 0, v[150:151]
	s_mov_b32 m0, s52
	s_nop 0
	global_load_lds_dwordx4 v[184:185], off
	s_mov_b32 m0, s53
	s_nop 0
	global_load_lds_dwordx4 v[242:243], off
	s_bitcmp1_b32 s10, 0
	s_cbranch_scc0 .Lwm_out1_1
	s_waitcnt vmcnt(8)
; #define PG8_STAGE(bufoff, gbase, voff) do { _Pragma("unroll") for (int _i = 0; _i < 2; ++_i) \
;         __builtin_amdgcn_global_load_lds((const unsigned*)((const char*)(gbase) + (voff)[_i]), (LAS unsigned*)(lds + (bufoff) + ldsw + _i * 8192), 16, 0, 0); } while (0)
; #define PG8_LDA(dst, b, h) do { _Pragma("unroll") for (int m = 0; m < 4; ++m) _Pragma("unroll") for (int k = 0; k < 2; ++k) dst[m][k] = *(const LAS bf16x8*)(lds + PG8_SA(b, h) + ((aoff ^ (k * 64)) + m * 2048)); } while (0)
; #define PG8_LDB(dst, b, h) do { _Pragma("unroll") for (int n = 0; n < 2; ++n) _Pragma("unroll") for (int k = 0; k < 2; ++k) dst[n][k] = *(const LAS bf16x8*)(lds + PG8_SB(b, h) + ((boff ^ (k * 64)) + n * 2048)); } while (0)
; #define PG8_MMA(ai, bj, At, Bt) do { __builtin_amdgcn_s_setprio(1); _Pragma("unroll") for (int m = 0; m < 4; ++m) _Pragma("unroll") for (int n = 0; n < 2; ++n) _Pragma("unroll") for (int k = 0; k < 2; ++k) \
;         acc[ai][bj][m][n] = __builtin_amdgcn_mfma_f32_16x16x32_bf16(Bt[n][k], At[m][k], acc[ai][bj][m][n], 0, 0, 0); __builtin_amdgcn_s_setprio(0); } while (0)
; #define PG8_WAIT_V(n) asm volatile("s_waitcnt vmcnt(" #n ")" ::: "memory")
; #define PG8_WAIT_L(n) asm volatile("s_waitcnt lgkmcnt(" #n ")" ::: "memory")
; #define PG8_BAR __builtin_amdgcn_s_barrier()
; #define PG8_SCHED __builtin_amdgcn_sched_barrier(0)
;     ...
;             PG8_WAIT_V(8); PG8_WAIT_L(0); PG8_BAR; if (do1) { PG8_MMA(1, 0, At, B0); PG8_MMA(1, 1, At, B1); } PG8_BAR; PG8_SCHED;
;             PG8_LDB(B0, 1, 0); PG8_LDB(B1, 1, 1); PG8_SCHED; PG8_LDA(At, 1, 0); PG8_STAGE(PG8_SA(0, 1), a2, vs[1]);
;             PG8_WAIT_V(8); PG8_WAIT_L(0); PG8_BAR; if (do0) { PG8_MMA(0, 0, At, B0); PG8_MMA(0, 1, At, B1); } PG8_BAR; PG8_SCHED;
.Lwm_out1_1:
	s_waitcnt lgkmcnt(0)
	s_barrier
	s_setprio 1
	s_waitcnt lgkmcnt(0)
	v_mfma_f32_16x16x32_bf16 v[110:113], v[74:77], v[210:213], v[110:113]
	v_mfma_f32_16x16x32_bf16 v[58:61], v[102:105], v[210:213], v[58:61]
	v_mfma_f32_16x16x32_bf16 v[94:97], v[74:77], v[214:217], v[94:97]
	v_mfma_f32_16x16x32_bf16 v[82:85], v[102:105], v[214:217], v[82:85]
	v_mfma_f32_16x16x32_bf16 v[66:69], v[74:77], v[226:229], v[66:69]
	v_mfma_f32_16x16x32_bf16 v[62:65], v[102:105], v[226:229], v[62:65]
	v_mfma_f32_16x16x32_bf16 v[42:45], v[74:77], v[230:233], v[42:45]
	v_mfma_f32_16x16x32_bf16 v[38:41], v[102:105], v[230:233], v[38:41]
	v_mfma_f32_16x16x32_bf16 v[110:113], v[78:81], v[218:221], v[110:113]
	v_mfma_f32_16x16x32_bf16 v[58:61], v[106:109], v[218:221], v[58:61]
	v_mfma_f32_16x16x32_bf16 v[94:97], v[78:81], v[222:225], v[94:97]
	v_mfma_f32_16x16x32_bf16 v[82:85], v[106:109], v[222:225], v[82:85]
	v_mfma_f32_16x16x32_bf16 v[66:69], v[78:81], v[234:237], v[66:69]
	v_mfma_f32_16x16x32_bf16 v[62:65], v[106:109], v[234:237], v[62:65]
	v_mfma_f32_16x16x32_bf16 v[42:45], v[78:81], v[238:241], v[42:45]
	v_mfma_f32_16x16x32_bf16 v[38:41], v[106:109], v[238:241], v[38:41]
	s_setprio 0
	s_setprio 1
	v_mfma_f32_16x16x32_bf16 v[70:73], v[176:179], v[210:213], v[70:73]
	v_mfma_f32_16x16x32_bf16 v[86:89], v[176:179], v[214:217], v[86:89]
	v_mfma_f32_16x16x32_bf16 v[54:57], v[168:171], v[226:229], v[54:57]
	v_mfma_f32_16x16x32_bf16 v[50:53], v[176:179], v[226:229], v[50:53]
	v_mfma_f32_16x16x32_bf16 v[6:9], v[168:171], v[230:233], v[6:9]
	v_mfma_f32_16x16x32_bf16 v[2:5], v[176:179], v[230:233], v[2:5]
	v_mfma_f32_16x16x32_bf16 v[74:77], v[168:171], v[210:213], v[98:101]
	v_mfma_f32_16x16x32_bf16 v[70:73], v[180:183], v[218:221], v[70:73]
	v_mfma_f32_16x16x32_bf16 v[78:81], v[168:171], v[214:217], v[90:93]
	v_mfma_f32_16x16x32_bf16 v[86:89], v[180:183], v[222:225], v[86:89]
	v_mfma_f32_16x16x32_bf16 v[54:57], v[172:175], v[234:237], v[54:57]
	v_mfma_f32_16x16x32_bf16 v[50:53], v[180:183], v[234:237], v[50:53]
	v_mfma_f32_16x16x32_bf16 v[6:9], v[172:175], v[238:241], v[6:9]
	v_mfma_f32_16x16x32_bf16 v[2:5], v[180:183], v[238:241], v[2:5]
	v_mfma_f32_16x16x32_bf16 v[74:77], v[172:175], v[218:221], v[74:77]
	v_mfma_f32_16x16x32_bf16 v[78:81], v[172:175], v[222:225], v[78:81]
	s_setprio 0
	s_waitcnt vmcnt(8)
	s_barrier
	s_add_i32 s46, 0, 0x18000
	s_add_i32 s47, 0, 0x1c000
	v_add_u32_e32 v90, s46, v189
	v_add_u32_e32 v98, s46, v190
	v_add_u32_e32 v158, s47, v189
	v_add_u32_e32 v172, s47, v190
	ds_read_b128 v[90:93], v90
	ds_read_b128 v[98:101], v98
	ds_read_b128 v[102:105], v202
	ds_read_b128 v[106:109], v203
	ds_read_b128 v[168:171], v158
	ds_read_b128 v[172:175], v172
	ds_read_b128 v[176:179], v204
	ds_read_b128 v[180:183], v205
	s_mov_b32 m0, s54
	v_lshl_add_u64 v[244:245], s[42:43], 0, v[154:155]
	ds_read_b128 v[210:213], v200 offset:32768
	ds_read_b128 v[214:217], v200 offset:34816
	ds_read_b128 v[218:221], v201 offset:32768
	ds_read_b128 v[222:225], v201 offset:34816
	ds_read_b128 v[226:229], v200 offset:36864
	ds_read_b128 v[230:233], v200 offset:38912
	ds_read_b128 v[234:237], v201 offset:36864
	ds_read_b128 v[238:241], v201 offset:38912
	global_load_lds_dwordx4 v[244:245], off
	v_lshl_add_u64 v[244:245], s[42:43], 0, v[156:157]
	s_mov_b32 m0, s55
	s_nop 0
	global_load_lds_dwordx4 v[244:245], off
	s_bitcmp1_b32 s10, 0
	s_cbranch_scc0 .Lwm_out1_2
	s_waitcnt vmcnt(8)
; #define PG8_STAGE(bufoff, gbase, voff) do { _Pragma("unroll") for (int _i = 0; _i < 2; ++_i) \
;         __builtin_amdgcn_global_load_lds((const unsigned*)((const char*)(gbase) + (voff)[_i]), (LAS unsigned*)(lds + (bufoff) + ldsw + _i * 8192), 16, 0, 0); } while (0)
; #define PG8_LDA(dst, b, h) do { _Pragma("unroll") for (int m = 0; m < 4; ++m) _Pragma("unroll") for (int k = 0; k < 2; ++k) dst[m][k] = *(const LAS bf16x8*)(lds + PG8_SA(b, h) + ((aoff ^ (k * 64)) + m * 2048)); } while (0)
; #define PG8_MMA(ai, bj, At, Bt) do { __builtin_amdgcn_s_setprio(1); _Pragma("unroll") for (int m = 0; m < 4; ++m) _Pragma("unroll") for (int n = 0; n < 2; ++n) _Pragma("unroll") for (int k = 0; k < 2; ++k) \
;         acc[ai][bj][m][n] = __builtin_amdgcn_mfma_f32_16x16x32_bf16(Bt[n][k], At[m][k], acc[ai][bj][m][n], 0, 0, 0); __builtin_amdgcn_s_setprio(0); } while (0)
; #define PG8_WAIT_V(n) asm volatile("s_waitcnt vmcnt(" #n ")" ::: "memory")
; #define PG8_WAIT_L(n) asm volatile("s_waitcnt lgkmcnt(" #n ")" ::: "memory")
; #define PG8_BAR __builtin_amdgcn_s_barrier()
; #define PG8_SCHED __builtin_amdgcn_sched_barrier(0)
;     ...
;             PG8_WAIT_V(8); PG8_WAIT_L(0); PG8_BAR; if (do0) { PG8_MMA(0, 0, At, B0); PG8_MMA(0, 1, At, B1); } PG8_BAR; PG8_SCHED;
;             PG8_LDA(At, 1, 1); PG8_STAGE(PG8_SB(1, 0), b3, voffB); PG8_STAGE(PG8_SB(1, 1), b3 + hstep, voffB); PG8_STAGE(PG8_SA(1, 0), a3, vs[0]);
;             PG8_WAIT_V(8); PG8_WAIT_L(0); PG8_BAR; if (do1) { PG8_MMA(1, 0, At, B0); PG8_MMA(1, 1, At, B1); } PG8_BAR; PG8_SCHED;
;         }
.Lwm_out1_2:
	s_waitcnt lgkmcnt(0)
	s_barrier
	s_setprio 1
	s_waitcnt lgkmcnt(0)
	v_mfma_f32_16x16x32_bf16 v[142:145], v[90:93], v[210:213], v[142:145]
	v_mfma_f32_16x16x32_bf16 v[10:13], v[102:105], v[210:213], v[10:13]
	v_mfma_f32_16x16x32_bf16 v[134:137], v[90:93], v[214:217], v[134:137]
	v_mfma_f32_16x16x32_bf16 v[18:21], v[102:105], v[214:217], v[18:21]
	v_mfma_f32_16x16x32_bf16 v[126:129], v[90:93], v[226:229], v[126:129]
	v_mfma_f32_16x16x32_bf16 v[22:25], v[102:105], v[226:229], v[22:25]
	v_mfma_f32_16x16x32_bf16 v[118:121], v[90:93], v[230:233], v[118:121]
	v_mfma_f32_16x16x32_bf16 v[34:37], v[102:105], v[230:233], v[34:37]
	v_mfma_f32_16x16x32_bf16 v[142:145], v[98:101], v[218:221], v[142:145]
	v_mfma_f32_16x16x32_bf16 v[10:13], v[106:109], v[218:221], v[10:13]
	v_mfma_f32_16x16x32_bf16 v[134:137], v[98:101], v[222:225], v[134:137]
	v_mfma_f32_16x16x32_bf16 v[18:21], v[106:109], v[222:225], v[18:21]
	v_mfma_f32_16x16x32_bf16 v[126:129], v[98:101], v[234:237], v[126:129]
	v_mfma_f32_16x16x32_bf16 v[22:25], v[106:109], v[234:237], v[22:25]
	v_mfma_f32_16x16x32_bf16 v[118:121], v[98:101], v[238:241], v[118:121]
	v_mfma_f32_16x16x32_bf16 v[34:37], v[106:109], v[238:241], v[34:37]
	s_setprio 0
	s_setprio 1
	v_mfma_f32_16x16x32_bf16 v[138:141], v[168:171], v[210:213], v[138:141]
	v_mfma_f32_16x16x32_bf16 v[14:17], v[176:179], v[210:213], v[14:17]
	v_mfma_f32_16x16x32_bf16 v[130:133], v[168:171], v[214:217], v[130:133]
	v_mfma_f32_16x16x32_bf16 v[30:33], v[176:179], v[214:217], v[30:33]
	v_mfma_f32_16x16x32_bf16 v[122:125], v[168:171], v[226:229], v[122:125]
	v_mfma_f32_16x16x32_bf16 v[26:29], v[176:179], v[226:229], v[26:29]
	v_mfma_f32_16x16x32_bf16 v[114:117], v[168:171], v[230:233], v[114:117]
	v_mfma_f32_16x16x32_bf16 v[46:49], v[176:179], v[230:233], v[46:49]
	v_mfma_f32_16x16x32_bf16 v[138:141], v[172:175], v[218:221], v[138:141]
	v_mfma_f32_16x16x32_bf16 v[14:17], v[180:183], v[218:221], v[14:17]
	v_mfma_f32_16x16x32_bf16 v[130:133], v[172:175], v[222:225], v[130:133]
	v_mfma_f32_16x16x32_bf16 v[30:33], v[180:183], v[222:225], v[30:33]
	v_mfma_f32_16x16x32_bf16 v[122:125], v[172:175], v[234:237], v[122:125]
	v_mfma_f32_16x16x32_bf16 v[26:29], v[180:183], v[234:237], v[26:29]
	v_mfma_f32_16x16x32_bf16 v[114:117], v[172:175], v[238:241], v[114:117]
	v_mfma_f32_16x16x32_bf16 v[46:49], v[180:183], v[238:241], v[46:49]
	s_setprio 0
	s_waitcnt vmcnt(8)
	s_barrier
	s_add_i32 s42, s46, s51
	v_lshl_add_u64 v[244:245], s[40:41], 0, v[146:147]
	s_mov_b32 m0, s42
	ds_read_b128 v[210:213], v200 offset:49152
	ds_read_b128 v[214:217], v200 offset:51200
	ds_read_b128 v[218:221], v201 offset:49152
	ds_read_b128 v[222:225], v201 offset:51200
	ds_read_b128 v[226:229], v200 offset:53248
	ds_read_b128 v[230:233], v200 offset:55296
	ds_read_b128 v[234:237], v201 offset:53248
	ds_read_b128 v[238:241], v201 offset:55296
	global_load_lds_dwordx4 v[244:245], off
	s_add_i32 m0, s42, 0x2000
	s_add_u32 s38, s38, 0x84000
	v_lshl_add_u64 v[244:245], s[40:41], 0, v[148:149]
	s_addc_u32 s39, s39, 0
	s_add_i32 s40, s47, s51
	global_load_lds_dwordx4 v[244:245], off
	v_lshl_add_u64 v[244:245], s[38:39], 0, v[146:147]
	s_mov_b32 m0, s40
	v_lshl_add_u64 v[184:185], v[184:185], 0, s[16:17]
	global_load_lds_dwordx4 v[244:245], off
	v_lshl_add_u64 v[244:245], s[38:39], 0, v[148:149]
	s_add_i32 m0, s40, 0x2000
	s_nop 0
	global_load_lds_dwordx4 v[244:245], off
	s_mov_b32 m0, s57
	s_nop 0
	global_load_lds_dwordx4 v[184:185], off
	v_lshl_add_u64 v[184:185], v[242:243], 0, s[16:17]
	s_mov_b32 m0, s58
	s_nop 0
	global_load_lds_dwordx4 v[184:185], off
	s_bitcmp1_b32 s10, 0
	s_cbranch_scc0 .Lwm_out1_3
	s_waitcnt vmcnt(8)
.Lwm_out1_3:
	s_waitcnt lgkmcnt(0)
	s_barrier
	s_setprio 1
	s_waitcnt lgkmcnt(0)
	v_mfma_f32_16x16x32_bf16 v[110:113], v[90:93], v[210:213], v[110:113]
	v_mfma_f32_16x16x32_bf16 v[58:61], v[102:105], v[210:213], v[58:61]
	v_mfma_f32_16x16x32_bf16 v[94:97], v[90:93], v[214:217], v[94:97]
	v_mfma_f32_16x16x32_bf16 v[82:85], v[102:105], v[214:217], v[82:85]
	v_mfma_f32_16x16x32_bf16 v[66:69], v[90:93], v[226:229], v[66:69]
	v_mfma_f32_16x16x32_bf16 v[62:65], v[102:105], v[226:229], v[62:65]
	v_mfma_f32_16x16x32_bf16 v[42:45], v[90:93], v[230:233], v[42:45]
	v_mfma_f32_16x16x32_bf16 v[38:41], v[102:105], v[230:233], v[38:41]
	v_mfma_f32_16x16x32_bf16 v[110:113], v[98:101], v[218:221], v[110:113]
	v_mfma_f32_16x16x32_bf16 v[58:61], v[106:109], v[218:221], v[58:61]
	v_mfma_f32_16x16x32_bf16 v[94:97], v[98:101], v[222:225], v[94:97]
	v_mfma_f32_16x16x32_bf16 v[82:85], v[106:109], v[222:225], v[82:85]
	v_mfma_f32_16x16x32_bf16 v[66:69], v[98:101], v[234:237], v[66:69]
	v_mfma_f32_16x16x32_bf16 v[62:65], v[106:109], v[234:237], v[62:65]
	v_mfma_f32_16x16x32_bf16 v[42:45], v[98:101], v[238:241], v[42:45]
	v_mfma_f32_16x16x32_bf16 v[38:41], v[106:109], v[238:241], v[38:41]
	s_setprio 0
	s_setprio 1
	v_mfma_f32_16x16x32_bf16 v[74:77], v[168:171], v[210:213], v[74:77]
	v_mfma_f32_16x16x32_bf16 v[98:101], v[172:175], v[218:221], v[74:77]
	v_mfma_f32_16x16x32_bf16 v[74:77], v[168:171], v[214:217], v[78:81]
	v_mfma_f32_16x16x32_bf16 v[70:73], v[176:179], v[210:213], v[70:73]
	v_mfma_f32_16x16x32_bf16 v[90:93], v[172:175], v[222:225], v[74:77]
	v_mfma_f32_16x16x32_bf16 v[74:77], v[176:179], v[214:217], v[86:89]
	v_mfma_f32_16x16x32_bf16 v[54:57], v[168:171], v[226:229], v[54:57]
	v_mfma_f32_16x16x32_bf16 v[50:53], v[176:179], v[226:229], v[50:53]
	v_mfma_f32_16x16x32_bf16 v[6:9], v[168:171], v[230:233], v[6:9]
	v_mfma_f32_16x16x32_bf16 v[2:5], v[176:179], v[230:233], v[2:5]
	v_mfma_f32_16x16x32_bf16 v[70:73], v[180:183], v[218:221], v[70:73]
	v_mfma_f32_16x16x32_bf16 v[86:89], v[180:183], v[222:225], v[74:77]
	v_mfma_f32_16x16x32_bf16 v[54:57], v[172:175], v[234:237], v[54:57]
	v_mfma_f32_16x16x32_bf16 v[50:53], v[180:183], v[234:237], v[50:53]
	v_mfma_f32_16x16x32_bf16 v[6:9], v[172:175], v[238:241], v[6:9]
	v_mfma_f32_16x16x32_bf16 v[2:5], v[180:183], v[238:241], v[2:5]
	s_setprio 0
	s_waitcnt vmcnt(8)
	s_barrier
	s_add_i32 s45, s45, 2
	s_add_u32 s37, s37, 0x8000
	s_addc_u32 s44, s44, 0
	s_add_u32 s0, s0, 0x100
	s_addc_u32 s1, s1, 0
	s_cmp_gt_u32 s45, 29
	s_cbranch_scc0 .LBB0_1934
	s_and_b64 vcc, exec, s[18:19]
	s_cbranch_vccz .LBB0_1937
	s_barrier

; #define PG8_STAGE(bufoff, gbase, voff) do { _Pragma("unroll") for (int _i = 0; _i < 2; ++_i) \
;         __builtin_amdgcn_global_load_lds((const unsigned*)((const char*)(gbase) + (voff)[_i]), (LAS unsigned*)(lds + (bufoff) + ldsw + _i * 8192), 16, 0, 0); } while (0)
; #define PG8_LDA(dst, b, h) do { _Pragma("unroll") for (int m = 0; m < 4; ++m) _Pragma("unroll") for (int k = 0; k < 2; ++k) dst[m][k] = *(const LAS bf16x8*)(lds + PG8_SA(b, h) + ((aoff ^ (k * 64)) + m * 2048)); } while (0)
; #define PG8_LDB(dst, b, h) do { _Pragma("unroll") for (int n = 0; n < 2; ++n) _Pragma("unroll") for (int k = 0; k < 2; ++k) dst[n][k] = *(const LAS bf16x8*)(lds + PG8_SB(b, h) + ((boff ^ (k * 64)) + n * 2048)); } while (0)
; #define PG8_BAR __builtin_amdgcn_s_barrier()
;     ...
;             const bool last = (t == nt - 2);
;             const char* a1 = cA + (size_t)(t + 1) * kstepA;
;             const char* a2 = last ? nA : cA + (size_t)(t + 2) * kstepA; const char* b2 = last ? nB : cB + (size_t)(t + 2) * kstepB;
;             const char* a3 = a2 + kstepA; const char* b3 = b2 + kstepB;
;             unsigned vs[2][2];
;             if constexpr (GATHER) {
;                 if (last && has_next) {
; #pragma unroll
;                     for (int hh = 0; hh < 2; ++hh)
; #pragma unroll
;                         for (int i = 0; i < 2; ++i) voffN[hh][i] = (unsigned)idxl[(ui + 1) * 256 + hh * HALF + sR[i]] * (unsigned)(K * 2) + (unsigned)sC[i] * 2u;
;                 }
; #pragma unroll
;                 for (int hh = 0; hh < 2; ++hh)
; #pragma unroll
;                     for (int i = 0; i < 2; ++i) vs[hh][i] = last ? voffN[hh][i] : voffA[hh][i];
;             } else {
; #pragma unroll
;                 for (int hh = 0; hh < 2; ++hh)
; #pragma unroll
;                     for (int i = 0; i < 2; ++i) vs[hh][i] = voffA[hh][i];
;             }
;             PG8_LDB(B0, 0, 0); PG8_LDB(B1, 0, 1); PG8_SCHED; PG8_LDA(At, 0, 0); PG8_STAGE(PG8_SA(1, 1), a1, voffA[1]);
;             PG8_WAIT_V(8); PG8_WAIT_L(0); PG8_BAR; if (do0) { PG8_MMA(0, 0, At, B0); PG8_MMA(0, 1, At, B1); } PG8_BAR; PG8_SCHED;
;             PG8_LDA(At, 0, 1); PG8_STAGE(PG8_SB(0, 0), b2, voffB); PG8_STAGE(PG8_SB(0, 1), b2 + hstep, voffB); PG8_STAGE(PG8_SA(0, 0), a2, vs[0]);
;             PG8_WAIT_V(8); PG8_WAIT_L(0); PG8_BAR; if (do1) { PG8_MMA(1, 0, At, B0); PG8_MMA(1, 1, At, B1); } PG8_BAR; PG8_SCHED;
.LBB0_2337:
	v_add_u32_e32 v136, s43, v159
	v_add_u32_e32 v145, s43, v160
	ds_read_b128 v[166:169], v136
	ds_read_b128 v[170:173], v145
	v_add_u32_e32 v136, s44, v159
	s_add_u32 s22, s90, s20
	v_add_u32_e32 v145, s44, v160
	ds_read_b128 v[174:177], v136
	ds_read_b128 v[178:181], v145
	v_add_u32_e32 v136, s45, v159
	s_addc_u32 s23, s91, s21
	v_add_u32_e32 v145, s45, v160
	ds_read_b128 v[182:185], v136
	ds_read_b128 v[186:189], v145
	v_add_u32_e32 v136, s46, v159
	s_add_u32 s24, s22, 0x4213700
	v_add_u32_e32 v145, s46, v160
	ds_read_b128 v[190:193], v136
	ds_read_b128 v[194:197], v145
	s_addc_u32 s25, s23, 0
	s_and_b64 s[22:23], s[2:3], exec
	s_cselect_b32 s22, s14, s13
	s_cselect_b32 s27, s83, s25
	s_cselect_b32 s26, s82, s24
	s_cselect_b32 s23, s15, s53
	s_add_u32 s24, s22, 0x4000
	s_addc_u32 s25, s23, 0
	v_cndmask_b32_e64 v136, v152, v146, s[2:3]
	v_cndmask_b32_e64 v232, v153, v147, s[2:3]
	v_cndmask_b32_e64 v145, v148, v164, s[2:3]
	v_cndmask_b32_e64 v149, v150, v165, s[2:3]
	v_lshl_add_u64 v[234:235], v[156:157], 0, s[20:21]
	s_add_i32 m0, s17, 0xc000
	ds_read_b128 v[200:203], v161
	ds_read_b128 v[204:207], v161 offset:2048
	ds_read_b128 v[208:211], v162
	ds_read_b128 v[212:215], v162 offset:2048
	ds_read_b128 v[216:219], v161 offset:4096
	ds_read_b128 v[220:223], v161 offset:6144
	ds_read_b128 v[224:227], v162 offset:4096
	ds_read_b128 v[228:231], v162 offset:6144
	global_load_lds_dwordx4 v[234:235], off
	v_lshl_add_u64 v[234:235], v[154:155], 0, s[20:21]
	s_add_i32 m0, s17, 0xe000
	s_nop 0
	global_load_lds_dwordx4 v[234:235], off
	s_bitcmp1_b32 s4, 0
	s_cbranch_scc0 .Lwm_guL1_0
	s_waitcnt vmcnt(8)
.Lwm_guL1_0:
	s_waitcnt lgkmcnt(0)
	s_barrier
	s_setprio 1
	s_waitcnt lgkmcnt(0)
	v_mfma_f32_16x16x32_bf16 v[126:129], v[166:169], v[200:203], v[126:129]
	v_mfma_f32_16x16x32_bf16 v[122:125], v[174:177], v[200:203], v[122:125]
	v_mfma_f32_16x16x32_bf16 v[110:113], v[166:169], v[204:207], v[110:113]
	v_mfma_f32_16x16x32_bf16 v[106:109], v[174:177], v[204:207], v[106:109]
	v_mfma_f32_16x16x32_bf16 v[94:97], v[166:169], v[216:219], v[94:97]
	v_mfma_f32_16x16x32_bf16 v[90:93], v[174:177], v[216:219], v[90:93]
	v_mfma_f32_16x16x32_bf16 v[78:81], v[166:169], v[220:223], v[78:81]
	v_mfma_f32_16x16x32_bf16 v[74:77], v[174:177], v[220:223], v[74:77]
	v_mfma_f32_16x16x32_bf16 v[126:129], v[170:173], v[208:211], v[126:129]
	v_mfma_f32_16x16x32_bf16 v[122:125], v[178:181], v[208:211], v[122:125]
	v_mfma_f32_16x16x32_bf16 v[110:113], v[170:173], v[212:215], v[110:113]
	v_mfma_f32_16x16x32_bf16 v[106:109], v[178:181], v[212:215], v[106:109]
	v_mfma_f32_16x16x32_bf16 v[94:97], v[170:173], v[224:227], v[94:97]
	v_mfma_f32_16x16x32_bf16 v[90:93], v[178:181], v[224:227], v[90:93]
	v_mfma_f32_16x16x32_bf16 v[78:81], v[170:173], v[228:231], v[78:81]
	v_mfma_f32_16x16x32_bf16 v[74:77], v[178:181], v[228:231], v[74:77]
	s_setprio 0
	s_setprio 1
	v_mfma_f32_16x16x32_bf16 v[118:121], v[182:185], v[200:203], v[118:121]
	v_mfma_f32_16x16x32_bf16 v[114:117], v[190:193], v[200:203], v[114:117]
	v_mfma_f32_16x16x32_bf16 v[102:105], v[182:185], v[204:207], v[102:105]
	v_mfma_f32_16x16x32_bf16 v[98:101], v[190:193], v[204:207], v[98:101]
	v_mfma_f32_16x16x32_bf16 v[86:89], v[182:185], v[216:219], v[86:89]
	v_mfma_f32_16x16x32_bf16 v[82:85], v[190:193], v[216:219], v[82:85]
	v_mfma_f32_16x16x32_bf16 v[70:73], v[182:185], v[220:223], v[70:73]
	v_mfma_f32_16x16x32_bf16 v[66:69], v[190:193], v[220:223], v[66:69]
	v_mfma_f32_16x16x32_bf16 v[118:121], v[186:189], v[208:211], v[118:121]
	v_mfma_f32_16x16x32_bf16 v[114:117], v[194:197], v[208:211], v[114:117]
	v_mfma_f32_16x16x32_bf16 v[102:105], v[186:189], v[212:215], v[102:105]
	v_mfma_f32_16x16x32_bf16 v[98:101], v[194:197], v[212:215], v[98:101]
	v_mfma_f32_16x16x32_bf16 v[86:89], v[186:189], v[224:227], v[86:89]
	v_mfma_f32_16x16x32_bf16 v[82:85], v[194:197], v[224:227], v[82:85]
	v_mfma_f32_16x16x32_bf16 v[70:73], v[186:189], v[228:231], v[70:73]
	v_mfma_f32_16x16x32_bf16 v[66:69], v[194:197], v[228:231], v[66:69]
	s_setprio 0
	s_waitcnt vmcnt(8)
	s_barrier
	s_add_i32 s2, s43, s34
	v_lshl_add_u64 v[234:235], s[22:23], 0, v[132:133]
	s_mov_b32 m0, s2
	ds_read_b128 v[200:203], v161 offset:16384
	ds_read_b128 v[204:207], v161 offset:18432
	ds_read_b128 v[208:211], v162 offset:16384
	ds_read_b128 v[212:215], v162 offset:18432
	ds_read_b128 v[216:219], v161 offset:20480
	ds_read_b128 v[220:223], v161 offset:22528
	ds_read_b128 v[224:227], v162 offset:20480
	ds_read_b128 v[228:231], v162 offset:22528
	global_load_lds_dwordx4 v[234:235], off
	s_add_i32 m0, s2, 0x2000
	s_add_u32 s2, s22, 0x40000
	v_lshl_add_u64 v[234:235], s[22:23], 0, v[134:135]
	s_addc_u32 s3, s23, 0
	s_add_i32 s55, s45, s34
	global_load_lds_dwordx4 v[234:235], off
	v_lshl_add_u64 v[234:235], s[2:3], 0, v[132:133]
	s_mov_b32 m0, s55
	v_mov_b32_e32 v233, v137
	global_load_lds_dwordx4 v[234:235], off
	v_lshl_add_u64 v[234:235], s[2:3], 0, v[134:135]
	s_add_i32 m0, s55, 0x2000
	s_nop 0
	global_load_lds_dwordx4 v[234:235], off
	s_mov_b32 m0, s17
	v_lshl_add_u64 v[234:235], s[26:27], 0, v[136:137]
	global_load_lds_dwordx4 v136, s[26:27]
	s_mov_b32 m0, s35
	s_nop 0
	global_load_lds_dwordx4 v232, s[26:27]
	s_bitcmp1_b32 s4, 0
	s_cbranch_scc0 .Lwm_guL1_1
	s_waitcnt vmcnt(8)
; #define PG8_STAGE(bufoff, gbase, voff) do { _Pragma("unroll") for (int _i = 0; _i < 2; ++_i) \
;         __builtin_amdgcn_global_load_lds((const unsigned*)((const char*)(gbase) + (voff)[_i]), (LAS unsigned*)(lds + (bufoff) + ldsw + _i * 8192), 16, 0, 0); } while (0)
; #define PG8_LDA(dst, b, h) do { _Pragma("unroll") for (int m = 0; m < 4; ++m) _Pragma("unroll") for (int k = 0; k < 2; ++k) dst[m][k] = *(const LAS bf16x8*)(lds + PG8_SA(b, h) + ((aoff ^ (k * 64)) + m * 2048)); } while (0)
; #define PG8_LDB(dst, b, h) do { _Pragma("unroll") for (int n = 0; n < 2; ++n) _Pragma("unroll") for (int k = 0; k < 2; ++k) dst[n][k] = *(const LAS bf16x8*)(lds + PG8_SB(b, h) + ((boff ^ (k * 64)) + n * 2048)); } while (0)
; #define PG8_MMA(ai, bj, At, Bt) do { __builtin_amdgcn_s_setprio(1); _Pragma("unroll") for (int m = 0; m < 4; ++m) _Pragma("unroll") for (int n = 0; n < 2; ++n) _Pragma("unroll") for (int k = 0; k < 2; ++k) \
;         acc[ai][bj][m][n] = __builtin_amdgcn_mfma_f32_16x16x32_bf16(Bt[n][k], At[m][k], acc[ai][bj][m][n], 0, 0, 0); __builtin_amdgcn_s_setprio(0); } while (0)
; #define PG8_WAIT_V(n) asm volatile("s_waitcnt vmcnt(" #n ")" ::: "memory")
; #define PG8_WAIT_L(n) asm volatile("s_waitcnt lgkmcnt(" #n ")" ::: "memory")
; #define PG8_BAR __builtin_amdgcn_s_barrier()
; #define PG8_SCHED __builtin_amdgcn_sched_barrier(0)
;     ...
;             PG8_WAIT_V(8); PG8_WAIT_L(0); PG8_BAR; if (do1) { PG8_MMA(1, 0, At, B0); PG8_MMA(1, 1, At, B1); } PG8_BAR; PG8_SCHED;
;             PG8_LDB(B0, 1, 0); PG8_LDB(B1, 1, 1); PG8_SCHED; PG8_LDA(At, 1, 0); PG8_STAGE(PG8_SA(0, 1), a2, vs[1]);
;             PG8_WAIT_V(8); PG8_WAIT_L(0); PG8_BAR; if (do0) { PG8_MMA(0, 0, At, B0); PG8_MMA(0, 1, At, B1); } PG8_BAR; PG8_SCHED;
.Lwm_guL1_1:
	s_waitcnt lgkmcnt(0)
	v_lshl_add_u64 v[232:233], s[26:27], 0, v[232:233]
	s_barrier
	s_setprio 1
	s_waitcnt lgkmcnt(0)
	v_mfma_f32_16x16x32_bf16 v[62:65], v[166:169], v[200:203], v[62:65]
	v_mfma_f32_16x16x32_bf16 v[58:61], v[174:177], v[200:203], v[58:61]
	v_mfma_f32_16x16x32_bf16 v[46:49], v[166:169], v[204:207], v[46:49]
	v_mfma_f32_16x16x32_bf16 v[42:45], v[174:177], v[204:207], v[42:45]
	v_mfma_f32_16x16x32_bf16 v[30:33], v[166:169], v[216:219], v[30:33]
	v_mfma_f32_16x16x32_bf16 v[26:29], v[174:177], v[216:219], v[26:29]
	v_mfma_f32_16x16x32_bf16 v[14:17], v[166:169], v[220:223], v[14:17]
	v_mfma_f32_16x16x32_bf16 v[10:13], v[174:177], v[220:223], v[10:13]
	v_mfma_f32_16x16x32_bf16 v[62:65], v[170:173], v[208:211], v[62:65]
	v_mfma_f32_16x16x32_bf16 v[58:61], v[178:181], v[208:211], v[58:61]
	v_mfma_f32_16x16x32_bf16 v[46:49], v[170:173], v[212:215], v[46:49]
	v_mfma_f32_16x16x32_bf16 v[42:45], v[178:181], v[212:215], v[42:45]
	v_mfma_f32_16x16x32_bf16 v[30:33], v[170:173], v[224:227], v[30:33]
	v_mfma_f32_16x16x32_bf16 v[26:29], v[178:181], v[224:227], v[26:29]
	v_mfma_f32_16x16x32_bf16 v[14:17], v[170:173], v[228:231], v[14:17]
	v_mfma_f32_16x16x32_bf16 v[10:13], v[178:181], v[228:231], v[10:13]
	s_setprio 0
	s_setprio 1
	v_mfma_f32_16x16x32_bf16 v[54:57], v[182:185], v[200:203], v[54:57]
	v_mfma_f32_16x16x32_bf16 v[50:53], v[190:193], v[200:203], v[50:53]
	v_mfma_f32_16x16x32_bf16 v[38:41], v[182:185], v[204:207], v[38:41]
	v_mfma_f32_16x16x32_bf16 v[34:37], v[190:193], v[204:207], v[34:37]
	v_mfma_f32_16x16x32_bf16 v[22:25], v[182:185], v[216:219], v[22:25]
	v_mfma_f32_16x16x32_bf16 v[18:21], v[190:193], v[216:219], v[18:21]
	v_mfma_f32_16x16x32_bf16 v[6:9], v[182:185], v[220:223], v[6:9]
	v_mfma_f32_16x16x32_bf16 v[2:5], v[190:193], v[220:223], v[2:5]
	v_mfma_f32_16x16x32_bf16 v[54:57], v[186:189], v[208:211], v[54:57]
	v_mfma_f32_16x16x32_bf16 v[50:53], v[194:197], v[208:211], v[50:53]
	v_mfma_f32_16x16x32_bf16 v[38:41], v[186:189], v[212:215], v[38:41]
	v_mfma_f32_16x16x32_bf16 v[34:37], v[194:197], v[212:215], v[34:37]
	v_mfma_f32_16x16x32_bf16 v[22:25], v[186:189], v[224:227], v[22:25]
	v_mfma_f32_16x16x32_bf16 v[18:21], v[194:197], v[224:227], v[18:21]
	v_mfma_f32_16x16x32_bf16 v[6:9], v[186:189], v[228:231], v[6:9]
	v_mfma_f32_16x16x32_bf16 v[2:5], v[194:197], v[228:231], v[2:5]
	s_setprio 0
	s_waitcnt vmcnt(8)
	s_barrier
	s_add_i32 s2, 0, 0x18000
	v_add_u32_e32 v136, s2, v159
	v_add_u32_e32 v151, s2, v160
	ds_read_b128 v[166:169], v136
	ds_read_b128 v[170:173], v151
	v_add_u32_e32 v136, s47, v159
	s_add_i32 s55, 0, 0x1c000
	v_add_u32_e32 v151, s47, v160
	ds_read_b128 v[174:177], v136
	ds_read_b128 v[178:181], v151
	v_add_u32_e32 v136, s55, v159
	v_add_u32_e32 v151, s55, v160
	ds_read_b128 v[182:185], v136
	ds_read_b128 v[186:189], v151
	v_add_u32_e32 v136, s48, v159
	v_add_u32_e32 v151, s48, v160
	ds_read_b128 v[190:193], v136
	ds_read_b128 v[194:197], v151
	s_mov_b32 m0, s36
	ds_read_b128 v[200:203], v161 offset:32768
	ds_read_b128 v[204:207], v161 offset:34816
	ds_read_b128 v[208:211], v162 offset:32768
	ds_read_b128 v[212:215], v162 offset:34816
	ds_read_b128 v[216:219], v161 offset:36864
	ds_read_b128 v[220:223], v161 offset:38912
	ds_read_b128 v[224:227], v162 offset:36864
	ds_read_b128 v[228:231], v162 offset:38912
	global_load_lds_dwordx4 v145, s[26:27]
	s_mov_b32 m0, s37
	s_nop 0
	global_load_lds_dwordx4 v149, s[26:27]
	s_bitcmp1_b32 s4, 0
	s_cbranch_scc0 .Lwm_guL1_2
	s_waitcnt vmcnt(8)
; #define PG8_STAGE(bufoff, gbase, voff) do { _Pragma("unroll") for (int _i = 0; _i < 2; ++_i) \
;         __builtin_amdgcn_global_load_lds((const unsigned*)((const char*)(gbase) + (voff)[_i]), (LAS unsigned*)(lds + (bufoff) + ldsw + _i * 8192), 16, 0, 0); } while (0)
; #define PG8_LDA(dst, b, h) do { _Pragma("unroll") for (int m = 0; m < 4; ++m) _Pragma("unroll") for (int k = 0; k < 2; ++k) dst[m][k] = *(const LAS bf16x8*)(lds + PG8_SA(b, h) + ((aoff ^ (k * 64)) + m * 2048)); } while (0)
; #define PG8_MMA(ai, bj, At, Bt) do { __builtin_amdgcn_s_setprio(1); _Pragma("unroll") for (int m = 0; m < 4; ++m) _Pragma("unroll") for (int n = 0; n < 2; ++n) _Pragma("unroll") for (int k = 0; k < 2; ++k) \
;         acc[ai][bj][m][n] = __builtin_amdgcn_mfma_f32_16x16x32_bf16(Bt[n][k], At[m][k], acc[ai][bj][m][n], 0, 0, 0); __builtin_amdgcn_s_setprio(0); } while (0)
; #define PG8_WAIT_V(n) asm volatile("s_waitcnt vmcnt(" #n ")" ::: "memory")
; #define PG8_WAIT_L(n) asm volatile("s_waitcnt lgkmcnt(" #n ")" ::: "memory")
; #define PG8_BAR __builtin_amdgcn_s_barrier()
; #define PG8_SCHED __builtin_amdgcn_sched_barrier(0)
;     ...
;             PG8_WAIT_V(8); PG8_WAIT_L(0); PG8_BAR; if (do0) { PG8_MMA(0, 0, At, B0); PG8_MMA(0, 1, At, B1); } PG8_BAR; PG8_SCHED;
;             PG8_LDA(At, 1, 1); PG8_STAGE(PG8_SB(1, 0), b3, voffB); PG8_STAGE(PG8_SB(1, 1), b3 + hstep, voffB); PG8_STAGE(PG8_SA(1, 0), a3, vs[0]);
;             PG8_WAIT_V(8); PG8_WAIT_L(0); PG8_BAR; if (do1) { PG8_MMA(1, 0, At, B0); PG8_MMA(1, 1, At, B1); } PG8_BAR; PG8_SCHED;
;         }
.Lwm_guL1_2:
	s_waitcnt lgkmcnt(0)
	s_barrier
	s_setprio 1
	s_waitcnt lgkmcnt(0)
	v_mfma_f32_16x16x32_bf16 v[126:129], v[166:169], v[200:203], v[126:129]
	v_mfma_f32_16x16x32_bf16 v[122:125], v[174:177], v[200:203], v[122:125]
	v_mfma_f32_16x16x32_bf16 v[110:113], v[166:169], v[204:207], v[110:113]
	v_mfma_f32_16x16x32_bf16 v[106:109], v[174:177], v[204:207], v[106:109]
	v_mfma_f32_16x16x32_bf16 v[94:97], v[166:169], v[216:219], v[94:97]
	v_mfma_f32_16x16x32_bf16 v[90:93], v[174:177], v[216:219], v[90:93]
	v_mfma_f32_16x16x32_bf16 v[78:81], v[166:169], v[220:223], v[78:81]
	v_mfma_f32_16x16x32_bf16 v[74:77], v[174:177], v[220:223], v[74:77]
	v_mfma_f32_16x16x32_bf16 v[126:129], v[170:173], v[208:211], v[126:129]
	v_mfma_f32_16x16x32_bf16 v[122:125], v[178:181], v[208:211], v[122:125]
	v_mfma_f32_16x16x32_bf16 v[110:113], v[170:173], v[212:215], v[110:113]
	v_mfma_f32_16x16x32_bf16 v[106:109], v[178:181], v[212:215], v[106:109]
	v_mfma_f32_16x16x32_bf16 v[94:97], v[170:173], v[224:227], v[94:97]
	v_mfma_f32_16x16x32_bf16 v[90:93], v[178:181], v[224:227], v[90:93]
	v_mfma_f32_16x16x32_bf16 v[78:81], v[170:173], v[228:231], v[78:81]
	v_mfma_f32_16x16x32_bf16 v[74:77], v[178:181], v[228:231], v[74:77]
	s_setprio 0
	s_setprio 1
	v_mfma_f32_16x16x32_bf16 v[118:121], v[182:185], v[200:203], v[118:121]
	v_mfma_f32_16x16x32_bf16 v[114:117], v[190:193], v[200:203], v[114:117]
	v_mfma_f32_16x16x32_bf16 v[102:105], v[182:185], v[204:207], v[102:105]
	v_mfma_f32_16x16x32_bf16 v[98:101], v[190:193], v[204:207], v[98:101]
	v_mfma_f32_16x16x32_bf16 v[86:89], v[182:185], v[216:219], v[86:89]
	v_mfma_f32_16x16x32_bf16 v[82:85], v[190:193], v[216:219], v[82:85]
	v_mfma_f32_16x16x32_bf16 v[70:73], v[182:185], v[220:223], v[70:73]
	v_mfma_f32_16x16x32_bf16 v[66:69], v[190:193], v[220:223], v[66:69]
	v_mfma_f32_16x16x32_bf16 v[118:121], v[186:189], v[208:211], v[118:121]
	v_mfma_f32_16x16x32_bf16 v[114:117], v[194:197], v[208:211], v[114:117]
	v_mfma_f32_16x16x32_bf16 v[102:105], v[186:189], v[212:215], v[102:105]
	v_mfma_f32_16x16x32_bf16 v[98:101], v[194:197], v[212:215], v[98:101]
	v_mfma_f32_16x16x32_bf16 v[86:89], v[186:189], v[224:227], v[86:89]
	v_mfma_f32_16x16x32_bf16 v[82:85], v[194:197], v[224:227], v[82:85]
	v_mfma_f32_16x16x32_bf16 v[70:73], v[186:189], v[228:231], v[70:73]
	v_mfma_f32_16x16x32_bf16 v[66:69], v[194:197], v[228:231], v[66:69]
	s_setprio 0
	s_waitcnt vmcnt(8)
	s_barrier
	s_add_i32 s2, s2, s34
	v_lshl_add_u64 v[236:237], s[24:25], 0, v[132:133]
	s_mov_b32 m0, s2
	ds_read_b128 v[200:203], v161 offset:49152
	ds_read_b128 v[204:207], v161 offset:51200
	ds_read_b128 v[208:211], v162 offset:49152
	ds_read_b128 v[212:215], v162 offset:51200
	ds_read_b128 v[216:219], v161 offset:53248
	ds_read_b128 v[220:223], v161 offset:55296
	ds_read_b128 v[224:227], v162 offset:53248
	ds_read_b128 v[228:231], v162 offset:55296
	global_load_lds_dwordx4 v[236:237], off
	s_add_i32 m0, s2, 0x2000
	s_add_u32 s2, s22, 0x44000
	v_lshl_add_u64 v[236:237], s[24:25], 0, v[134:135]
	s_addc_u32 s3, s23, 0
	s_add_i32 s22, s55, s34
	global_load_lds_dwordx4 v[236:237], off
	v_lshl_add_u64 v[236:237], s[2:3], 0, v[132:133]
	s_mov_b32 m0, s22
	v_lshl_add_u64 v[234:235], v[234:235], 0, s[10:11]
	global_load_lds_dwordx4 v[236:237], off
	v_lshl_add_u64 v[236:237], s[2:3], 0, v[134:135]
	s_add_i32 m0, s22, 0x2000
	v_lshl_add_u64 v[232:233], v[232:233], 0, s[10:11]
	global_load_lds_dwordx4 v[236:237], off
	s_mov_b32 m0, s41
	s_nop 0
	global_load_lds_dwordx4 v[234:235], off
	s_mov_b32 m0, s42
	s_nop 0
	global_load_lds_dwordx4 v[232:233], off
	s_bitcmp1_b32 s4, 0
	s_cbranch_scc0 .Lwm_guL1_3
	s_waitcnt vmcnt(8)
.Lwm_guL1_3:
	s_waitcnt lgkmcnt(0)
	s_barrier
	s_setprio 1
	s_waitcnt lgkmcnt(0)
	v_mfma_f32_16x16x32_bf16 v[62:65], v[166:169], v[200:203], v[62:65]
	v_mfma_f32_16x16x32_bf16 v[58:61], v[174:177], v[200:203], v[58:61]
	v_mfma_f32_16x16x32_bf16 v[46:49], v[166:169], v[204:207], v[46:49]
	v_mfma_f32_16x16x32_bf16 v[42:45], v[174:177], v[204:207], v[42:45]
	v_mfma_f32_16x16x32_bf16 v[30:33], v[166:169], v[216:219], v[30:33]
	v_mfma_f32_16x16x32_bf16 v[26:29], v[174:177], v[216:219], v[26:29]
	v_mfma_f32_16x16x32_bf16 v[14:17], v[166:169], v[220:223], v[14:17]
	v_mfma_f32_16x16x32_bf16 v[10:13], v[174:177], v[220:223], v[10:13]
	v_mfma_f32_16x16x32_bf16 v[62:65], v[170:173], v[208:211], v[62:65]
	v_mfma_f32_16x16x32_bf16 v[58:61], v[178:181], v[208:211], v[58:61]
	v_mfma_f32_16x16x32_bf16 v[46:49], v[170:173], v[212:215], v[46:49]
	v_mfma_f32_16x16x32_bf16 v[42:45], v[178:181], v[212:215], v[42:45]
	v_mfma_f32_16x16x32_bf16 v[30:33], v[170:173], v[224:227], v[30:33]
	v_mfma_f32_16x16x32_bf16 v[26:29], v[178:181], v[224:227], v[26:29]
	v_mfma_f32_16x16x32_bf16 v[14:17], v[170:173], v[228:231], v[14:17]
	v_mfma_f32_16x16x32_bf16 v[10:13], v[178:181], v[228:231], v[10:13]
	s_setprio 0
	s_setprio 1
	v_mfma_f32_16x16x32_bf16 v[54:57], v[182:185], v[200:203], v[54:57]
	v_mfma_f32_16x16x32_bf16 v[50:53], v[190:193], v[200:203], v[50:53]
	v_mfma_f32_16x16x32_bf16 v[38:41], v[182:185], v[204:207], v[38:41]
	v_mfma_f32_16x16x32_bf16 v[34:37], v[190:193], v[204:207], v[34:37]
	v_mfma_f32_16x16x32_bf16 v[22:25], v[182:185], v[216:219], v[22:25]
	v_mfma_f32_16x16x32_bf16 v[18:21], v[190:193], v[216:219], v[18:21]
	v_mfma_f32_16x16x32_bf16 v[6:9], v[182:185], v[220:223], v[6:9]
	v_mfma_f32_16x16x32_bf16 v[2:5], v[190:193], v[220:223], v[2:5]
	v_mfma_f32_16x16x32_bf16 v[54:57], v[186:189], v[208:211], v[54:57]
	v_mfma_f32_16x16x32_bf16 v[50:53], v[194:197], v[208:211], v[50:53]
	v_mfma_f32_16x16x32_bf16 v[38:41], v[186:189], v[212:215], v[38:41]
	v_mfma_f32_16x16x32_bf16 v[34:37], v[194:197], v[212:215], v[34:37]
	v_mfma_f32_16x16x32_bf16 v[22:25], v[186:189], v[224:227], v[22:25]
	v_mfma_f32_16x16x32_bf16 v[18:21], v[194:197], v[224:227], v[18:21]
	v_mfma_f32_16x16x32_bf16 v[6:9], v[186:189], v[228:231], v[6:9]
	v_mfma_f32_16x16x32_bf16 v[2:5], v[194:197], v[228:231], v[2:5]
	s_setprio 0
	s_waitcnt vmcnt(8)
	s_barrier
	s_add_i32 s54, s54, 2
	s_add_u32 s13, s13, 0x8000
	s_addc_u32 s53, s53, 0
	s_add_u32 s20, s20, 0x100
	s_addc_u32 s21, s21, 0
	s_cmp_gt_u32 s54, 13
	s_cbranch_scc1 .LBB0_2340

; #define PG8_STAGE(bufoff, gbase, voff) do { _Pragma("unroll") for (int _i = 0; _i < 2; ++_i) \
;         __builtin_amdgcn_global_load_lds((const unsigned*)((const char*)(gbase) + (voff)[_i]), (LAS unsigned*)(lds + (bufoff) + ldsw + _i * 8192), 16, 0, 0); } while (0)
; #define PG8_LDA(dst, b, h) do { _Pragma("unroll") for (int m = 0; m < 4; ++m) _Pragma("unroll") for (int k = 0; k < 2; ++k) dst[m][k] = *(const LAS bf16x8*)(lds + PG8_SA(b, h) + ((aoff ^ (k * 64)) + m * 2048)); } while (0)
; #define PG8_LDB(dst, b, h) do { _Pragma("unroll") for (int n = 0; n < 2; ++n) _Pragma("unroll") for (int k = 0; k < 2; ++k) dst[n][k] = *(const LAS bf16x8*)(lds + PG8_SB(b, h) + ((boff ^ (k * 64)) + n * 2048)); } while (0)
;     ...
;         for (int t = 0; t < nt; t += 2) {
;             const bool last = (t == nt - 2);
;             const char* a1 = cA + (size_t)(t + 1) * kstepA;
;             const char* a2 = last ? nA : cA + (size_t)(t + 2) * kstepA; const char* b2 = last ? nB : cB + (size_t)(t + 2) * kstepB;
;             const char* a3 = a2 + kstepA; const char* b3 = b2 + kstepB;
;             unsigned vs[2][2];
;             if constexpr (GATHER) {
;                 if (last && has_next) {
; #pragma unroll
;                     for (int hh = 0; hh < 2; ++hh)
; #pragma unroll
;                         for (int i = 0; i < 2; ++i) voffN[hh][i] = (unsigned)idxl[(ui + 1) * 256 + hh * HALF + sR[i]] * (unsigned)(K * 2) + (unsigned)sC[i] * 2u;
;                 }
; #pragma unroll
;                 for (int hh = 0; hh < 2; ++hh)
; #pragma unroll
;                     for (int i = 0; i < 2; ++i) vs[hh][i] = last ? voffN[hh][i] : voffA[hh][i];
;             } else {
; #pragma unroll
;                 for (int hh = 0; hh < 2; ++hh)
; #pragma unroll
;                     for (int i = 0; i < 2; ++i) vs[hh][i] = voffA[hh][i];
;             }
;             PG8_LDB(B0, 0, 0); PG8_LDB(B1, 0, 1); PG8_SCHED; PG8_LDA(At, 0, 0); PG8_STAGE(PG8_SA(1, 1), a1, voffA[1]);
;             PG8_WAIT_V(8); PG8_WAIT_L(0); PG8_BAR; if (do0) { PG8_MMA(0, 0, At, B0); PG8_MMA(0, 1, At, B1); } PG8_BAR; PG8_SCHED;
;             PG8_LDA(At, 0, 1); PG8_STAGE(PG8_SB(0, 0), b2, voffB); PG8_STAGE(PG8_SB(0, 1), b2 + hstep, voffB); PG8_STAGE(PG8_SA(0, 0), a2, vs[0]);
;             PG8_WAIT_V(8); PG8_WAIT_L(0); PG8_BAR; if (do1) { PG8_MMA(1, 0, At, B0); PG8_MMA(1, 1, At, B1); } PG8_BAR; PG8_SCHED;
.LBB0_2411:
	ds_read_b128 v[146:149], v153
	ds_read_b128 v[168:171], v154
	ds_read_b128 v[172:175], v155
	ds_read_b128 v[176:179], v156
	ds_read_b128 v[180:183], v157
	ds_read_b128 v[184:187], v158
	ds_read_b128 v[188:191], v159
	ds_read_b128 v[192:195], v160
	s_add_u32 s20, s18, 0x4000
	s_addc_u32 s21, s19, 0
	s_cmp_eq_u32 s56, 40
	s_cselect_b32 s26, s14, s20
	s_cselect_b32 s27, s15, s21
	s_cselect_b32 s22, s16, s54
	s_cselect_b32 s23, s17, s55
	s_add_u32 s20, s26, 0x4000
	s_addc_u32 s21, s27, 0
	v_lshl_add_u64 v[196:197], s[18:19], 0, v[142:143]
	s_add_i32 m0, s34, 0xc000
	ds_read_b128 v[200:203], v161
	ds_read_b128 v[204:207], v161 offset:2048
	ds_read_b128 v[208:211], v162
	ds_read_b128 v[212:215], v162 offset:2048
	ds_read_b128 v[216:219], v161 offset:4096
	ds_read_b128 v[220:223], v161 offset:6144
	ds_read_b128 v[224:227], v162 offset:4096
	ds_read_b128 v[228:231], v162 offset:6144
	global_load_lds_dwordx4 v[196:197], off
	v_lshl_add_u64 v[196:197], s[18:19], 0, v[144:145]
	s_add_i32 m0, s34, 0xe000
	s_add_u32 s24, s22, 0x4000
	global_load_lds_dwordx4 v[196:197], off
	s_mov_b64 vcc, s[2:3]
	s_cbranch_vccz .Lwm_dnL1_0
	s_waitcnt vmcnt(8)
.Lwm_dnL1_0:
	s_waitcnt lgkmcnt(0)
	s_addc_u32 s25, s23, 0
	s_barrier
	s_setprio 1
	s_waitcnt lgkmcnt(0)
	v_mfma_f32_16x16x32_bf16 v[126:129], v[146:149], v[200:203], v[126:129]
	v_mfma_f32_16x16x32_bf16 v[122:125], v[172:175], v[200:203], v[122:125]
	v_mfma_f32_16x16x32_bf16 v[114:117], v[146:149], v[204:207], v[114:117]
	v_mfma_f32_16x16x32_bf16 v[106:109], v[172:175], v[204:207], v[106:109]
	v_mfma_f32_16x16x32_bf16 v[98:101], v[146:149], v[216:219], v[98:101]
	v_mfma_f32_16x16x32_bf16 v[90:93], v[172:175], v[216:219], v[90:93]
	v_mfma_f32_16x16x32_bf16 v[82:85], v[146:149], v[220:223], v[82:85]
	v_mfma_f32_16x16x32_bf16 v[74:77], v[172:175], v[220:223], v[74:77]
	v_mfma_f32_16x16x32_bf16 v[126:129], v[168:171], v[208:211], v[126:129]
	v_mfma_f32_16x16x32_bf16 v[122:125], v[176:179], v[208:211], v[122:125]
	v_mfma_f32_16x16x32_bf16 v[114:117], v[168:171], v[212:215], v[114:117]
	v_mfma_f32_16x16x32_bf16 v[106:109], v[176:179], v[212:215], v[106:109]
	v_mfma_f32_16x16x32_bf16 v[98:101], v[168:171], v[224:227], v[98:101]
	v_mfma_f32_16x16x32_bf16 v[90:93], v[176:179], v[224:227], v[90:93]
	v_mfma_f32_16x16x32_bf16 v[82:85], v[168:171], v[228:231], v[82:85]
	v_mfma_f32_16x16x32_bf16 v[74:77], v[176:179], v[228:231], v[74:77]
	s_setprio 0
	s_setprio 1
	v_mfma_f32_16x16x32_bf16 v[118:121], v[180:183], v[200:203], v[118:121]
	v_mfma_f32_16x16x32_bf16 v[110:113], v[188:191], v[200:203], v[110:113]
	v_mfma_f32_16x16x32_bf16 v[102:105], v[180:183], v[204:207], v[102:105]
	v_mfma_f32_16x16x32_bf16 v[94:97], v[188:191], v[204:207], v[94:97]
	v_mfma_f32_16x16x32_bf16 v[86:89], v[180:183], v[216:219], v[86:89]
	v_mfma_f32_16x16x32_bf16 v[78:81], v[188:191], v[216:219], v[78:81]
	v_mfma_f32_16x16x32_bf16 v[70:73], v[180:183], v[220:223], v[70:73]
	v_mfma_f32_16x16x32_bf16 v[66:69], v[188:191], v[220:223], v[66:69]
	v_mfma_f32_16x16x32_bf16 v[118:121], v[184:187], v[208:211], v[118:121]
	v_mfma_f32_16x16x32_bf16 v[110:113], v[192:195], v[208:211], v[110:113]
	v_mfma_f32_16x16x32_bf16 v[102:105], v[184:187], v[212:215], v[102:105]
	v_mfma_f32_16x16x32_bf16 v[94:97], v[192:195], v[212:215], v[94:97]
	v_mfma_f32_16x16x32_bf16 v[86:89], v[184:187], v[224:227], v[86:89]
	v_mfma_f32_16x16x32_bf16 v[78:81], v[192:195], v[224:227], v[78:81]
	v_mfma_f32_16x16x32_bf16 v[70:73], v[184:187], v[228:231], v[70:73]
	v_mfma_f32_16x16x32_bf16 v[66:69], v[192:195], v[228:231], v[66:69]
	s_setprio 0
	s_waitcnt vmcnt(8)
	s_barrier
	s_add_i32 s57, s42, s30
	v_lshl_add_u64 v[196:197], s[22:23], 0, v[132:133]
	s_mov_b32 m0, s57
	ds_read_b128 v[200:203], v161 offset:16384
	ds_read_b128 v[204:207], v161 offset:18432
	ds_read_b128 v[208:211], v162 offset:16384
	ds_read_b128 v[212:215], v162 offset:18432
	ds_read_b128 v[216:219], v161 offset:20480
	ds_read_b128 v[220:223], v161 offset:22528
	ds_read_b128 v[224:227], v162 offset:20480
	ds_read_b128 v[228:231], v162 offset:22528
	global_load_lds_dwordx4 v[196:197], off
	s_add_i32 m0, s57, 0x2000
	s_add_u32 s58, s22, 0xb0000
	v_lshl_add_u64 v[196:197], s[22:23], 0, v[130:131]
	s_addc_u32 s59, s23, 0
	s_add_i32 s57, s43, s30
	global_load_lds_dwordx4 v[196:197], off
	v_lshl_add_u64 v[196:197], s[58:59], 0, v[132:133]
	s_mov_b32 m0, s57
	s_nop 0
	global_load_lds_dwordx4 v[196:197], off
	v_lshl_add_u64 v[196:197], s[58:59], 0, v[130:131]
	s_add_i32 m0, s57, 0x2000
	s_nop 0
	global_load_lds_dwordx4 v[196:197], off
	v_lshl_add_u64 v[196:197], s[26:27], 0, v[134:135]
	s_mov_b32 m0, s34
	s_nop 0
	global_load_lds_dwordx4 v[196:197], off
	v_lshl_add_u64 v[196:197], s[26:27], 0, v[136:137]
	s_mov_b32 m0, s35
	s_nop 0
	global_load_lds_dwordx4 v[196:197], off
	s_bitcmp1_b32 s2, 0
	s_cbranch_scc0 .Lwm_dnL1_1
	s_waitcnt vmcnt(8)
; #define PG8_STAGE(bufoff, gbase, voff) do { _Pragma("unroll") for (int _i = 0; _i < 2; ++_i) \
;         __builtin_amdgcn_global_load_lds((const unsigned*)((const char*)(gbase) + (voff)[_i]), (LAS unsigned*)(lds + (bufoff) + ldsw + _i * 8192), 16, 0, 0); } while (0)
; #define PG8_LDA(dst, b, h) do { _Pragma("unroll") for (int m = 0; m < 4; ++m) _Pragma("unroll") for (int k = 0; k < 2; ++k) dst[m][k] = *(const LAS bf16x8*)(lds + PG8_SA(b, h) + ((aoff ^ (k * 64)) + m * 2048)); } while (0)
; #define PG8_LDB(dst, b, h) do { _Pragma("unroll") for (int n = 0; n < 2; ++n) _Pragma("unroll") for (int k = 0; k < 2; ++k) dst[n][k] = *(const LAS bf16x8*)(lds + PG8_SB(b, h) + ((boff ^ (k * 64)) + n * 2048)); } while (0)
; #define PG8_MMA(ai, bj, At, Bt) do { __builtin_amdgcn_s_setprio(1); _Pragma("unroll") for (int m = 0; m < 4; ++m) _Pragma("unroll") for (int n = 0; n < 2; ++n) _Pragma("unroll") for (int k = 0; k < 2; ++k) \
;         acc[ai][bj][m][n] = __builtin_amdgcn_mfma_f32_16x16x32_bf16(Bt[n][k], At[m][k], acc[ai][bj][m][n], 0, 0, 0); __builtin_amdgcn_s_setprio(0); } while (0)
; #define PG8_WAIT_V(n) asm volatile("s_waitcnt vmcnt(" #n ")" ::: "memory")
; #define PG8_WAIT_L(n) asm volatile("s_waitcnt lgkmcnt(" #n ")" ::: "memory")
; #define PG8_BAR __builtin_amdgcn_s_barrier()
; #define PG8_SCHED __builtin_amdgcn_sched_barrier(0)
;     ...
;             PG8_WAIT_V(8); PG8_WAIT_L(0); PG8_BAR; if (do1) { PG8_MMA(1, 0, At, B0); PG8_MMA(1, 1, At, B1); } PG8_BAR; PG8_SCHED;
;             PG8_LDB(B0, 1, 0); PG8_LDB(B1, 1, 1); PG8_SCHED; PG8_LDA(At, 1, 0); PG8_STAGE(PG8_SA(0, 1), a2, vs[1]);
;             PG8_WAIT_V(8); PG8_WAIT_L(0); PG8_BAR; if (do0) { PG8_MMA(0, 0, At, B0); PG8_MMA(0, 1, At, B1); } PG8_BAR; PG8_SCHED;
;             PG8_LDA(At, 1, 1); PG8_STAGE(PG8_SB(1, 0), b3, voffB); PG8_STAGE(PG8_SB(1, 1), b3 + hstep, voffB); PG8_STAGE(PG8_SA(1, 0), a3, vs[0]);
.Lwm_dnL1_1:
	s_waitcnt lgkmcnt(0)
	s_barrier
	s_setprio 1
	s_waitcnt lgkmcnt(0)
	v_mfma_f32_16x16x32_bf16 v[62:65], v[146:149], v[200:203], v[62:65]
	v_mfma_f32_16x16x32_bf16 v[58:61], v[172:175], v[200:203], v[58:61]
	v_mfma_f32_16x16x32_bf16 v[46:49], v[146:149], v[204:207], v[46:49]
	v_mfma_f32_16x16x32_bf16 v[42:45], v[172:175], v[204:207], v[42:45]
	v_mfma_f32_16x16x32_bf16 v[30:33], v[146:149], v[216:219], v[30:33]
	v_mfma_f32_16x16x32_bf16 v[26:29], v[172:175], v[216:219], v[26:29]
	v_mfma_f32_16x16x32_bf16 v[14:17], v[146:149], v[220:223], v[14:17]
	v_mfma_f32_16x16x32_bf16 v[10:13], v[172:175], v[220:223], v[10:13]
	v_mfma_f32_16x16x32_bf16 v[62:65], v[168:171], v[208:211], v[62:65]
	v_mfma_f32_16x16x32_bf16 v[58:61], v[176:179], v[208:211], v[58:61]
	v_mfma_f32_16x16x32_bf16 v[46:49], v[168:171], v[212:215], v[46:49]
	v_mfma_f32_16x16x32_bf16 v[42:45], v[176:179], v[212:215], v[42:45]
	v_mfma_f32_16x16x32_bf16 v[30:33], v[168:171], v[224:227], v[30:33]
	v_mfma_f32_16x16x32_bf16 v[26:29], v[176:179], v[224:227], v[26:29]
	v_mfma_f32_16x16x32_bf16 v[14:17], v[168:171], v[228:231], v[14:17]
	v_mfma_f32_16x16x32_bf16 v[10:13], v[176:179], v[228:231], v[10:13]
	s_setprio 0
	s_setprio 1
	v_mfma_f32_16x16x32_bf16 v[54:57], v[180:183], v[200:203], v[54:57]
	v_mfma_f32_16x16x32_bf16 v[50:53], v[188:191], v[200:203], v[50:53]
	v_mfma_f32_16x16x32_bf16 v[38:41], v[180:183], v[204:207], v[38:41]
	v_mfma_f32_16x16x32_bf16 v[34:37], v[188:191], v[204:207], v[34:37]
	v_mfma_f32_16x16x32_bf16 v[22:25], v[180:183], v[216:219], v[22:25]
	v_mfma_f32_16x16x32_bf16 v[18:21], v[188:191], v[216:219], v[18:21]
	v_mfma_f32_16x16x32_bf16 v[6:9], v[180:183], v[220:223], v[6:9]
	v_mfma_f32_16x16x32_bf16 v[2:5], v[188:191], v[220:223], v[2:5]
	v_mfma_f32_16x16x32_bf16 v[54:57], v[184:187], v[208:211], v[54:57]
	v_mfma_f32_16x16x32_bf16 v[50:53], v[192:195], v[208:211], v[50:53]
	v_mfma_f32_16x16x32_bf16 v[38:41], v[184:187], v[212:215], v[38:41]
	v_mfma_f32_16x16x32_bf16 v[34:37], v[192:195], v[212:215], v[34:37]
	v_mfma_f32_16x16x32_bf16 v[22:25], v[184:187], v[224:227], v[22:25]
	v_mfma_f32_16x16x32_bf16 v[18:21], v[192:195], v[224:227], v[18:21]
	v_mfma_f32_16x16x32_bf16 v[6:9], v[184:187], v[228:231], v[6:9]
	v_mfma_f32_16x16x32_bf16 v[2:5], v[192:195], v[228:231], v[2:5]
	s_setprio 0
	s_waitcnt vmcnt(8)
	s_barrier
	s_add_i32 s57, 0, 0x18000
	v_add_u32_e32 v146, s57, v150
	v_add_u32_e32 v167, s57, v151
	s_add_i32 s58, 0, 0x1c000
	ds_read_b128 v[146:149], v146
	ds_read_b128 v[168:171], v167
	ds_read_b128 v[172:175], v163
	ds_read_b128 v[176:179], v164
	v_add_u32_e32 v167, s58, v150
	v_add_u32_e32 v184, s58, v151
	ds_read_b128 v[180:183], v167
	ds_read_b128 v[184:187], v184
	ds_read_b128 v[188:191], v165
	ds_read_b128 v[192:195], v166
	s_mov_b32 m0, s36
	v_lshl_add_u64 v[196:197], s[26:27], 0, v[138:139]
	ds_read_b128 v[200:203], v161 offset:32768
	ds_read_b128 v[204:207], v161 offset:34816
	ds_read_b128 v[208:211], v162 offset:32768
	ds_read_b128 v[212:215], v162 offset:34816
	ds_read_b128 v[216:219], v161 offset:36864
	ds_read_b128 v[220:223], v161 offset:38912
	ds_read_b128 v[224:227], v162 offset:36864
	ds_read_b128 v[228:231], v162 offset:38912
	global_load_lds_dwordx4 v[196:197], off
	v_lshl_add_u64 v[196:197], s[26:27], 0, v[140:141]
	s_mov_b32 m0, s37
	s_nop 0
	global_load_lds_dwordx4 v[196:197], off
	s_bitcmp1_b32 s2, 0
	s_cbranch_scc0 .Lwm_dnL1_2
	s_waitcnt vmcnt(8)
; #define PG8_STAGE(bufoff, gbase, voff) do { _Pragma("unroll") for (int _i = 0; _i < 2; ++_i) \
;         __builtin_amdgcn_global_load_lds((const unsigned*)((const char*)(gbase) + (voff)[_i]), (LAS unsigned*)(lds + (bufoff) + ldsw + _i * 8192), 16, 0, 0); } while (0)
; #define PG8_LDA(dst, b, h) do { _Pragma("unroll") for (int m = 0; m < 4; ++m) _Pragma("unroll") for (int k = 0; k < 2; ++k) dst[m][k] = *(const LAS bf16x8*)(lds + PG8_SA(b, h) + ((aoff ^ (k * 64)) + m * 2048)); } while (0)
; #define PG8_MMA(ai, bj, At, Bt) do { __builtin_amdgcn_s_setprio(1); _Pragma("unroll") for (int m = 0; m < 4; ++m) _Pragma("unroll") for (int n = 0; n < 2; ++n) _Pragma("unroll") for (int k = 0; k < 2; ++k) \
;         acc[ai][bj][m][n] = __builtin_amdgcn_mfma_f32_16x16x32_bf16(Bt[n][k], At[m][k], acc[ai][bj][m][n], 0, 0, 0); __builtin_amdgcn_s_setprio(0); } while (0)
; #define PG8_WAIT_V(n) asm volatile("s_waitcnt vmcnt(" #n ")" ::: "memory")
; #define PG8_WAIT_L(n) asm volatile("s_waitcnt lgkmcnt(" #n ")" ::: "memory")
; #define PG8_BAR __builtin_amdgcn_s_barrier()
; #define PG8_SCHED __builtin_amdgcn_sched_barrier(0)
;     ...
;             PG8_WAIT_V(8); PG8_WAIT_L(0); PG8_BAR; if (do0) { PG8_MMA(0, 0, At, B0); PG8_MMA(0, 1, At, B1); } PG8_BAR; PG8_SCHED;
;             PG8_LDA(At, 1, 1); PG8_STAGE(PG8_SB(1, 0), b3, voffB); PG8_STAGE(PG8_SB(1, 1), b3 + hstep, voffB); PG8_STAGE(PG8_SA(1, 0), a3, vs[0]);
;             PG8_WAIT_V(8); PG8_WAIT_L(0); PG8_BAR; if (do1) { PG8_MMA(1, 0, At, B0); PG8_MMA(1, 1, At, B1); } PG8_BAR; PG8_SCHED;
;         }
;         if (wr == 0) PG8_BAR;
.Lwm_dnL1_2:
	s_waitcnt lgkmcnt(0)
	s_barrier
	s_setprio 1
	s_waitcnt lgkmcnt(0)
	v_mfma_f32_16x16x32_bf16 v[126:129], v[146:149], v[200:203], v[126:129]
	v_mfma_f32_16x16x32_bf16 v[122:125], v[172:175], v[200:203], v[122:125]
	v_mfma_f32_16x16x32_bf16 v[114:117], v[146:149], v[204:207], v[114:117]
	v_mfma_f32_16x16x32_bf16 v[106:109], v[172:175], v[204:207], v[106:109]
	v_mfma_f32_16x16x32_bf16 v[98:101], v[146:149], v[216:219], v[98:101]
	v_mfma_f32_16x16x32_bf16 v[90:93], v[172:175], v[216:219], v[90:93]
	v_mfma_f32_16x16x32_bf16 v[82:85], v[146:149], v[220:223], v[82:85]
	v_mfma_f32_16x16x32_bf16 v[74:77], v[172:175], v[220:223], v[74:77]
	v_mfma_f32_16x16x32_bf16 v[126:129], v[168:171], v[208:211], v[126:129]
	v_mfma_f32_16x16x32_bf16 v[122:125], v[176:179], v[208:211], v[122:125]
	v_mfma_f32_16x16x32_bf16 v[114:117], v[168:171], v[212:215], v[114:117]
	v_mfma_f32_16x16x32_bf16 v[106:109], v[176:179], v[212:215], v[106:109]
	v_mfma_f32_16x16x32_bf16 v[98:101], v[168:171], v[224:227], v[98:101]
	v_mfma_f32_16x16x32_bf16 v[90:93], v[176:179], v[224:227], v[90:93]
	v_mfma_f32_16x16x32_bf16 v[82:85], v[168:171], v[228:231], v[82:85]
	v_mfma_f32_16x16x32_bf16 v[74:77], v[176:179], v[228:231], v[74:77]
	s_setprio 0
	s_setprio 1
	v_mfma_f32_16x16x32_bf16 v[118:121], v[180:183], v[200:203], v[118:121]
	v_mfma_f32_16x16x32_bf16 v[110:113], v[188:191], v[200:203], v[110:113]
	v_mfma_f32_16x16x32_bf16 v[102:105], v[180:183], v[204:207], v[102:105]
	v_mfma_f32_16x16x32_bf16 v[94:97], v[188:191], v[204:207], v[94:97]
	v_mfma_f32_16x16x32_bf16 v[86:89], v[180:183], v[216:219], v[86:89]
	v_mfma_f32_16x16x32_bf16 v[78:81], v[188:191], v[216:219], v[78:81]
	v_mfma_f32_16x16x32_bf16 v[70:73], v[180:183], v[220:223], v[70:73]
	v_mfma_f32_16x16x32_bf16 v[66:69], v[188:191], v[220:223], v[66:69]
	v_mfma_f32_16x16x32_bf16 v[118:121], v[184:187], v[208:211], v[118:121]
	v_mfma_f32_16x16x32_bf16 v[110:113], v[192:195], v[208:211], v[110:113]
	v_mfma_f32_16x16x32_bf16 v[102:105], v[184:187], v[212:215], v[102:105]
	v_mfma_f32_16x16x32_bf16 v[94:97], v[192:195], v[212:215], v[94:97]
	v_mfma_f32_16x16x32_bf16 v[86:89], v[184:187], v[224:227], v[86:89]
	v_mfma_f32_16x16x32_bf16 v[78:81], v[192:195], v[224:227], v[78:81]
	v_mfma_f32_16x16x32_bf16 v[70:73], v[184:187], v[228:231], v[70:73]
	v_mfma_f32_16x16x32_bf16 v[66:69], v[192:195], v[228:231], v[66:69]
	s_setprio 0
	s_waitcnt vmcnt(8)
	s_barrier
	s_add_i32 s26, s57, s30
	v_lshl_add_u64 v[196:197], s[24:25], 0, v[132:133]
	s_mov_b32 m0, s26
	ds_read_b128 v[200:203], v161 offset:49152
	ds_read_b128 v[204:207], v161 offset:51200
	ds_read_b128 v[208:211], v162 offset:49152
	ds_read_b128 v[212:215], v162 offset:51200
	ds_read_b128 v[216:219], v161 offset:53248
	ds_read_b128 v[220:223], v161 offset:55296
	ds_read_b128 v[224:227], v162 offset:53248
	ds_read_b128 v[228:231], v162 offset:55296
	global_load_lds_dwordx4 v[196:197], off
	s_add_i32 m0, s26, 0x2000
	s_add_u32 s22, s22, 0xb4000
	v_lshl_add_u64 v[196:197], s[24:25], 0, v[130:131]
	s_addc_u32 s23, s23, 0
	s_add_i32 s24, s58, s30
	global_load_lds_dwordx4 v[196:197], off
	v_lshl_add_u64 v[196:197], s[22:23], 0, v[132:133]
	s_mov_b32 m0, s24
	s_nop 0
	global_load_lds_dwordx4 v[196:197], off
	v_lshl_add_u64 v[196:197], s[22:23], 0, v[130:131]
	s_add_i32 m0, s24, 0x2000
	s_nop 0
	global_load_lds_dwordx4 v[196:197], off
	v_lshl_add_u64 v[196:197], s[20:21], 0, v[134:135]
	s_mov_b32 m0, s39
	s_nop 0
	global_load_lds_dwordx4 v[196:197], off
	v_lshl_add_u64 v[196:197], s[20:21], 0, v[136:137]
	s_mov_b32 m0, s40
	s_nop 0
	global_load_lds_dwordx4 v[196:197], off
	s_bitcmp1_b32 s2, 0
	s_cbranch_scc0 .Lwm_dnL1_3
	s_waitcnt vmcnt(8)
.Lwm_dnL1_3:
	s_waitcnt lgkmcnt(0)
	s_barrier
	s_setprio 1
	s_waitcnt lgkmcnt(0)
	v_mfma_f32_16x16x32_bf16 v[62:65], v[146:149], v[200:203], v[62:65]
	v_mfma_f32_16x16x32_bf16 v[58:61], v[172:175], v[200:203], v[58:61]
	v_mfma_f32_16x16x32_bf16 v[46:49], v[146:149], v[204:207], v[46:49]
	v_mfma_f32_16x16x32_bf16 v[42:45], v[172:175], v[204:207], v[42:45]
	v_mfma_f32_16x16x32_bf16 v[30:33], v[146:149], v[216:219], v[30:33]
	v_mfma_f32_16x16x32_bf16 v[26:29], v[172:175], v[216:219], v[26:29]
	v_mfma_f32_16x16x32_bf16 v[14:17], v[146:149], v[220:223], v[14:17]
	v_mfma_f32_16x16x32_bf16 v[10:13], v[172:175], v[220:223], v[10:13]
	v_mfma_f32_16x16x32_bf16 v[62:65], v[168:171], v[208:211], v[62:65]
	v_mfma_f32_16x16x32_bf16 v[58:61], v[176:179], v[208:211], v[58:61]
	v_mfma_f32_16x16x32_bf16 v[46:49], v[168:171], v[212:215], v[46:49]
	v_mfma_f32_16x16x32_bf16 v[42:45], v[176:179], v[212:215], v[42:45]
	v_mfma_f32_16x16x32_bf16 v[30:33], v[168:171], v[224:227], v[30:33]
	v_mfma_f32_16x16x32_bf16 v[26:29], v[176:179], v[224:227], v[26:29]
	v_mfma_f32_16x16x32_bf16 v[14:17], v[168:171], v[228:231], v[14:17]
	v_mfma_f32_16x16x32_bf16 v[10:13], v[176:179], v[228:231], v[10:13]
	s_setprio 0
	s_setprio 1
	v_mfma_f32_16x16x32_bf16 v[54:57], v[180:183], v[200:203], v[54:57]
	v_mfma_f32_16x16x32_bf16 v[50:53], v[188:191], v[200:203], v[50:53]
	v_mfma_f32_16x16x32_bf16 v[38:41], v[180:183], v[204:207], v[38:41]
	v_mfma_f32_16x16x32_bf16 v[34:37], v[188:191], v[204:207], v[34:37]
	v_mfma_f32_16x16x32_bf16 v[22:25], v[180:183], v[216:219], v[22:25]
	v_mfma_f32_16x16x32_bf16 v[18:21], v[188:191], v[216:219], v[18:21]
	v_mfma_f32_16x16x32_bf16 v[6:9], v[180:183], v[220:223], v[6:9]
	v_mfma_f32_16x16x32_bf16 v[2:5], v[188:191], v[220:223], v[2:5]
	v_mfma_f32_16x16x32_bf16 v[54:57], v[184:187], v[208:211], v[54:57]
	v_mfma_f32_16x16x32_bf16 v[50:53], v[192:195], v[208:211], v[50:53]
	v_mfma_f32_16x16x32_bf16 v[38:41], v[184:187], v[212:215], v[38:41]
	v_mfma_f32_16x16x32_bf16 v[34:37], v[192:195], v[212:215], v[34:37]
	v_mfma_f32_16x16x32_bf16 v[22:25], v[184:187], v[224:227], v[22:25]
	v_mfma_f32_16x16x32_bf16 v[18:21], v[192:195], v[224:227], v[18:21]
	v_mfma_f32_16x16x32_bf16 v[6:9], v[184:187], v[228:231], v[6:9]
	v_mfma_f32_16x16x32_bf16 v[2:5], v[192:195], v[228:231], v[2:5]
	s_setprio 0
	s_waitcnt vmcnt(8)
	s_barrier
	s_add_i32 s56, s56, 2
	s_add_u32 s18, s18, 0x8000
	s_addc_u32 s19, s19, 0
	s_add_u32 s54, s54, 0x8000
	s_addc_u32 s55, s55, 0
	s_cmp_gt_u32 s56, 41
	s_cbranch_scc0 .LBB0_2411
	s_and_b64 vcc, exec, s[4:5]
	s_cbranch_vccz .LBB0_2414
	s_barrier
